# first two K-loop waits of each unit after an epilogue relaxed to vmcnt(8+S) in P6/P7/P10/P11 (epilogue stores drain under the first K-tile); P6 pre-loop vmcnt(0) removed
# speedup vs baseline: 1.0603x; 1.0085x over previous
;     __device__ __forceinline__ void init(int G_, int c_) { G = G_; c = c_; so.init(M, NPROJ, G_, c_); }
; #define PHASE_BASES() const KAS char* KA = (const KAS char*)__builtin_amdgcn_kernarg_segment_ptr(); asm volatile("" : "+s"(KA)); unsigned char* const ws = *(unsigned char* const KAS*)(KA + 8 * 27)
;     __device__ __forceinline__ bool next(int i, pg8::Unit& u) const { const int s = i >= R ? 1 : 0; const bool ok = so.next(i - s * R, u); u.sel = s; return ok && i < 2 * R; }
; __global__ void __launch_bounds__(NWAVES * 64, 2) mk_fwd(Args args) {
;     ...
;     if (IN(6)) { PHASE_BASES();
;         { pg8::Gemm g{Yn, WSSD, M, D, D, SCY, WSC}; OrderTwice S; S.so.init(M, D, G, bx); S.R = (512 + G - 1) / G; EpiGate E{Gt, b_gate, MERGED};
;           pg8::gemm_phase<EpiGate, OrderTwice, true, true>(lds, g, S, E); }
.LBB0_880:
	s_mov_b32 s98, 0
	s_cmp_lt_i32 s78, 7
	s_cselect_b64 s[0:1], -1, 0
	s_cmp_gt_i32 s79, 6
	s_cselect_b64 s[2:3], -1, 0
	s_and_b64 s[0:1], s[0:1], s[2:3]
	s_andn2_b64 vcc, exec, s[0:1]
	s_cbranch_vccnz .LBB0_993
	s_abs_i32 s0, s86
	v_cvt_f32_u32_e32 v1, s0
	s_sub_i32 s5, 0, s0
	s_add_i32 s1, s86, 0x1ff
	s_xor_b32 s4, s1, s86
	v_rcp_iflag_f32_e32 v1, v1
	s_abs_i32 s1, s1
	s_ashr_i32 s4, s4, 31
	s_mov_b64 s[2:3], s[74:75]
	v_mul_f32_e32 v1, 0x4f7ffffe, v1
	v_cvt_u32_f32_e32 v1, v1
	v_mov_b64_e32 v[2:3], 0x200
	v_readfirstlane_b32 s12, v0
	v_readfirstlane_b32 s6, v1
	s_mul_i32 s5, s5, s6
	s_mul_hi_u32 s5, s6, s5
	s_add_i32 s6, s6, s5
	s_mul_hi_u32 s5, s1, s6
	s_mul_i32 s6, s5, s0
	s_sub_i32 s1, s1, s6
	s_add_i32 s7, s5, 1
	s_sub_i32 s6, s1, s0
	s_cmp_ge_u32 s1, s0
	s_cselect_b32 s5, s7, s5
	s_cselect_b32 s1, s6, s1
	s_add_i32 s6, s5, 1
	s_cmp_ge_u32 s1, s0
	s_cselect_b32 s0, s6, s5
	s_xor_b32 s0, s0, s4
	s_sub_i32 s6, s0, s4
	s_load_dwordx2 s[4:5], s[2:3], 0xd8
	s_load_dwordx2 s[0:1], s[2:3], 0x90
	s_min_i32 s2, s6, 0
	s_sub_i32 s2, 0, s2
	s_mul_i32 s3, s2, s87
	s_mul_hi_u32 s7, s2, s86
	s_add_i32 s7, s7, s3
	s_mul_i32 s2, s2, s86
	s_add_u32 s2, s2, s88
	s_addc_u32 s3, s7, s89
	v_cmp_lt_i64_e64 s[8:9], s[2:3], v[2:3]
	v_mov_b64_e32 v[2:3], 0x1ff
	v_cmp_gt_i64_e32 vcc, s[2:3], v[2:3]
	s_cbranch_vccnz .LBB0_887
	s_ashr_i32 s3, s2, 31
	s_lshr_b32 s3, s3, 29
	s_add_i32 s11, s2, s3
	s_and_b32 s3, s11, -8
	s_sub_i32 s7, s2, s3
	s_cmp_gt_i32 s7, -1
	s_cbranch_scc0 .LBB0_884
	s_lshl_b32 s10, s7, 6
	s_ashr_i32 s2, s11, 3
	s_cbranch_execz .LBB0_885
	s_branch .LBB0_886

;     __device__ __forceinline__ unsigned claim_issue(int wid, int lane) const { unsigned r = 0u; if (wid == 0 && lane == 0) { unsigned z; asm volatile("v_mov_b32 %0, 0" : "=v"(z)); r = __hip_atomic_fetch_add(q + z, 1u, __ATOMIC_RELAXED, __HIP_MEMORY_SCOPE_AGENT); } return r; }
;     __device__ __forceinline__ bool next(int i, pg8::Unit& u) const { const int s = i >= R ? 1 : 0; const bool ok = so.next(i - s * R, u); u.sel = s; return ok && i < 2 * R; }
; template <class Epi, class Sched, bool ALIGN_EPI = false, bool SP2 = false>
; __device__ __forceinline__ void gemm_phase(PG8_LAS unsigned char* lds, const Gemm g, const Sched& S, const Epi& E) {
;     ...
;         const bool has_next = S.next(ui + 1, nxt);
;         unsigned pend = 0u; if constexpr (Sched::DYNAMIC) pend = S.claim_issue(wid, lane);
;         const char* nA = has_next ? (const char*)(nxt.sel ? g.A2 : g.A) + (size_t)nxt.pm * tstep : cA; const char* nB = has_next ? (const char*)(nxt.sel ? g.Bt2 : g.Bt) + (size_t)nxt.pn * tstep : cB;
;         for (int t = 0; t < nt; t += 2) {
;             const bool last = (t == nt - 2);
;             const char* a1 = cA + (size_t)(t + 1) * kstep;
;             const char* a2 = last ? nA : cA + (size_t)(t + 2) * kstep; const char* b2 = last ? nB : cB + (size_t)(t + 2) * kstep;
;             const char* a3 = a2 + kstep; const char* b3 = b2 + kstep;
;     ...
; #pragma unroll
;         for (int a = 0; a < 2; ++a)
; #pragma unroll
;             for (int b = 0; b < 2; ++b)
; #pragma unroll
;                 for (int m = 0; m < 4; ++m)
; #pragma unroll
;                     for (int n = 0; n < 2; ++n) acc[a][b][m][n] = (f32x4){0.f, 0.f, 0.f, 0.f};
;         cur = nxt; cA = nA; cB = nB; ++ui;
.LBB0_899:
	s_cmp_lt_u32 s43, s53
	s_cselect_b64 s[20:21], -1, 0
	s_and_b64 s[24:25], s[8:9], s[20:21]
	s_and_b64 s[8:9], s[14:15], exec
	s_cselect_b32 s17, s45, s33
	s_cselect_b32 s20, s44, s7
	s_ashr_i32 s19, s18, 31
	s_lshl_b64 s[8:9], s[18:19], 20
	s_add_u32 s20, s20, s8
	s_addc_u32 s21, s17, s9
	s_and_b64 s[8:9], s[24:25], exec
	s_cselect_b32 s19, s21, s37
	s_cselect_b32 s56, s20, s36
	s_and_b64 s[8:9], s[14:15], exec
	s_cselect_b32 s23, s47, s39
	s_cselect_b32 s22, s46, s38
	s_ashr_i32 s17, s16, 31
	s_lshl_b64 s[8:9], s[16:17], 20
	s_add_u32 s22, s22, s8
	s_addc_u32 s23, s23, s9
	s_and_b64 s[8:9], s[24:25], exec
	s_cselect_b32 s17, s23, s35
	s_cselect_b32 s57, s22, s34
	s_add_u32 s8, s36, 0x80080
	s_addc_u32 s9, s37, 0
	s_add_u32 s58, s34, 0x100
	v_mov_b32_e32 v2, 0
	s_addc_u32 s59, s35, 0
	s_mov_b32 s60, -2
	v_mov_b32_e32 v3, v2
	v_mov_b32_e32 v4, v2
	v_mov_b32_e32 v5, v2
	v_mov_b32_e32 v6, v2
	v_mov_b32_e32 v7, v2
	v_mov_b32_e32 v8, v2
	v_mov_b32_e32 v9, v2
	v_mov_b32_e32 v10, v2
	v_mov_b32_e32 v11, v2
	v_mov_b32_e32 v12, v2
	v_mov_b32_e32 v13, v2
	v_mov_b32_e32 v14, v2
	v_mov_b32_e32 v15, v2
	v_mov_b32_e32 v16, v2
	v_mov_b32_e32 v17, v2
	v_mov_b32_e32 v18, v2
	v_mov_b32_e32 v19, v2
	v_mov_b32_e32 v20, v2
	v_mov_b32_e32 v21, v2
	v_mov_b32_e32 v22, v2
	v_mov_b32_e32 v23, v2
	v_mov_b32_e32 v24, v2
	v_mov_b32_e32 v25, v2
	v_mov_b32_e32 v26, v2
	v_mov_b32_e32 v27, v2
	v_mov_b32_e32 v28, v2
	v_mov_b32_e32 v29, v2
	v_mov_b32_e32 v30, v2
	v_mov_b32_e32 v31, v2
	v_mov_b32_e32 v32, v2
	v_mov_b32_e32 v33, v2
	v_mov_b32_e32 v66, v2
	v_mov_b32_e32 v67, v2
	v_mov_b32_e32 v68, v2
	v_mov_b32_e32 v69, v2
	v_mov_b32_e32 v70, v2
	v_mov_b32_e32 v71, v2
	v_mov_b32_e32 v72, v2
	v_mov_b32_e32 v73, v2
	v_mov_b32_e32 v74, v2
	v_mov_b32_e32 v75, v2
	v_mov_b32_e32 v76, v2
	v_mov_b32_e32 v77, v2
	v_mov_b32_e32 v78, v2
	v_mov_b32_e32 v79, v2
	v_mov_b32_e32 v80, v2
	v_mov_b32_e32 v81, v2
	v_mov_b32_e32 v82, v2
	v_mov_b32_e32 v83, v2
	v_mov_b32_e32 v84, v2
	v_mov_b32_e32 v85, v2
	v_mov_b32_e32 v86, v2
	v_mov_b32_e32 v87, v2
	v_mov_b32_e32 v88, v2
	v_mov_b32_e32 v89, v2
	v_mov_b32_e32 v90, v2
	v_mov_b32_e32 v91, v2
	v_mov_b32_e32 v92, v2
	v_mov_b32_e32 v93, v2
	v_mov_b32_e32 v94, v2
	v_mov_b32_e32 v95, v2
	v_mov_b32_e32 v96, v2
	v_mov_b32_e32 v97, v2
	v_mov_b32_e32 v34, v2
	v_mov_b32_e32 v35, v2
	v_mov_b32_e32 v36, v2
	v_mov_b32_e32 v37, v2
	v_mov_b32_e32 v38, v2
	v_mov_b32_e32 v39, v2
	v_mov_b32_e32 v40, v2
	v_mov_b32_e32 v41, v2
	v_mov_b32_e32 v42, v2
	v_mov_b32_e32 v43, v2
	v_mov_b32_e32 v44, v2
	v_mov_b32_e32 v45, v2
	v_mov_b32_e32 v46, v2
	v_mov_b32_e32 v47, v2
	v_mov_b32_e32 v48, v2
	v_mov_b32_e32 v49, v2
	v_mov_b32_e32 v50, v2
	v_mov_b32_e32 v51, v2
	v_mov_b32_e32 v52, v2
	v_mov_b32_e32 v53, v2
	v_mov_b32_e32 v54, v2
	v_mov_b32_e32 v55, v2
	v_mov_b32_e32 v56, v2
	v_mov_b32_e32 v57, v2
	v_mov_b32_e32 v58, v2
	v_mov_b32_e32 v59, v2
	v_mov_b32_e32 v60, v2
	v_mov_b32_e32 v61, v2
	v_mov_b32_e32 v62, v2
	v_mov_b32_e32 v63, v2
	v_mov_b32_e32 v64, v2
	v_mov_b32_e32 v65, v2
	v_mov_b32_e32 v98, v2
	v_mov_b32_e32 v99, v2
	v_mov_b32_e32 v100, v2
	v_mov_b32_e32 v101, v2
	v_mov_b32_e32 v102, v2
	v_mov_b32_e32 v103, v2
	v_mov_b32_e32 v104, v2
	v_mov_b32_e32 v105, v2
	v_mov_b32_e32 v106, v2
	v_mov_b32_e32 v107, v2
	v_mov_b32_e32 v108, v2
	v_mov_b32_e32 v109, v2
	v_mov_b32_e32 v110, v2
	v_mov_b32_e32 v111, v2
	v_mov_b32_e32 v112, v2
	v_mov_b32_e32 v113, v2
	v_mov_b32_e32 v122, v2
	v_mov_b32_e32 v123, v2
	v_mov_b32_e32 v124, v2
	v_mov_b32_e32 v125, v2
	v_mov_b32_e32 v126, v2
	v_mov_b32_e32 v127, v2
	v_mov_b32_e32 v128, v2
	v_mov_b32_e32 v129, v2
	v_mov_b32_e32 v130, v2
	v_mov_b32_e32 v131, v2
	v_mov_b32_e32 v132, v2
	v_mov_b32_e32 v133, v2
	v_mov_b32_e32 v134, v2
	v_mov_b32_e32 v135, v2
	v_mov_b32_e32 v136, v2
	v_mov_b32_e32 v137, v2
	s_cmp_lg_u32 s98, 0
	s_cselect_b32 s99, -2, 0x7ffffff0
	s_branch .LBB0_900
.Lrx6_a:
	s_waitcnt vmcnt(24)
	s_branch .Lrx6_a_done

; #define PG8_STAGE(bufoff, gbase, voff) do { _Pragma("unroll") for (int _i = 0; _i < 2; ++_i) \
;         __builtin_amdgcn_global_load_lds((const unsigned*)((const char*)(gbase) + (voff)[_i]), (PG8_LAS unsigned*)(lds + (bufoff) + ldsw + _i * 8192), 16, 0, 0); } while (0)
; #define PG8_LDA(dst, b, h) do { _Pragma("unroll") for (int m = 0; m < 4; ++m) _Pragma("unroll") for (int k = 0; k < 2; ++k) dst[m][k] = *(const PG8_LAS bf16x8*)(lds + PG8_SA(b, h) + aoff + m * 2048 + k * 1024); } while (0)
; #define PG8_LDB(dst, b, h) do { _Pragma("unroll") for (int n = 0; n < 2; ++n) _Pragma("unroll") for (int k = 0; k < 2; ++k) dst[n][k] = *(const PG8_LAS bf16x8*)(lds + PG8_SB(b, h) + boff + n * 2048 + k * 1024); } while (0)
; #define PG8_MMA(ai, bj, At, Bt) do { __builtin_amdgcn_s_setprio(1); _Pragma("unroll") for (int m = 0; m < 4; ++m) _Pragma("unroll") for (int n = 0; n < 2; ++n) _Pragma("unroll") for (int k = 0; k < 2; ++k) \
;         acc[ai][bj][m][n] = __builtin_amdgcn_mfma_f32_16x16x32_bf16(Bt[n][k], At[m][k], acc[ai][bj][m][n], 0, 0, 0); __builtin_amdgcn_s_setprio(0); } while (0)
; #define PG8_WAIT_V(n) asm volatile("s_waitcnt vmcnt(" #n ")" ::: "memory")
; #define PG8_BAR __builtin_amdgcn_s_barrier()
; template <class Epi, class Sched, bool ALIGN_EPI = false, bool SP2 = false>
; __device__ __forceinline__ void gemm_phase(PG8_LAS unsigned char* lds, const Gemm g, const Sched& S, const Epi& E) {
;     ...
;         for (int t = 0; t < nt; t += 2) {
;             const bool last = (t == nt - 2);
;             const char* a1 = cA + (size_t)(t + 1) * kstep;
;             const char* a2 = last ? nA : cA + (size_t)(t + 2) * kstep; const char* b2 = last ? nB : cB + (size_t)(t + 2) * kstep;
;             const char* a3 = a2 + kstep; const char* b3 = b2 + kstep;
;             if (last && has_next) S.a_ready(nxt);
;             if constexpr (SP2) {
;             PG8_LDB(B0, 0, 0); PG8_LDB(B1, 0, 1); PG8_SCHED; PG8_LDA(At, 0, 0); PG8_STAGE(PG8_SA(1, 1), a1 + hstep, voffA);
;             PG8_WAIT_V(8); PG8_WAIT_L(0); PG8_BAR; PG8_MMA(0, 0, At, B0); PG8_MMA(0, 1, At, B1); PG8_BAR; PG8_SCHED;
;             PG8_LDA(At, 0, 1); PG8_STAGE(PG8_SB(0, 0), b2, voffB); PG8_STAGE(PG8_SB(0, 1), b2 + hstep, voffB); PG8_STAGE(PG8_SA(0, 0), a2, voffA);
;             PG8_WAIT_V(8); PG8_WAIT_L(0); PG8_BAR; PG8_MMA(1, 0, At, B0); PG8_MMA(1, 1, At, B1); PG8_BAR; PG8_SCHED;
.LBB0_900:
	ds_read_b128 v[114:117], v218
	ds_read_b128 v[118:121], v218 offset:1024
	ds_read_b128 v[138:141], v218 offset:2048
	ds_read_b128 v[142:145], v218 offset:3072
	ds_read_b128 v[146:149], v219
	ds_read_b128 v[150:153], v219 offset:1024
	ds_read_b128 v[154:157], v219 offset:2048
	ds_read_b128 v[158:161], v219 offset:3072
	s_add_u32 s34, s8, 0xfff80080
	s_addc_u32 s35, s9, -1
	s_cmp_eq_u32 s60, 28
	s_cselect_b32 s37, s19, s35
	s_cselect_b32 s36, s56, s34
	s_cselect_b32 s35, s17, s59
	s_cselect_b32 s34, s57, s58
	v_lshl_add_u64 v[170:171], s[8:9], 0, v[180:181]
	s_add_i32 m0, s27, 0xc000
	ds_read_b128 v[162:165], v220
	ds_read_b128 v[166:169], v220 offset:1024
	ds_read_b128 v[190:193], v220 offset:2048
	ds_read_b128 v[194:197], v220 offset:3072
	ds_read_b128 v[198:201], v220 offset:4096
	ds_read_b128 v[202:205], v220 offset:5120
	ds_read_b128 v[206:209], v220 offset:6144
	ds_read_b128 v[210:213], v220 offset:7168
	global_load_lds_dwordx4 v[170:171], off
	v_lshl_add_u64 v[170:171], s[8:9], 0, v[182:183]
	s_add_i32 m0, s27, 0xe000
	s_nop 0
	global_load_lds_dwordx4 v[170:171], off
	s_cmp_eq_u32 s60, s99
	s_cbranch_scc1 .Lrx6_a
	s_waitcnt vmcnt(8)
.Lrx6_a_done:
	s_waitcnt lgkmcnt(0)
	s_barrier
	s_setprio 1
	s_waitcnt lgkmcnt(0)
	v_mfma_f32_16x16x32_bf16 v[134:137], v[114:117], v[162:165], v[134:137]
	v_mfma_f32_16x16x32_bf16 v[130:133], v[138:141], v[162:165], v[130:133]
	v_mfma_f32_16x16x32_bf16 v[126:129], v[114:117], v[190:193], v[126:129]
	v_mfma_f32_16x16x32_bf16 v[122:125], v[138:141], v[190:193], v[122:125]
	v_mfma_f32_16x16x32_bf16 v[110:113], v[114:117], v[198:201], v[110:113]
	v_mfma_f32_16x16x32_bf16 v[106:109], v[138:141], v[198:201], v[106:109]
	v_mfma_f32_16x16x32_bf16 v[102:105], v[114:117], v[206:209], v[102:105]
	v_mfma_f32_16x16x32_bf16 v[98:101], v[138:141], v[206:209], v[98:101]
	v_mfma_f32_16x16x32_bf16 v[134:137], v[118:121], v[166:169], v[134:137]
	v_mfma_f32_16x16x32_bf16 v[130:133], v[142:145], v[166:169], v[130:133]
	v_mfma_f32_16x16x32_bf16 v[126:129], v[118:121], v[194:197], v[126:129]
	v_mfma_f32_16x16x32_bf16 v[122:125], v[142:145], v[194:197], v[122:125]
	v_mfma_f32_16x16x32_bf16 v[110:113], v[118:121], v[202:205], v[110:113]
	v_mfma_f32_16x16x32_bf16 v[106:109], v[142:145], v[202:205], v[106:109]
	v_mfma_f32_16x16x32_bf16 v[102:105], v[118:121], v[210:213], v[102:105]
	v_mfma_f32_16x16x32_bf16 v[98:101], v[142:145], v[210:213], v[98:101]
	s_setprio 0
	s_setprio 1
	v_mfma_f32_16x16x32_bf16 v[62:65], v[146:149], v[162:165], v[62:65]
	v_mfma_f32_16x16x32_bf16 v[58:61], v[154:157], v[162:165], v[58:61]
	v_mfma_f32_16x16x32_bf16 v[54:57], v[146:149], v[190:193], v[54:57]
	v_mfma_f32_16x16x32_bf16 v[50:53], v[154:157], v[190:193], v[50:53]
	v_mfma_f32_16x16x32_bf16 v[46:49], v[146:149], v[198:201], v[46:49]
	v_mfma_f32_16x16x32_bf16 v[42:45], v[154:157], v[198:201], v[42:45]
	v_mfma_f32_16x16x32_bf16 v[38:41], v[146:149], v[206:209], v[38:41]
	v_mfma_f32_16x16x32_bf16 v[34:37], v[154:157], v[206:209], v[34:37]
	v_mfma_f32_16x16x32_bf16 v[62:65], v[150:153], v[166:169], v[62:65]
	v_mfma_f32_16x16x32_bf16 v[58:61], v[158:161], v[166:169], v[58:61]
	v_mfma_f32_16x16x32_bf16 v[54:57], v[150:153], v[194:197], v[54:57]
	v_mfma_f32_16x16x32_bf16 v[50:53], v[158:161], v[194:197], v[50:53]
	v_mfma_f32_16x16x32_bf16 v[46:49], v[150:153], v[202:205], v[46:49]
	v_mfma_f32_16x16x32_bf16 v[42:45], v[158:161], v[202:205], v[42:45]
	v_mfma_f32_16x16x32_bf16 v[38:41], v[150:153], v[210:213], v[38:41]
	v_mfma_f32_16x16x32_bf16 v[34:37], v[158:161], v[210:213], v[34:37]
	s_setprio 0
	s_barrier
	s_add_i32 s61, s54, s40
	v_lshl_add_u64 v[170:171], s[34:35], 0, v[174:175]
	s_mov_b32 m0, s61
	ds_read_b128 v[162:165], v220 offset:16384
	ds_read_b128 v[166:169], v220 offset:17408
	ds_read_b128 v[190:193], v220 offset:18432
	ds_read_b128 v[194:197], v220 offset:19456
	ds_read_b128 v[198:201], v220 offset:20480
	ds_read_b128 v[202:205], v220 offset:21504
	ds_read_b128 v[206:209], v220 offset:22528
	ds_read_b128 v[210:213], v220 offset:23552
	global_load_lds_dwordx4 v[170:171], off
	s_add_i32 m0, s61, 0x2000
	s_add_u32 s62, s34, 0x80000
	v_lshl_add_u64 v[214:215], s[34:35], 0, v[178:179]
	s_addc_u32 s63, s35, 0
	s_add_i32 s61, s55, s40
	global_load_lds_dwordx4 v[214:215], off
	v_lshl_add_u64 v[222:223], s[62:63], 0, v[174:175]
	s_mov_b32 m0, s61
	v_lshl_add_u64 v[224:225], s[36:37], 0, v[176:177]
	global_load_lds_dwordx4 v[222:223], off
	v_lshl_add_u64 v[222:223], s[62:63], 0, v[178:179]
	s_add_i32 m0, s61, 0x2000
	s_nop 0
	global_load_lds_dwordx4 v[222:223], off
	v_lshl_add_u64 v[222:223], s[36:37], 0, v[172:173]
	s_mov_b32 m0, s27
	s_nop 0
	global_load_lds_dwordx4 v[222:223], off
	s_mov_b32 m0, s29
	s_nop 0
	global_load_lds_dwordx4 v[224:225], off
	s_cmp_eq_u32 s60, s99
	s_cbranch_scc1 .Lrx6_b
	s_waitcnt vmcnt(8)
; #define PG8_STAGE(bufoff, gbase, voff) do { _Pragma("unroll") for (int _i = 0; _i < 2; ++_i) \
;         __builtin_amdgcn_global_load_lds((const unsigned*)((const char*)(gbase) + (voff)[_i]), (PG8_LAS unsigned*)(lds + (bufoff) + ldsw + _i * 8192), 16, 0, 0); } while (0)
; #define PG8_LDA(dst, b, h) do { _Pragma("unroll") for (int m = 0; m < 4; ++m) _Pragma("unroll") for (int k = 0; k < 2; ++k) dst[m][k] = *(const PG8_LAS bf16x8*)(lds + PG8_SA(b, h) + aoff + m * 2048 + k * 1024); } while (0)
; #define PG8_LDB(dst, b, h) do { _Pragma("unroll") for (int n = 0; n < 2; ++n) _Pragma("unroll") for (int k = 0; k < 2; ++k) dst[n][k] = *(const PG8_LAS bf16x8*)(lds + PG8_SB(b, h) + boff + n * 2048 + k * 1024); } while (0)
; #define PG8_MMA(ai, bj, At, Bt) do { __builtin_amdgcn_s_setprio(1); _Pragma("unroll") for (int m = 0; m < 4; ++m) _Pragma("unroll") for (int n = 0; n < 2; ++n) _Pragma("unroll") for (int k = 0; k < 2; ++k) \
;         acc[ai][bj][m][n] = __builtin_amdgcn_mfma_f32_16x16x32_bf16(Bt[n][k], At[m][k], acc[ai][bj][m][n], 0, 0, 0); __builtin_amdgcn_s_setprio(0); } while (0)
; #define PG8_WAIT_V(n) asm volatile("s_waitcnt vmcnt(" #n ")" ::: "memory")
; #define PG8_WAIT_L(n) asm volatile("s_waitcnt lgkmcnt(" #n ")" ::: "memory")
; #define PG8_BAR __builtin_amdgcn_s_barrier()
; #define PG8_SCHED __builtin_amdgcn_sched_barrier(0)
; #define PG8_WAIT_V(n) asm volatile("s_waitcnt vmcnt(" #n ")" ::: "memory")
; #define PG8_WAIT_L(n) asm volatile("s_waitcnt lgkmcnt(" #n ")" ::: "memory")
; #define PG8_BAR __builtin_amdgcn_s_barrier()
; template <class Epi, class Sched, bool ALIGN_EPI = false, bool SP2 = false>
; __device__ __forceinline__ void gemm_phase(PG8_LAS unsigned char* lds, const Gemm g, const Sched& S, const Epi& E) {
;     ...
;             PG8_WAIT_V(8); PG8_WAIT_L(0); PG8_BAR; PG8_MMA(0, 0, At, B0); PG8_MMA(0, 1, At, B1); PG8_BAR; PG8_SCHED;
;             PG8_LDA(At, 0, 1); PG8_STAGE(PG8_SB(0, 0), b2, voffB); PG8_STAGE(PG8_SB(0, 1), b2 + hstep, voffB); PG8_STAGE(PG8_SA(0, 0), a2, voffA);
;             PG8_WAIT_V(8); PG8_WAIT_L(0); PG8_BAR; PG8_MMA(1, 0, At, B0); PG8_MMA(1, 1, At, B1); PG8_BAR; PG8_SCHED;
;             PG8_LDB(B0, 1, 0); PG8_LDB(B1, 1, 1); PG8_SCHED; PG8_LDA(At, 1, 0); PG8_STAGE(PG8_SA(0, 1), a2 + hstep, voffA);
;             PG8_WAIT_V(8); PG8_WAIT_L(0); PG8_BAR; PG8_MMA(0, 0, At, B0); PG8_MMA(0, 1, At, B1); PG8_BAR; PG8_SCHED;
.Lrx6_b_done:
	s_waitcnt lgkmcnt(0)
	s_barrier
	s_setprio 1
	s_waitcnt lgkmcnt(0)
	v_mfma_f32_16x16x32_bf16 v[94:97], v[114:117], v[162:165], v[94:97]
	v_mfma_f32_16x16x32_bf16 v[90:93], v[138:141], v[162:165], v[90:93]
	v_mfma_f32_16x16x32_bf16 v[86:89], v[114:117], v[190:193], v[86:89]
	v_mfma_f32_16x16x32_bf16 v[82:85], v[138:141], v[190:193], v[82:85]
	v_mfma_f32_16x16x32_bf16 v[78:81], v[114:117], v[198:201], v[78:81]
	v_mfma_f32_16x16x32_bf16 v[74:77], v[138:141], v[198:201], v[74:77]
	v_mfma_f32_16x16x32_bf16 v[70:73], v[114:117], v[206:209], v[70:73]
	v_mfma_f32_16x16x32_bf16 v[66:69], v[138:141], v[206:209], v[66:69]
	v_mfma_f32_16x16x32_bf16 v[94:97], v[118:121], v[166:169], v[94:97]
	v_mfma_f32_16x16x32_bf16 v[90:93], v[142:145], v[166:169], v[90:93]
	v_mfma_f32_16x16x32_bf16 v[86:89], v[118:121], v[194:197], v[86:89]
	v_mfma_f32_16x16x32_bf16 v[82:85], v[142:145], v[194:197], v[82:85]
	v_mfma_f32_16x16x32_bf16 v[78:81], v[118:121], v[202:205], v[78:81]
	v_mfma_f32_16x16x32_bf16 v[74:77], v[142:145], v[202:205], v[74:77]
	v_mfma_f32_16x16x32_bf16 v[70:73], v[118:121], v[210:213], v[70:73]
	v_mfma_f32_16x16x32_bf16 v[66:69], v[142:145], v[210:213], v[66:69]
	s_setprio 0
	s_setprio 1
	v_mfma_f32_16x16x32_bf16 v[30:33], v[146:149], v[162:165], v[30:33]
	v_mfma_f32_16x16x32_bf16 v[26:29], v[154:157], v[162:165], v[26:29]
	v_mfma_f32_16x16x32_bf16 v[22:25], v[146:149], v[190:193], v[22:25]
	v_mfma_f32_16x16x32_bf16 v[18:21], v[154:157], v[190:193], v[18:21]
	v_mfma_f32_16x16x32_bf16 v[14:17], v[146:149], v[198:201], v[14:17]
	v_mfma_f32_16x16x32_bf16 v[10:13], v[154:157], v[198:201], v[10:13]
	v_mfma_f32_16x16x32_bf16 v[6:9], v[146:149], v[206:209], v[6:9]
	v_mfma_f32_16x16x32_bf16 v[2:5], v[154:157], v[206:209], v[2:5]
	v_mfma_f32_16x16x32_bf16 v[30:33], v[150:153], v[166:169], v[30:33]
	v_mfma_f32_16x16x32_bf16 v[26:29], v[158:161], v[166:169], v[26:29]
	v_mfma_f32_16x16x32_bf16 v[22:25], v[150:153], v[194:197], v[22:25]
	v_mfma_f32_16x16x32_bf16 v[18:21], v[158:161], v[194:197], v[18:21]
	v_mfma_f32_16x16x32_bf16 v[14:17], v[150:153], v[202:205], v[14:17]
	v_mfma_f32_16x16x32_bf16 v[10:13], v[158:161], v[202:205], v[10:13]
	v_mfma_f32_16x16x32_bf16 v[6:9], v[150:153], v[210:213], v[6:9]
	v_mfma_f32_16x16x32_bf16 v[2:5], v[158:161], v[210:213], v[2:5]
	s_setprio 0
	s_barrier
	s_add_i32 s61, 0, 0x18000
	s_add_i32 s62, 0, 0x1c000
	v_add_u32_e32 v142, s61, v217
	v_add_u32_e32 v158, s62, v217
	ds_read_b128 v[114:117], v142
	ds_read_b128 v[118:121], v142 offset:1024
	ds_read_b128 v[138:141], v142 offset:2048
	ds_read_b128 v[142:145], v142 offset:3072
	ds_read_b128 v[146:149], v158
	ds_read_b128 v[150:153], v158 offset:1024
	ds_read_b128 v[154:157], v158 offset:2048
	ds_read_b128 v[158:161], v158 offset:3072
	s_add_u32 s36, s36, 0x80000
	s_addc_u32 s37, s37, 0
	s_mov_b32 m0, s41
	v_lshl_add_u64 v[226:227], s[36:37], 0, v[172:173]
	ds_read_b128 v[162:165], v220 offset:32768
	ds_read_b128 v[166:169], v220 offset:33792
	ds_read_b128 v[190:193], v220 offset:34816
	ds_read_b128 v[194:197], v220 offset:35840
	ds_read_b128 v[198:201], v220 offset:36864
	ds_read_b128 v[202:205], v220 offset:37888
	ds_read_b128 v[206:209], v220 offset:38912
	ds_read_b128 v[210:213], v220 offset:39936
	global_load_lds_dwordx4 v[226:227], off
	v_lshl_add_u64 v[226:227], s[36:37], 0, v[176:177]
	s_mov_b32 m0, s42
	s_nop 0
	global_load_lds_dwordx4 v[226:227], off
	s_waitcnt vmcnt(8)
	s_waitcnt lgkmcnt(0)
	s_barrier
	s_setprio 1
	s_waitcnt lgkmcnt(0)
	v_mfma_f32_16x16x32_bf16 v[134:137], v[114:117], v[162:165], v[134:137]
	v_mfma_f32_16x16x32_bf16 v[130:133], v[138:141], v[162:165], v[130:133]
	v_mfma_f32_16x16x32_bf16 v[126:129], v[114:117], v[190:193], v[126:129]
	v_mfma_f32_16x16x32_bf16 v[122:125], v[138:141], v[190:193], v[122:125]
	v_mfma_f32_16x16x32_bf16 v[110:113], v[114:117], v[198:201], v[110:113]
	v_mfma_f32_16x16x32_bf16 v[106:109], v[138:141], v[198:201], v[106:109]
	v_mfma_f32_16x16x32_bf16 v[102:105], v[114:117], v[206:209], v[102:105]
	v_mfma_f32_16x16x32_bf16 v[98:101], v[138:141], v[206:209], v[98:101]
	v_mfma_f32_16x16x32_bf16 v[134:137], v[118:121], v[166:169], v[134:137]
	v_mfma_f32_16x16x32_bf16 v[130:133], v[142:145], v[166:169], v[130:133]
	v_mfma_f32_16x16x32_bf16 v[126:129], v[118:121], v[194:197], v[126:129]
	v_mfma_f32_16x16x32_bf16 v[122:125], v[142:145], v[194:197], v[122:125]
	v_mfma_f32_16x16x32_bf16 v[110:113], v[118:121], v[202:205], v[110:113]
	v_mfma_f32_16x16x32_bf16 v[106:109], v[142:145], v[202:205], v[106:109]
	v_mfma_f32_16x16x32_bf16 v[102:105], v[118:121], v[210:213], v[102:105]
	v_mfma_f32_16x16x32_bf16 v[98:101], v[142:145], v[210:213], v[98:101]
	s_setprio 0
	s_setprio 1
	v_mfma_f32_16x16x32_bf16 v[62:65], v[146:149], v[162:165], v[62:65]
	v_mfma_f32_16x16x32_bf16 v[58:61], v[154:157], v[162:165], v[58:61]
	v_mfma_f32_16x16x32_bf16 v[54:57], v[146:149], v[190:193], v[54:57]
	v_mfma_f32_16x16x32_bf16 v[50:53], v[154:157], v[190:193], v[50:53]
	v_mfma_f32_16x16x32_bf16 v[46:49], v[146:149], v[198:201], v[46:49]
	v_mfma_f32_16x16x32_bf16 v[42:45], v[154:157], v[198:201], v[42:45]
	v_mfma_f32_16x16x32_bf16 v[38:41], v[146:149], v[206:209], v[38:41]
	v_mfma_f32_16x16x32_bf16 v[34:37], v[154:157], v[206:209], v[34:37]
	v_mfma_f32_16x16x32_bf16 v[62:65], v[150:153], v[166:169], v[62:65]
	v_mfma_f32_16x16x32_bf16 v[58:61], v[158:161], v[166:169], v[58:61]
	v_mfma_f32_16x16x32_bf16 v[54:57], v[150:153], v[194:197], v[54:57]
	v_mfma_f32_16x16x32_bf16 v[50:53], v[158:161], v[194:197], v[50:53]
	v_mfma_f32_16x16x32_bf16 v[46:49], v[150:153], v[202:205], v[46:49]
	v_mfma_f32_16x16x32_bf16 v[42:45], v[158:161], v[202:205], v[42:45]
	v_mfma_f32_16x16x32_bf16 v[38:41], v[150:153], v[210:213], v[38:41]
	v_mfma_f32_16x16x32_bf16 v[34:37], v[158:161], v[210:213], v[34:37]
	s_setprio 0
	s_barrier
; #define PG8_STAGE(bufoff, gbase, voff) do { _Pragma("unroll") for (int _i = 0; _i < 2; ++_i) \
;         __builtin_amdgcn_global_load_lds((const unsigned*)((const char*)(gbase) + (voff)[_i]), (PG8_LAS unsigned*)(lds + (bufoff) + ldsw + _i * 8192), 16, 0, 0); } while (0)
; #define PG8_LDA(dst, b, h) do { _Pragma("unroll") for (int m = 0; m < 4; ++m) _Pragma("unroll") for (int k = 0; k < 2; ++k) dst[m][k] = *(const PG8_LAS bf16x8*)(lds + PG8_SA(b, h) + aoff + m * 2048 + k * 1024); } while (0)
; #define PG8_MMA(ai, bj, At, Bt) do { __builtin_amdgcn_s_setprio(1); _Pragma("unroll") for (int m = 0; m < 4; ++m) _Pragma("unroll") for (int n = 0; n < 2; ++n) _Pragma("unroll") for (int k = 0; k < 2; ++k) \
;         acc[ai][bj][m][n] = __builtin_amdgcn_mfma_f32_16x16x32_bf16(Bt[n][k], At[m][k], acc[ai][bj][m][n], 0, 0, 0); __builtin_amdgcn_s_setprio(0); } while (0)
; #define PG8_WAIT_V(n) asm volatile("s_waitcnt vmcnt(" #n ")" ::: "memory")
; #define PG8_WAIT_L(n) asm volatile("s_waitcnt lgkmcnt(" #n ")" ::: "memory")
; #define PG8_BAR __builtin_amdgcn_s_barrier()
; #define PG8_SCHED __builtin_amdgcn_sched_barrier(0)
; #define PG8_STAGE(bufoff, gbase, voff) do { _Pragma("unroll") for (int _i = 0; _i < 2; ++_i) \
;         __builtin_amdgcn_global_load_lds((const unsigned*)((const char*)(gbase) + (voff)[_i]), (PG8_LAS unsigned*)(lds + (bufoff) + ldsw + _i * 8192), 16, 0, 0); } while (0)
; #define PG8_LDA(dst, b, h) do { _Pragma("unroll") for (int m = 0; m < 4; ++m) _Pragma("unroll") for (int k = 0; k < 2; ++k) dst[m][k] = *(const PG8_LAS bf16x8*)(lds + PG8_SA(b, h) + aoff + m * 2048 + k * 1024); } while (0)
; #define PG8_WAIT_V(n) asm volatile("s_waitcnt vmcnt(" #n ")" ::: "memory")
; #define PG8_WAIT_L(n) asm volatile("s_waitcnt lgkmcnt(" #n ")" ::: "memory")
; #define PG8_BAR __builtin_amdgcn_s_barrier()
; #define PG8_SCHED __builtin_amdgcn_sched_barrier(0)
; template <class Epi, class Sched, bool ALIGN_EPI = false, bool SP2 = false>
; __device__ __forceinline__ void gemm_phase(PG8_LAS unsigned char* lds, const Gemm g, const Sched& S, const Epi& E) {
;     ...
;         for (int t = 0; t < nt; t += 2) {
;     ...
;             PG8_LDA(At, 1, 1); PG8_STAGE(PG8_SB(1, 0), b3, voffB); PG8_STAGE(PG8_SB(1, 1), b3 + hstep, voffB); PG8_STAGE(PG8_SA(1, 0), a3, voffA);
;             PG8_WAIT_V(8); PG8_WAIT_L(0); PG8_BAR; PG8_MMA(1, 0, At, B0); PG8_MMA(1, 1, At, B1); PG8_BAR; PG8_SCHED;
	s_add_i32 s36, s61, s40
	v_lshl_add_u64 v[170:171], v[170:171], 0, s[10:11]
	s_mov_b32 m0, s36
	ds_read_b128 v[162:165], v220 offset:49152
	ds_read_b128 v[166:169], v220 offset:50176
	ds_read_b128 v[190:193], v220 offset:51200
	ds_read_b128 v[194:197], v220 offset:52224
	ds_read_b128 v[198:201], v220 offset:53248
	ds_read_b128 v[202:205], v220 offset:54272
	ds_read_b128 v[206:209], v220 offset:55296
	ds_read_b128 v[210:213], v220 offset:56320
	global_load_lds_dwordx4 v[170:171], off
	s_add_i32 m0, s36, 0x2000
	s_add_u32 s34, s34, 0x80080
	v_lshl_add_u64 v[170:171], v[214:215], 0, s[10:11]
	s_addc_u32 s35, s35, 0
	s_add_i32 s36, s62, s40
	global_load_lds_dwordx4 v[170:171], off
	v_lshl_add_u64 v[170:171], s[34:35], 0, v[174:175]
	s_mov_b32 m0, s36
	s_nop 0
	global_load_lds_dwordx4 v[170:171], off
	v_lshl_add_u64 v[170:171], s[34:35], 0, v[178:179]
	s_add_i32 m0, s36, 0x2000
	s_nop 0
	global_load_lds_dwordx4 v[170:171], off
	v_lshl_add_u64 v[170:171], v[222:223], 0, s[10:11]
	s_mov_b32 m0, s51
	s_nop 0
	global_load_lds_dwordx4 v[170:171], off
	v_lshl_add_u64 v[170:171], v[224:225], 0, s[10:11]
	s_mov_b32 m0, s52
	s_nop 0
	global_load_lds_dwordx4 v[170:171], off
	s_waitcnt vmcnt(8)
	s_waitcnt lgkmcnt(0)
	s_barrier
	s_setprio 1
	s_waitcnt lgkmcnt(0)
	v_mfma_f32_16x16x32_bf16 v[94:97], v[114:117], v[162:165], v[94:97]
	v_mfma_f32_16x16x32_bf16 v[90:93], v[138:141], v[162:165], v[90:93]
	v_mfma_f32_16x16x32_bf16 v[86:89], v[114:117], v[190:193], v[86:89]
	v_mfma_f32_16x16x32_bf16 v[82:85], v[138:141], v[190:193], v[82:85]
	v_mfma_f32_16x16x32_bf16 v[78:81], v[114:117], v[198:201], v[78:81]
	v_mfma_f32_16x16x32_bf16 v[74:77], v[138:141], v[198:201], v[74:77]
	v_mfma_f32_16x16x32_bf16 v[70:73], v[114:117], v[206:209], v[70:73]
	v_mfma_f32_16x16x32_bf16 v[66:69], v[138:141], v[206:209], v[66:69]
	v_mfma_f32_16x16x32_bf16 v[94:97], v[118:121], v[166:169], v[94:97]
	v_mfma_f32_16x16x32_bf16 v[90:93], v[142:145], v[166:169], v[90:93]
	v_mfma_f32_16x16x32_bf16 v[86:89], v[118:121], v[194:197], v[86:89]
	v_mfma_f32_16x16x32_bf16 v[82:85], v[142:145], v[194:197], v[82:85]
	v_mfma_f32_16x16x32_bf16 v[78:81], v[118:121], v[202:205], v[78:81]
	v_mfma_f32_16x16x32_bf16 v[74:77], v[142:145], v[202:205], v[74:77]
	v_mfma_f32_16x16x32_bf16 v[70:73], v[118:121], v[210:213], v[70:73]
	v_mfma_f32_16x16x32_bf16 v[66:69], v[142:145], v[210:213], v[66:69]
	s_setprio 0
	s_setprio 1
	v_mfma_f32_16x16x32_bf16 v[30:33], v[146:149], v[162:165], v[30:33]
	v_mfma_f32_16x16x32_bf16 v[26:29], v[154:157], v[162:165], v[26:29]
	v_mfma_f32_16x16x32_bf16 v[22:25], v[146:149], v[190:193], v[22:25]
	v_mfma_f32_16x16x32_bf16 v[18:21], v[154:157], v[190:193], v[18:21]
	v_mfma_f32_16x16x32_bf16 v[14:17], v[146:149], v[198:201], v[14:17]
	v_mfma_f32_16x16x32_bf16 v[10:13], v[154:157], v[198:201], v[10:13]
	v_mfma_f32_16x16x32_bf16 v[6:9], v[146:149], v[206:209], v[6:9]
	v_mfma_f32_16x16x32_bf16 v[2:5], v[154:157], v[206:209], v[2:5]
	v_mfma_f32_16x16x32_bf16 v[30:33], v[150:153], v[166:169], v[30:33]
	v_mfma_f32_16x16x32_bf16 v[26:29], v[158:161], v[166:169], v[26:29]
	v_mfma_f32_16x16x32_bf16 v[22:25], v[150:153], v[194:197], v[22:25]
	v_mfma_f32_16x16x32_bf16 v[18:21], v[158:161], v[194:197], v[18:21]
	v_mfma_f32_16x16x32_bf16 v[14:17], v[150:153], v[202:205], v[14:17]
	v_mfma_f32_16x16x32_bf16 v[10:13], v[158:161], v[202:205], v[10:13]
	v_mfma_f32_16x16x32_bf16 v[6:9], v[150:153], v[210:213], v[6:9]
	v_mfma_f32_16x16x32_bf16 v[2:5], v[158:161], v[210:213], v[2:5]
	s_setprio 0
	s_barrier
	s_add_i32 s60, s60, 2
	s_add_u32 s8, s8, 0x100
	s_addc_u32 s9, s9, 0
	s_add_u32 s58, s58, 0x100
	s_addc_u32 s59, s59, 0
	s_cmp_gt_u32 s60, 29
	s_cbranch_scc0 .LBB0_900
	s_and_b64 vcc, exec, s[12:13]
	s_cbranch_vccz .LBB0_903
	s_barrier

; __device__ __forceinline__ v4u pack8(const float (&o)[8]) { v4u w; w.x = pk2(o[0], o[1]); w.y = pk2(o[2], o[3]); w.z = pk2(o[4], o[5]); w.w = pk2(o[6], o[7]); return w; }
; __device__ __forceinline__ float sigmf(float x) { return __builtin_amdgcn_rcpf(1.f + __expf(-x)); }
; __device__ __forceinline__ unsigned pk2(float lo, float hi) { typedef float f2v __attribute__((ext_vector_type(2))); typedef __bf16 b2v __attribute__((ext_vector_type(2))); const f2v v = {lo, hi}; return __builtin_bit_cast(unsigned, __builtin_convertvector(v, b2v)); }
; __device__ __forceinline__ void unpack8(const v4u w, float (&o)[8]) { o[0] = bflo(w.x); o[1] = bfhi(w.x); o[2] = bflo(w.y); o[3] = bfhi(w.y); o[4] = bflo(w.z); o[5] = bfhi(w.z); o[6] = bflo(w.w); o[7] = bfhi(w.w); }
;     __device__ __forceinline__ void operator()(const f32x4 (&acc)[2][2][4][2], const pg8::Unit& u, int wr, int wc, int fr, int fq_in) const {
;     ...
;                 for (int m = 0; m < 4; ++m) { const size_t row = (size_t)(row0 + ai * 128 + m * 16);
;                     gw_[m] = *(const v4u*)(Gt + row * (2 * D) + goff + col); pw_[m] = first ? (v4u){0u, 0u, 0u, 0u} : *(const v4u*)(O + row * D + col); }
;                 __builtin_amdgcn_sched_barrier(0);
; #pragma unroll
;                 for (int m = 0; m < 4; ++m) { const size_t row = (size_t)(row0 + ai * 128 + m * 16);
;                     float g0[8], p[8]; unpack8(gw_[m], g0); unpack8(pw_[m], p);
;                     float o[8];
; #pragma unroll
;                     for (int q = 0; q < 4; ++q) { o[q] = p[q] + sigmf(g0[q] + b0[q]) * acc[ai][bj][m][0][q]; o[4 + q] = p[4 + q] + sigmf(g0[4 + q] + b0[4 + q]) * acc[ai][bj][m][1][q]; }
;                     *(v4u*)(O + row * D + col) = pack8(o); }
.LBB0_935:
	s_waitcnt vmcnt(3)
	v_lshlrev_b32_e32 v62, 16, v58
	v_lshlrev_b32_e32 v64, 16, v59
	v_and_b32_e32 v65, 0xffff0000, v59
	v_lshlrev_b32_e32 v59, 16, v60
	v_and_b32_e32 v58, 0xffff0000, v58
	v_add_f32_e32 v62, v70, v62
	v_add_f32_e32 v59, v66, v59
	v_mul_f32_e32 v62, 0xbfb8aa3b, v62
	v_mul_f32_e32 v59, 0xbfb8aa3b, v59
	v_add_f32_e32 v58, v71, v58
	v_exp_f32_e32 v62, v62
	v_exp_f32_e32 v59, v59
	v_mul_f32_e32 v58, 0xbfb8aa3b, v58
	v_lshlrev_b32_e32 v78, 16, v61
	v_and_b32_e32 v79, 0xffff0000, v61
	v_exp_f32_e32 v61, v58
	v_and_b32_e32 v63, 0xffff0000, v60
	v_add_f32_e32 v60, 1.0, v62
	v_add_f32_e32 v59, 1.0, v59
	v_rcp_f32_e32 v58, v60
	v_rcp_f32_e32 v60, v59
	v_add_f32_e32 v59, 1.0, v61
	v_add_f32_e32 v61, v67, v63
	v_mul_f32_e32 v61, 0xbfb8aa3b, v61
	v_rcp_f32_e32 v59, v59
	v_exp_f32_e32 v61, v61
	v_lshlrev_b32_e32 v62, 16, v74
	v_and_b32_e32 v63, 0xffff0000, v74
	v_pk_fma_f32 v[30:31], v[30:31], v[58:59], v[62:63]
	v_add_f32_e32 v58, 1.0, v61
	v_rcp_f32_e32 v61, v58
	v_add_f32_e32 v58, v72, v64
	v_mul_f32_e32 v58, 0xbfb8aa3b, v58
	v_exp_f32_e32 v62, v58
	v_lshlrev_b32_e32 v58, 16, v76
	v_and_b32_e32 v59, 0xffff0000, v76
	v_pk_fma_f32 v[58:59], v[26:27], v[60:61], v[58:59]
	v_add_f32_e32 v27, v68, v78
	v_mul_f32_e32 v27, 0xbfb8aa3b, v27
	v_add_f32_e32 v60, v73, v65
	v_exp_f32_e32 v27, v27
	v_mul_f32_e32 v60, 0xbfb8aa3b, v60
	v_exp_f32_e32 v61, v60
	v_add_f32_e32 v26, 1.0, v62
	v_add_f32_e32 v27, 1.0, v27
	v_rcp_f32_e32 v60, v27
	v_add_f32_e32 v27, 1.0, v61
	v_add_f32_e32 v61, v69, v79
	v_mul_f32_e32 v61, 0xbfb8aa3b, v61
	v_exp_f32_e32 v61, v61
	v_rcp_f32_e32 v26, v26
	v_rcp_f32_e32 v27, v27
	v_lshlrev_b32_e32 v62, 16, v75
	v_add_f32_e32 v61, 1.0, v61
	v_rcp_f32_e32 v61, v61
	v_and_b32_e32 v63, 0xffff0000, v75
	v_pk_fma_f32 v[32:33], v[32:33], v[26:27], v[62:63]
	v_lshlrev_b32_e32 v26, 16, v77
	v_and_b32_e32 v27, 0xffff0000, v77
	v_pk_fma_f32 v[60:61], v[28:29], v[60:61], v[26:27]
	v_cvt_pk_bf16_f32 v26, v30, v31
	v_cvt_pk_bf16_f32 v27, v32, v33
	v_cvt_pk_bf16_f32 v28, v58, v59
	v_cvt_pk_bf16_f32 v29, v60, v61
	global_store_dwordx4 v[96:97], v[26:29], off offset:256
	s_waitcnt vmcnt(3)
	v_lshlrev_b32_e32 v30, 16, v50
	v_and_b32_e32 v31, 0xffff0000, v50
	v_lshlrev_b32_e32 v26, 16, v54
	v_and_b32_e32 v27, 0xffff0000, v54
	v_add_f32_e32 v26, v70, v26
	v_add_f32_e32 v27, v71, v27
	v_mul_f32_e32 v26, 0xbfb8aa3b, v26
	v_mul_f32_e32 v27, 0xbfb8aa3b, v27
	v_exp_f32_e32 v26, v26
	v_exp_f32_e32 v27, v27
	v_lshlrev_b32_e32 v28, 16, v56
	v_and_b32_e32 v29, 0xffff0000, v56
	v_add_f32_e32 v28, v66, v28
	v_add_f32_e32 v29, v67, v29
	v_add_f32_e32 v26, 1.0, v26
	v_mul_f32_e32 v28, 0xbfb8aa3b, v28
	v_add_f32_e32 v27, 1.0, v27
	v_mul_f32_e32 v29, 0xbfb8aa3b, v29
	v_exp_f32_e32 v28, v28
	v_rcp_f32_e32 v26, v26
	v_rcp_f32_e32 v27, v27
	v_exp_f32_e32 v29, v29
	v_add_f32_e32 v28, 1.0, v28
	v_lshlrev_b32_e32 v32, 16, v55
	v_pk_fma_f32 v[22:23], v[22:23], v[26:27], v[30:31]
	v_add_f32_e32 v26, 1.0, v29
	v_rcp_f32_e32 v28, v28
	v_rcp_f32_e32 v29, v26
	v_add_f32_e32 v26, v72, v32
	v_mul_f32_e32 v26, 0xbfb8aa3b, v26
	v_lshlrev_b32_e32 v54, 16, v57
	v_exp_f32_e32 v30, v26
	v_lshlrev_b32_e32 v26, 16, v52
	v_and_b32_e32 v27, 0xffff0000, v52
	v_and_b32_e32 v33, 0xffff0000, v55
	v_pk_fma_f32 v[26:27], v[18:19], v[28:29], v[26:27]
	v_add_f32_e32 v19, v68, v54
	v_mul_f32_e32 v19, 0xbfb8aa3b, v19
	v_add_f32_e32 v28, v73, v33
	v_exp_f32_e32 v19, v19
	v_mul_f32_e32 v28, 0xbfb8aa3b, v28
	v_exp_f32_e32 v29, v28
	v_and_b32_e32 v55, 0xffff0000, v57
	v_add_f32_e32 v19, 1.0, v19
	v_rcp_f32_e32 v28, v19
	v_add_f32_e32 v19, 1.0, v29
	v_add_f32_e32 v29, v69, v55
	v_mul_f32_e32 v29, 0xbfb8aa3b, v29
	v_exp_f32_e32 v29, v29
	v_add_f32_e32 v18, 1.0, v30
	v_rcp_f32_e32 v18, v18
	v_rcp_f32_e32 v19, v19
	v_add_f32_e32 v29, 1.0, v29
	v_rcp_f32_e32 v29, v29
	v_lshlrev_b32_e32 v30, 16, v51
	v_and_b32_e32 v31, 0xffff0000, v51
	v_pk_fma_f32 v[24:25], v[24:25], v[18:19], v[30:31]
	v_lshlrev_b32_e32 v18, 16, v53
	v_and_b32_e32 v19, 0xffff0000, v53
	v_pk_fma_f32 v[28:29], v[20:21], v[28:29], v[18:19]
	v_cvt_pk_bf16_f32 v18, v22, v23
	v_cvt_pk_bf16_f32 v19, v24, v25
	v_cvt_pk_bf16_f32 v20, v26, v27
	v_cvt_pk_bf16_f32 v21, v28, v29
	global_store_dwordx4 v[126:127], v[18:21], off offset:256
	s_waitcnt vmcnt(3)
; __device__ __forceinline__ v4u pack8(const float (&o)[8]) { v4u w; w.x = pk2(o[0], o[1]); w.y = pk2(o[2], o[3]); w.z = pk2(o[4], o[5]); w.w = pk2(o[6], o[7]); return w; }
; __device__ __forceinline__ float sigmf(float x) { return __builtin_amdgcn_rcpf(1.f + __expf(-x)); }
; __device__ __forceinline__ unsigned pk2(float lo, float hi) { typedef float f2v __attribute__((ext_vector_type(2))); typedef __bf16 b2v __attribute__((ext_vector_type(2))); const f2v v = {lo, hi}; return __builtin_bit_cast(unsigned, __builtin_convertvector(v, b2v)); }
; __device__ __forceinline__ void unpack8(const v4u w, float (&o)[8]) { o[0] = bflo(w.x); o[1] = bfhi(w.x); o[2] = bflo(w.y); o[3] = bfhi(w.y); o[4] = bflo(w.z); o[5] = bfhi(w.z); o[6] = bflo(w.w); o[7] = bfhi(w.w); }
;     __device__ __forceinline__ void operator()(const f32x4 (&acc)[2][2][4][2], const pg8::Unit& u, int wr, int wc, int fr, int fq_in) const {
;     ...
;                 for (int m = 0; m < 4; ++m) { const size_t row = (size_t)(row0 + ai * 128 + m * 16);
;                     gw_[m] = *(const v4u*)(Gt + row * (2 * D) + goff + col); pw_[m] = first ? (v4u){0u, 0u, 0u, 0u} : *(const v4u*)(O + row * D + col); }
;                 __builtin_amdgcn_sched_barrier(0);
; #pragma unroll
;                 for (int m = 0; m < 4; ++m) { const size_t row = (size_t)(row0 + ai * 128 + m * 16);
;                     float g0[8], p[8]; unpack8(gw_[m], g0); unpack8(pw_[m], p);
;                     float o[8];
; #pragma unroll
;                     for (int q = 0; q < 4; ++q) { o[q] = p[q] + sigmf(g0[q] + b0[q]) * acc[ai][bj][m][0][q]; o[4 + q] = p[4 + q] + sigmf(g0[4 + q] + b0[4 + q]) * acc[ai][bj][m][1][q]; }
;                     *(v4u*)(O + row * D + col) = pack8(o); }
	v_lshlrev_b32_e32 v22, 16, v38
	v_and_b32_e32 v23, 0xffff0000, v38
	v_lshlrev_b32_e32 v18, 16, v46
	v_and_b32_e32 v19, 0xffff0000, v46
	v_add_f32_e32 v18, v70, v18
	v_add_f32_e32 v19, v71, v19
	v_mul_f32_e32 v18, 0xbfb8aa3b, v18
	v_mul_f32_e32 v19, 0xbfb8aa3b, v19
	v_exp_f32_e32 v18, v18
	v_exp_f32_e32 v19, v19
	v_lshlrev_b32_e32 v20, 16, v48
	v_and_b32_e32 v21, 0xffff0000, v48
	v_add_f32_e32 v20, v66, v20
	v_add_f32_e32 v21, v67, v21
	v_add_f32_e32 v18, 1.0, v18
	v_mul_f32_e32 v20, 0xbfb8aa3b, v20
	v_add_f32_e32 v19, 1.0, v19
	v_mul_f32_e32 v21, 0xbfb8aa3b, v21
	v_exp_f32_e32 v20, v20
	v_rcp_f32_e32 v18, v18
	v_rcp_f32_e32 v19, v19
	v_exp_f32_e32 v21, v21
	v_add_f32_e32 v20, 1.0, v20
	v_lshlrev_b32_e32 v24, 16, v47
	v_pk_fma_f32 v[14:15], v[14:15], v[18:19], v[22:23]
	v_add_f32_e32 v18, 1.0, v21
	v_rcp_f32_e32 v20, v20
	v_rcp_f32_e32 v21, v18
	v_add_f32_e32 v18, v72, v24
	v_mul_f32_e32 v18, 0xbfb8aa3b, v18
	v_lshlrev_b32_e32 v26, 16, v49
	v_exp_f32_e32 v22, v18
	v_lshlrev_b32_e32 v18, 16, v40
	v_and_b32_e32 v19, 0xffff0000, v40
	v_and_b32_e32 v25, 0xffff0000, v47
	v_pk_fma_f32 v[18:19], v[10:11], v[20:21], v[18:19]
	v_add_f32_e32 v11, v68, v26
	v_mul_f32_e32 v11, 0xbfb8aa3b, v11
	v_add_f32_e32 v20, v73, v25
	v_exp_f32_e32 v11, v11
	v_mul_f32_e32 v20, 0xbfb8aa3b, v20
	v_exp_f32_e32 v21, v20
	v_and_b32_e32 v27, 0xffff0000, v49
	v_add_f32_e32 v11, 1.0, v11
	v_rcp_f32_e32 v20, v11
	v_add_f32_e32 v11, 1.0, v21
	v_add_f32_e32 v21, v69, v27
	v_mul_f32_e32 v21, 0xbfb8aa3b, v21
	v_exp_f32_e32 v21, v21
	v_add_f32_e32 v10, 1.0, v22
	v_rcp_f32_e32 v10, v10
	v_rcp_f32_e32 v11, v11
	v_add_f32_e32 v21, 1.0, v21
	v_rcp_f32_e32 v21, v21
	v_lshlrev_b32_e32 v22, 16, v39
	v_and_b32_e32 v23, 0xffff0000, v39
	v_pk_fma_f32 v[16:17], v[16:17], v[10:11], v[22:23]
	v_lshlrev_b32_e32 v10, 16, v41
	v_and_b32_e32 v11, 0xffff0000, v41
	v_pk_fma_f32 v[20:21], v[12:13], v[20:21], v[10:11]
	v_cvt_pk_bf16_f32 v10, v14, v15
	v_cvt_pk_bf16_f32 v11, v16, v17
	v_cvt_pk_bf16_f32 v12, v18, v19
	v_cvt_pk_bf16_f32 v13, v20, v21
	global_store_dwordx4 v[122:123], v[10:13], off offset:256
	s_waitcnt vmcnt(3)
	v_lshlrev_b32_e32 v14, 16, v34
	v_and_b32_e32 v15, 0xffff0000, v34
	v_lshlrev_b32_e32 v10, 16, v42
	v_and_b32_e32 v11, 0xffff0000, v42
	v_add_f32_e32 v10, v70, v10
	v_add_f32_e32 v11, v71, v11
	v_mul_f32_e32 v10, 0xbfb8aa3b, v10
	v_mul_f32_e32 v11, 0xbfb8aa3b, v11
	v_exp_f32_e32 v10, v10
	v_exp_f32_e32 v11, v11
	v_lshlrev_b32_e32 v12, 16, v44
	v_and_b32_e32 v13, 0xffff0000, v44
	v_add_f32_e32 v12, v66, v12
	v_add_f32_e32 v13, v67, v13
	v_add_f32_e32 v10, 1.0, v10
	v_mul_f32_e32 v12, 0xbfb8aa3b, v12
	v_add_f32_e32 v11, 1.0, v11
	v_mul_f32_e32 v13, 0xbfb8aa3b, v13
	v_exp_f32_e32 v12, v12
	v_rcp_f32_e32 v10, v10
	v_rcp_f32_e32 v11, v11
	v_exp_f32_e32 v13, v13
	v_add_f32_e32 v12, 1.0, v12
	v_lshlrev_b32_e32 v16, 16, v43
	v_pk_fma_f32 v[6:7], v[6:7], v[10:11], v[14:15]
	v_add_f32_e32 v10, 1.0, v13
	v_rcp_f32_e32 v12, v12
	v_rcp_f32_e32 v13, v10
	v_add_f32_e32 v10, v72, v16
	v_mul_f32_e32 v10, 0xbfb8aa3b, v10
	v_lshlrev_b32_e32 v18, 16, v45
	v_exp_f32_e32 v14, v10
	v_lshlrev_b32_e32 v10, 16, v36
	v_and_b32_e32 v11, 0xffff0000, v36
	v_and_b32_e32 v17, 0xffff0000, v43
	v_pk_fma_f32 v[10:11], v[2:3], v[12:13], v[10:11]
	v_add_f32_e32 v3, v68, v18
	v_mul_f32_e32 v3, 0xbfb8aa3b, v3
	v_add_f32_e32 v12, v73, v17
	v_exp_f32_e32 v3, v3
	v_mul_f32_e32 v12, 0xbfb8aa3b, v12
	v_exp_f32_e32 v13, v12
	v_and_b32_e32 v19, 0xffff0000, v45
	v_add_f32_e32 v3, 1.0, v3
	v_rcp_f32_e32 v12, v3
	v_add_f32_e32 v3, 1.0, v13
	v_add_f32_e32 v13, v69, v19
	v_mul_f32_e32 v13, 0xbfb8aa3b, v13
	v_exp_f32_e32 v13, v13
	v_add_f32_e32 v2, 1.0, v14
	v_rcp_f32_e32 v2, v2
	v_rcp_f32_e32 v3, v3
	v_add_f32_e32 v13, 1.0, v13
	v_rcp_f32_e32 v13, v13
	v_lshlrev_b32_e32 v14, 16, v35
	v_and_b32_e32 v15, 0xffff0000, v35
	v_pk_fma_f32 v[8:9], v[8:9], v[2:3], v[14:15]
	v_lshlrev_b32_e32 v2, 16, v37
	v_and_b32_e32 v3, 0xffff0000, v37
	v_pk_fma_f32 v[12:13], v[4:5], v[12:13], v[2:3]
	v_cvt_pk_bf16_f32 v2, v6, v7
	v_cvt_pk_bf16_f32 v3, v8, v9
	v_cvt_pk_bf16_f32 v4, v10, v11
	v_cvt_pk_bf16_f32 v5, v12, v13
	s_andn2_b64 vcc, exec, s[24:25]
	s_mov_b64 s[8:9], -1
	s_mov_b32 s98, 1
	global_store_dwordx4 v[110:111], v[2:5], off offset:256
	s_cbranch_vccnz .LBB0_892
	s_andn2_b64 vcc, exec, s[2:3]
	s_cbranch_vccnz .LBB0_891
	s_barrier
	s_branch .LBB0_891

;     __device__ __forceinline__ void init(int G_, int c_) { G = G_; c = c_; so.init(M, NPROJ, G_, c_); }
;     __device__ __forceinline__ bool next(int i, pg8::Unit& u) const { const int s = i >= R ? 1 : 0; const bool ok = so.next(i - s * R, u); u.sel = s; return ok && i < 2 * R; }
; #define PHASE_BASES() const KAS char* KA = (const KAS char*)__builtin_amdgcn_kernarg_segment_ptr(); asm volatile("" : "+s"(KA)); unsigned char* const ws = *(unsigned char* const KAS*)(KA + 8 * 27)
;     __host__ __device__ __forceinline__ bool next(int i, Unit& u) const {
;         const long L = (long)i * G + c; if (L >= nwg) return false;
;         int wgid = (int)L; { const int q = nwg / NXCD, r = nwg % NXCD, xcd = wgid % NXCD, off = wgid / NXCD; wgid = (xcd < r ? xcd * (q + 1) : r * (q + 1) + (xcd - r) * q) + off; }
;         const int nig = WGM * nN, gid = wgid / nig, fm = gid * WGM, gsz = (nM - fm) < WGM ? (nM - fm) : WGM;
;         u.pm = fm + ((wgid % nig) % gsz); u.pn = (wgid % nig) / gsz; return true;
; __global__ void __launch_bounds__(NWAVES * 64, 2) mk_fwd(Args args) {
;     ...
;     if (IN(7)) { PHASE_BASES();
;         pg8::Gemm g{MERGED, WO, M, D, D}; pg8::StaticOrder S; S.init(M, D, G, bx); EpiBf16Plain E{OUTX, D};
;         pg8::gemm_phase<EpiBf16Plain, pg8::StaticOrder, true, true>(lds, g, S, E);
.LBB0_993:
	s_mov_b32 s98, 0
	s_cmp_lt_i32 s78, 8
	s_waitcnt lgkmcnt(0)
	s_cselect_b64 s[0:1], -1, 0
	s_cmp_gt_i32 s79, 7
	s_cselect_b64 s[2:3], -1, 0
	s_and_b64 s[0:1], s[0:1], s[2:3]
	s_andn2_b64 vcc, exec, s[0:1]
	s_cbranch_vccnz .LBB0_1072
	s_mov_b64 s[0:1], s[74:75]
	s_cmpk_gt_i32 s88, 0x1ff
	v_readfirstlane_b32 s9, v0
	s_cbranch_scc1 .LBB0_1018
	s_load_dwordx2 s[4:5], s[0:1], 0xd8
	s_lshr_b32 s0, s89, 29
	s_add_i32 s3, s88, s0
	s_and_b32 s0, s3, -8
	s_sub_i32 s6, s88, s0
	s_cmp_gt_i32 s6, -1
	s_cbranch_scc0 .LBB0_997
	s_lshl_b32 s2, s6, 6
	s_cbranch_execz .LBB0_998
	s_branch .LBB0_999

;     __device__ __forceinline__ unsigned claim_issue(int wid, int lane) const { unsigned r = 0u; if (wid == 0 && lane == 0) { unsigned z; asm volatile("v_mov_b32 %0, 0" : "=v"(z)); r = __hip_atomic_fetch_add(q + z, 1u, __ATOMIC_RELAXED, __HIP_MEMORY_SCOPE_AGENT); } return r; }
;     __device__ __forceinline__ bool next(int i, pg8::Unit& u) const { const int s = i >= R ? 1 : 0; const bool ok = so.next(i - s * R, u); u.sel = s; return ok && i < 2 * R; }
; template <class Epi, class Sched, bool ALIGN_EPI = false, bool SP2 = false>
; __device__ __forceinline__ void gemm_phase(PG8_LAS unsigned char* lds, const Gemm g, const Sched& S, const Epi& E) {
;     ...
;         const bool has_next = S.next(ui + 1, nxt);
;         unsigned pend = 0u; if constexpr (Sched::DYNAMIC) pend = S.claim_issue(wid, lane);
;         const char* nA = has_next ? (const char*)(nxt.sel ? g.A2 : g.A) + (size_t)nxt.pm * tstep : cA; const char* nB = has_next ? (const char*)(nxt.sel ? g.Bt2 : g.Bt) + (size_t)nxt.pn * tstep : cB;
;         for (int t = 0; t < nt; t += 2) {
;             const bool last = (t == nt - 2);
;             const char* a1 = cA + (size_t)(t + 1) * kstep;
;             const char* a2 = last ? nA : cA + (size_t)(t + 2) * kstep; const char* b2 = last ? nB : cB + (size_t)(t + 2) * kstep;
;             const char* a3 = a2 + kstep; const char* b3 = b2 + kstep;
;     ...
; #pragma unroll
;         for (int a = 0; a < 2; ++a)
; #pragma unroll
;             for (int b = 0; b < 2; ++b)
; #pragma unroll
;                 for (int m = 0; m < 4; ++m)
; #pragma unroll
;                     for (int n = 0; n < 2; ++n) acc[a][b][m][n] = (f32x4){0.f, 0.f, 0.f, 0.f};
;         cur = nxt; cA = nA; cB = nB; ++ui;
.LBB0_1010:
	s_ashr_i32 s23, s22, 31
	s_lshl_b64 s[24:25], s[22:23], 20
	s_add_u32 s24, s6, s24
	s_addc_u32 s25, s7, s25
	s_and_b64 s[26:27], s[8:9], exec
	s_cselect_b32 s23, s25, s31
	s_cselect_b32 s53, s24, s30
	s_ashr_i32 s21, s20, 31
	s_lshl_b64 s[26:27], s[20:21], 20
	s_add_u32 s26, s33, s26
	s_addc_u32 s27, s38, s27
	s_and_b64 s[36:37], s[8:9], exec
	s_cselect_b32 s21, s27, s35
	s_cselect_b32 s54, s26, s34
	s_add_u32 s30, s30, 0x80080
	s_addc_u32 s31, s31, 0
	s_add_u32 s55, s34, 0x100
	v_mov_b32_e32 v2, 0
	s_addc_u32 s56, s35, 0
	s_mov_b32 s57, -2
	v_mov_b32_e32 v3, v2
	v_mov_b32_e32 v4, v2
	v_mov_b32_e32 v5, v2
	v_mov_b32_e32 v6, v2
	v_mov_b32_e32 v7, v2
	v_mov_b32_e32 v8, v2
	v_mov_b32_e32 v9, v2
	v_mov_b32_e32 v10, v2
	v_mov_b32_e32 v11, v2
	v_mov_b32_e32 v12, v2
	v_mov_b32_e32 v13, v2
	v_mov_b32_e32 v18, v2
	v_mov_b32_e32 v19, v2
	v_mov_b32_e32 v20, v2
	v_mov_b32_e32 v21, v2
	v_mov_b32_e32 v26, v2
	v_mov_b32_e32 v27, v2
	v_mov_b32_e32 v28, v2
	v_mov_b32_e32 v29, v2
	v_mov_b32_e32 v34, v2
	v_mov_b32_e32 v35, v2
	v_mov_b32_e32 v36, v2
	v_mov_b32_e32 v37, v2
	v_mov_b32_e32 v42, v2
	v_mov_b32_e32 v43, v2
	v_mov_b32_e32 v44, v2
	v_mov_b32_e32 v45, v2
	v_mov_b32_e32 v50, v2
	v_mov_b32_e32 v51, v2
	v_mov_b32_e32 v52, v2
	v_mov_b32_e32 v53, v2
	v_mov_b32_e32 v14, v2
	v_mov_b32_e32 v15, v2
	v_mov_b32_e32 v16, v2
	v_mov_b32_e32 v17, v2
	v_mov_b32_e32 v22, v2
	v_mov_b32_e32 v23, v2
	v_mov_b32_e32 v24, v2
	v_mov_b32_e32 v25, v2
	v_mov_b32_e32 v30, v2
	v_mov_b32_e32 v31, v2
	v_mov_b32_e32 v32, v2
	v_mov_b32_e32 v33, v2
	v_mov_b32_e32 v38, v2
	v_mov_b32_e32 v39, v2
	v_mov_b32_e32 v40, v2
	v_mov_b32_e32 v41, v2
	v_mov_b32_e32 v46, v2
	v_mov_b32_e32 v47, v2
	v_mov_b32_e32 v48, v2
	v_mov_b32_e32 v49, v2
	v_mov_b32_e32 v54, v2
	v_mov_b32_e32 v55, v2
	v_mov_b32_e32 v56, v2
	v_mov_b32_e32 v57, v2
	v_mov_b32_e32 v58, v2
	v_mov_b32_e32 v59, v2
	v_mov_b32_e32 v60, v2
	v_mov_b32_e32 v61, v2
	v_mov_b32_e32 v62, v2
	v_mov_b32_e32 v63, v2
	v_mov_b32_e32 v64, v2
	v_mov_b32_e32 v65, v2
	v_mov_b32_e32 v66, v2
	v_mov_b32_e32 v67, v2
	v_mov_b32_e32 v68, v2
	v_mov_b32_e32 v69, v2
	v_mov_b32_e32 v70, v2
	v_mov_b32_e32 v71, v2
	v_mov_b32_e32 v72, v2
	v_mov_b32_e32 v73, v2
	v_mov_b32_e32 v74, v2
	v_mov_b32_e32 v75, v2
	v_mov_b32_e32 v76, v2
	v_mov_b32_e32 v77, v2
	v_mov_b32_e32 v82, v2
	v_mov_b32_e32 v83, v2
	v_mov_b32_e32 v84, v2
	v_mov_b32_e32 v85, v2
	v_mov_b32_e32 v90, v2
	v_mov_b32_e32 v91, v2
	v_mov_b32_e32 v92, v2
	v_mov_b32_e32 v93, v2
	v_mov_b32_e32 v98, v2
	v_mov_b32_e32 v99, v2
	v_mov_b32_e32 v100, v2
	v_mov_b32_e32 v101, v2
	v_mov_b32_e32 v106, v2
	v_mov_b32_e32 v107, v2
	v_mov_b32_e32 v108, v2
	v_mov_b32_e32 v109, v2
	v_mov_b32_e32 v114, v2
	v_mov_b32_e32 v115, v2
	v_mov_b32_e32 v116, v2
	v_mov_b32_e32 v117, v2
	v_mov_b32_e32 v78, v2
	v_mov_b32_e32 v79, v2
	v_mov_b32_e32 v80, v2
	v_mov_b32_e32 v81, v2
	v_mov_b32_e32 v86, v2
	v_mov_b32_e32 v87, v2
	v_mov_b32_e32 v88, v2
	v_mov_b32_e32 v89, v2
	v_mov_b32_e32 v94, v2
	v_mov_b32_e32 v95, v2
	v_mov_b32_e32 v96, v2
	v_mov_b32_e32 v97, v2
	v_mov_b32_e32 v102, v2
	v_mov_b32_e32 v103, v2
	v_mov_b32_e32 v104, v2
	v_mov_b32_e32 v105, v2
	v_mov_b32_e32 v110, v2
	v_mov_b32_e32 v111, v2
	v_mov_b32_e32 v112, v2
	v_mov_b32_e32 v113, v2
	v_mov_b32_e32 v118, v2
	v_mov_b32_e32 v119, v2
	v_mov_b32_e32 v120, v2
	v_mov_b32_e32 v121, v2
	v_mov_b32_e32 v122, v2
	v_mov_b32_e32 v123, v2
	v_mov_b32_e32 v124, v2
	v_mov_b32_e32 v125, v2
	v_mov_b32_e32 v126, v2
	v_mov_b32_e32 v127, v2
	v_mov_b32_e32 v128, v2
	v_mov_b32_e32 v129, v2
	s_cmp_lg_u32 s98, 0
	s_cselect_b32 s99, -2, 0x7ffffff0
	s_branch .LBB0_1011

; #define PG8_STAGE(bufoff, gbase, voff) do { _Pragma("unroll") for (int _i = 0; _i < 2; ++_i) \
;         __builtin_amdgcn_global_load_lds((const unsigned*)((const char*)(gbase) + (voff)[_i]), (PG8_LAS unsigned*)(lds + (bufoff) + ldsw + _i * 8192), 16, 0, 0); } while (0)
; #define PG8_LDA(dst, b, h) do { _Pragma("unroll") for (int m = 0; m < 4; ++m) _Pragma("unroll") for (int k = 0; k < 2; ++k) dst[m][k] = *(const PG8_LAS bf16x8*)(lds + PG8_SA(b, h) + aoff + m * 2048 + k * 1024); } while (0)
; #define PG8_LDB(dst, b, h) do { _Pragma("unroll") for (int n = 0; n < 2; ++n) _Pragma("unroll") for (int k = 0; k < 2; ++k) dst[n][k] = *(const PG8_LAS bf16x8*)(lds + PG8_SB(b, h) + boff + n * 2048 + k * 1024); } while (0)
; #define PG8_MMA(ai, bj, At, Bt) do { __builtin_amdgcn_s_setprio(1); _Pragma("unroll") for (int m = 0; m < 4; ++m) _Pragma("unroll") for (int n = 0; n < 2; ++n) _Pragma("unroll") for (int k = 0; k < 2; ++k) \
;         acc[ai][bj][m][n] = __builtin_amdgcn_mfma_f32_16x16x32_bf16(Bt[n][k], At[m][k], acc[ai][bj][m][n], 0, 0, 0); __builtin_amdgcn_s_setprio(0); } while (0)
; #define PG8_WAIT_V(n) asm volatile("s_waitcnt vmcnt(" #n ")" ::: "memory")
; #define PG8_WAIT_L(n) asm volatile("s_waitcnt lgkmcnt(" #n ")" ::: "memory")
; #define PG8_BAR __builtin_amdgcn_s_barrier()
; #define PG8_SCHED __builtin_amdgcn_sched_barrier(0)
; #define PG8_STAGE(bufoff, gbase, voff) do { _Pragma("unroll") for (int _i = 0; _i < 2; ++_i) \
;         __builtin_amdgcn_global_load_lds((const unsigned*)((const char*)(gbase) + (voff)[_i]), (PG8_LAS unsigned*)(lds + (bufoff) + ldsw + _i * 8192), 16, 0, 0); } while (0)
; template <class Epi, class Sched, bool ALIGN_EPI = false, bool SP2 = false>
; __device__ __forceinline__ void gemm_phase(PG8_LAS unsigned char* lds, const Gemm g, const Sched& S, const Epi& E) {
;     ...
;             if constexpr (SP2) {
;             PG8_LDB(B0, 0, 0); PG8_LDB(B1, 0, 1); PG8_SCHED; PG8_LDA(At, 0, 0); PG8_STAGE(PG8_SA(1, 1), a1 + hstep, voffA);
;             PG8_WAIT_V(8); PG8_WAIT_L(0); PG8_BAR; PG8_MMA(0, 0, At, B0); PG8_MMA(0, 1, At, B1); PG8_BAR; PG8_SCHED;
;             PG8_LDA(At, 0, 1); PG8_STAGE(PG8_SB(0, 0), b2, voffB); PG8_STAGE(PG8_SB(0, 1), b2 + hstep, voffB); PG8_STAGE(PG8_SA(0, 0), a2, voffA);
;             PG8_WAIT_V(8); PG8_WAIT_L(0); PG8_BAR; PG8_MMA(1, 0, At, B0); PG8_MMA(1, 1, At, B1); PG8_BAR; PG8_SCHED;
.LBB0_1011:
	ds_read_b128 v[154:157], v150
	ds_read_b128 v[158:161], v150 offset:1024
	ds_read_b128 v[162:165], v150 offset:2048
	ds_read_b128 v[166:169], v150 offset:3072
	ds_read_b128 v[170:173], v151
	ds_read_b128 v[174:177], v151 offset:1024
	ds_read_b128 v[178:181], v151 offset:2048
	ds_read_b128 v[182:185], v151 offset:3072
	s_add_u32 s34, s30, 0xfff80080
	s_addc_u32 s35, s31, -1
	s_cmp_eq_u32 s57, 28
	s_cselect_b32 s37, s23, s35
	s_cselect_b32 s36, s53, s34
	s_cselect_b32 s35, s21, s56
	s_cselect_b32 s34, s54, s55
	v_lshl_add_u64 v[146:147], s[30:31], 0, v[138:139]
	s_add_i32 m0, s29, 0xc000
	ds_read_b128 v[188:191], v152
	ds_read_b128 v[192:195], v152 offset:1024
	ds_read_b128 v[196:199], v152 offset:2048
	ds_read_b128 v[200:203], v152 offset:3072
	ds_read_b128 v[204:207], v152 offset:4096
	ds_read_b128 v[208:211], v152 offset:5120
	ds_read_b128 v[212:215], v152 offset:6144
	ds_read_b128 v[216:219], v152 offset:7168
	global_load_lds_dwordx4 v[146:147], off
	v_lshl_add_u64 v[146:147], s[30:31], 0, v[140:141]
	s_add_i32 m0, s29, 0xe000
	s_nop 0
	global_load_lds_dwordx4 v[146:147], off
	s_cmp_eq_u32 s57, s99
	s_cbranch_scc1 .Lrx7_a
	s_waitcnt vmcnt(8)
.Lrx7_a_done:
	s_waitcnt lgkmcnt(0)
	s_barrier
	s_setprio 1
	s_waitcnt lgkmcnt(0)
	v_mfma_f32_16x16x32_bf16 v[126:129], v[154:157], v[188:191], v[126:129]
	v_mfma_f32_16x16x32_bf16 v[122:125], v[162:165], v[188:191], v[122:125]
	v_mfma_f32_16x16x32_bf16 v[118:121], v[154:157], v[196:199], v[118:121]
	v_mfma_f32_16x16x32_bf16 v[110:113], v[162:165], v[196:199], v[110:113]
	v_mfma_f32_16x16x32_bf16 v[102:105], v[154:157], v[204:207], v[102:105]
	v_mfma_f32_16x16x32_bf16 v[94:97], v[162:165], v[204:207], v[94:97]
	v_mfma_f32_16x16x32_bf16 v[86:89], v[154:157], v[212:215], v[86:89]
	v_mfma_f32_16x16x32_bf16 v[78:81], v[162:165], v[212:215], v[78:81]
	v_mfma_f32_16x16x32_bf16 v[126:129], v[158:161], v[192:195], v[126:129]
	v_mfma_f32_16x16x32_bf16 v[122:125], v[166:169], v[192:195], v[122:125]
	v_mfma_f32_16x16x32_bf16 v[118:121], v[158:161], v[200:203], v[118:121]
	v_mfma_f32_16x16x32_bf16 v[110:113], v[166:169], v[200:203], v[110:113]
	v_mfma_f32_16x16x32_bf16 v[102:105], v[158:161], v[208:211], v[102:105]
	v_mfma_f32_16x16x32_bf16 v[94:97], v[166:169], v[208:211], v[94:97]
	v_mfma_f32_16x16x32_bf16 v[86:89], v[158:161], v[216:219], v[86:89]
	v_mfma_f32_16x16x32_bf16 v[78:81], v[166:169], v[216:219], v[78:81]
	s_setprio 0
	s_setprio 1
	v_mfma_f32_16x16x32_bf16 v[114:117], v[170:173], v[188:191], v[114:117]
	v_mfma_f32_16x16x32_bf16 v[106:109], v[178:181], v[188:191], v[106:109]
	v_mfma_f32_16x16x32_bf16 v[98:101], v[170:173], v[196:199], v[98:101]
	v_mfma_f32_16x16x32_bf16 v[90:93], v[178:181], v[196:199], v[90:93]
	v_mfma_f32_16x16x32_bf16 v[82:85], v[170:173], v[204:207], v[82:85]
	v_mfma_f32_16x16x32_bf16 v[74:77], v[178:181], v[204:207], v[74:77]
	v_mfma_f32_16x16x32_bf16 v[70:73], v[170:173], v[212:215], v[70:73]
	v_mfma_f32_16x16x32_bf16 v[66:69], v[178:181], v[212:215], v[66:69]
	v_mfma_f32_16x16x32_bf16 v[114:117], v[174:177], v[192:195], v[114:117]
	v_mfma_f32_16x16x32_bf16 v[106:109], v[182:185], v[192:195], v[106:109]
	v_mfma_f32_16x16x32_bf16 v[98:101], v[174:177], v[200:203], v[98:101]
	v_mfma_f32_16x16x32_bf16 v[90:93], v[182:185], v[200:203], v[90:93]
	v_mfma_f32_16x16x32_bf16 v[82:85], v[174:177], v[208:211], v[82:85]
	v_mfma_f32_16x16x32_bf16 v[74:77], v[182:185], v[208:211], v[74:77]
	v_mfma_f32_16x16x32_bf16 v[70:73], v[174:177], v[216:219], v[70:73]
	v_mfma_f32_16x16x32_bf16 v[66:69], v[182:185], v[216:219], v[66:69]
	s_setprio 0
	s_barrier
	s_add_i32 s58, s46, s39
	v_lshl_add_u64 v[146:147], s[34:35], 0, v[132:133]
	s_mov_b32 m0, s58
	ds_read_b128 v[188:191], v152 offset:16384
	ds_read_b128 v[192:195], v152 offset:17408
	ds_read_b128 v[196:199], v152 offset:18432
	ds_read_b128 v[200:203], v152 offset:19456
	ds_read_b128 v[204:207], v152 offset:20480
	ds_read_b128 v[208:211], v152 offset:21504
	ds_read_b128 v[212:215], v152 offset:22528
	ds_read_b128 v[216:219], v152 offset:23552
	global_load_lds_dwordx4 v[146:147], off
	s_add_i32 m0, s58, 0x2000
	s_add_u32 s58, s34, 0x80000
	v_lshl_add_u64 v[220:221], s[34:35], 0, v[136:137]
	s_addc_u32 s59, s35, 0
	s_add_i32 s60, s47, s39
	global_load_lds_dwordx4 v[220:221], off
	v_lshl_add_u64 v[222:223], s[58:59], 0, v[132:133]
	s_mov_b32 m0, s60
	v_lshl_add_u64 v[224:225], s[36:37], 0, v[134:135]
	global_load_lds_dwordx4 v[222:223], off
	v_lshl_add_u64 v[222:223], s[58:59], 0, v[136:137]
	s_add_i32 m0, s60, 0x2000
	s_nop 0
	global_load_lds_dwordx4 v[222:223], off
	v_lshl_add_u64 v[222:223], s[36:37], 0, v[130:131]
	s_mov_b32 m0, s29
	s_nop 0
	global_load_lds_dwordx4 v[222:223], off
	s_mov_b32 m0, s40
	s_nop 0
	global_load_lds_dwordx4 v[224:225], off
	s_cmp_eq_u32 s57, s99
	s_cbranch_scc1 .Lrx7_b
	s_waitcnt vmcnt(8)
; #define PG8_STAGE(bufoff, gbase, voff) do { _Pragma("unroll") for (int _i = 0; _i < 2; ++_i) \
;         __builtin_amdgcn_global_load_lds((const unsigned*)((const char*)(gbase) + (voff)[_i]), (PG8_LAS unsigned*)(lds + (bufoff) + ldsw + _i * 8192), 16, 0, 0); } while (0)
; #define PG8_LDA(dst, b, h) do { _Pragma("unroll") for (int m = 0; m < 4; ++m) _Pragma("unroll") for (int k = 0; k < 2; ++k) dst[m][k] = *(const PG8_LAS bf16x8*)(lds + PG8_SA(b, h) + aoff + m * 2048 + k * 1024); } while (0)
; #define PG8_LDB(dst, b, h) do { _Pragma("unroll") for (int n = 0; n < 2; ++n) _Pragma("unroll") for (int k = 0; k < 2; ++k) dst[n][k] = *(const PG8_LAS bf16x8*)(lds + PG8_SB(b, h) + boff + n * 2048 + k * 1024); } while (0)
; #define PG8_MMA(ai, bj, At, Bt) do { __builtin_amdgcn_s_setprio(1); _Pragma("unroll") for (int m = 0; m < 4; ++m) _Pragma("unroll") for (int n = 0; n < 2; ++n) _Pragma("unroll") for (int k = 0; k < 2; ++k) \
;         acc[ai][bj][m][n] = __builtin_amdgcn_mfma_f32_16x16x32_bf16(Bt[n][k], At[m][k], acc[ai][bj][m][n], 0, 0, 0); __builtin_amdgcn_s_setprio(0); } while (0)
; #define PG8_WAIT_V(n) asm volatile("s_waitcnt vmcnt(" #n ")" ::: "memory")
; #define PG8_WAIT_L(n) asm volatile("s_waitcnt lgkmcnt(" #n ")" ::: "memory")
; #define PG8_BAR __builtin_amdgcn_s_barrier()
; #define PG8_SCHED __builtin_amdgcn_sched_barrier(0)
; #define PG8_STAGE(bufoff, gbase, voff) do { _Pragma("unroll") for (int _i = 0; _i < 2; ++_i) \
;         __builtin_amdgcn_global_load_lds((const unsigned*)((const char*)(gbase) + (voff)[_i]), (PG8_LAS unsigned*)(lds + (bufoff) + ldsw + _i * 8192), 16, 0, 0); } while (0)
; #define PG8_WAIT_V(n) asm volatile("s_waitcnt vmcnt(" #n ")" ::: "memory")
; #define PG8_WAIT_L(n) asm volatile("s_waitcnt lgkmcnt(" #n ")" ::: "memory")
; #define PG8_BAR __builtin_amdgcn_s_barrier()
; template <class Epi, class Sched, bool ALIGN_EPI = false, bool SP2 = false>
; __device__ __forceinline__ void gemm_phase(PG8_LAS unsigned char* lds, const Gemm g, const Sched& S, const Epi& E) {
;     ...
;             PG8_WAIT_V(8); PG8_WAIT_L(0); PG8_BAR; PG8_MMA(1, 0, At, B0); PG8_MMA(1, 1, At, B1); PG8_BAR; PG8_SCHED;
;             PG8_LDB(B0, 1, 0); PG8_LDB(B1, 1, 1); PG8_SCHED; PG8_LDA(At, 1, 0); PG8_STAGE(PG8_SA(0, 1), a2 + hstep, voffA);
;             PG8_WAIT_V(8); PG8_WAIT_L(0); PG8_BAR; PG8_MMA(0, 0, At, B0); PG8_MMA(0, 1, At, B1); PG8_BAR; PG8_SCHED;
.Lrx7_b_done:
	s_waitcnt lgkmcnt(0)
	s_barrier
	s_setprio 1
	s_waitcnt lgkmcnt(0)
	v_mfma_f32_16x16x32_bf16 v[62:65], v[154:157], v[188:191], v[62:65]
	v_mfma_f32_16x16x32_bf16 v[58:61], v[162:165], v[188:191], v[58:61]
	v_mfma_f32_16x16x32_bf16 v[54:57], v[154:157], v[196:199], v[54:57]
	v_mfma_f32_16x16x32_bf16 v[46:49], v[162:165], v[196:199], v[46:49]
	v_mfma_f32_16x16x32_bf16 v[38:41], v[154:157], v[204:207], v[38:41]
	v_mfma_f32_16x16x32_bf16 v[30:33], v[162:165], v[204:207], v[30:33]
	v_mfma_f32_16x16x32_bf16 v[22:25], v[154:157], v[212:215], v[22:25]
	v_mfma_f32_16x16x32_bf16 v[14:17], v[162:165], v[212:215], v[14:17]
	v_mfma_f32_16x16x32_bf16 v[62:65], v[158:161], v[192:195], v[62:65]
	v_mfma_f32_16x16x32_bf16 v[58:61], v[166:169], v[192:195], v[58:61]
	v_mfma_f32_16x16x32_bf16 v[54:57], v[158:161], v[200:203], v[54:57]
	v_mfma_f32_16x16x32_bf16 v[46:49], v[166:169], v[200:203], v[46:49]
	v_mfma_f32_16x16x32_bf16 v[38:41], v[158:161], v[208:211], v[38:41]
	v_mfma_f32_16x16x32_bf16 v[30:33], v[166:169], v[208:211], v[30:33]
	v_mfma_f32_16x16x32_bf16 v[22:25], v[158:161], v[216:219], v[22:25]
	v_mfma_f32_16x16x32_bf16 v[14:17], v[166:169], v[216:219], v[14:17]
	s_setprio 0
	s_setprio 1
	v_mfma_f32_16x16x32_bf16 v[50:53], v[170:173], v[188:191], v[50:53]
	v_mfma_f32_16x16x32_bf16 v[42:45], v[178:181], v[188:191], v[42:45]
	v_mfma_f32_16x16x32_bf16 v[34:37], v[170:173], v[196:199], v[34:37]
	v_mfma_f32_16x16x32_bf16 v[26:29], v[178:181], v[196:199], v[26:29]
	v_mfma_f32_16x16x32_bf16 v[18:21], v[170:173], v[204:207], v[18:21]
	v_mfma_f32_16x16x32_bf16 v[10:13], v[178:181], v[204:207], v[10:13]
	v_mfma_f32_16x16x32_bf16 v[6:9], v[170:173], v[212:215], v[6:9]
	v_mfma_f32_16x16x32_bf16 v[2:5], v[178:181], v[212:215], v[2:5]
	v_mfma_f32_16x16x32_bf16 v[50:53], v[174:177], v[192:195], v[50:53]
	v_mfma_f32_16x16x32_bf16 v[42:45], v[182:185], v[192:195], v[42:45]
	v_mfma_f32_16x16x32_bf16 v[34:37], v[174:177], v[200:203], v[34:37]
	v_mfma_f32_16x16x32_bf16 v[26:29], v[182:185], v[200:203], v[26:29]
	v_mfma_f32_16x16x32_bf16 v[18:21], v[174:177], v[208:211], v[18:21]
	v_mfma_f32_16x16x32_bf16 v[10:13], v[182:185], v[208:211], v[10:13]
	v_mfma_f32_16x16x32_bf16 v[6:9], v[174:177], v[216:219], v[6:9]
	v_mfma_f32_16x16x32_bf16 v[2:5], v[182:185], v[216:219], v[2:5]
	s_setprio 0
	s_barrier
	s_add_i32 s58, 0, 0x18000
	v_add_u32_e32 v153, s58, v148
	s_add_i32 s59, 0, 0x1c000
	ds_read_b128 v[154:157], v153
	ds_read_b128 v[158:161], v153 offset:1024
	ds_read_b128 v[162:165], v153 offset:2048
	ds_read_b128 v[166:169], v153 offset:3072
	v_add_u32_e32 v153, s59, v148
	ds_read_b128 v[170:173], v153
	ds_read_b128 v[174:177], v153 offset:1024
	ds_read_b128 v[178:181], v153 offset:2048
	ds_read_b128 v[182:185], v153 offset:3072
	s_add_u32 s36, s36, 0x80000
	s_addc_u32 s37, s37, 0
	s_mov_b32 m0, s41
	v_lshl_add_u64 v[226:227], s[36:37], 0, v[130:131]
	ds_read_b128 v[188:191], v152 offset:32768
	ds_read_b128 v[192:195], v152 offset:33792
	ds_read_b128 v[196:199], v152 offset:34816
	ds_read_b128 v[200:203], v152 offset:35840
	ds_read_b128 v[204:207], v152 offset:36864
	ds_read_b128 v[208:211], v152 offset:37888
	ds_read_b128 v[212:215], v152 offset:38912
	ds_read_b128 v[216:219], v152 offset:39936
	global_load_lds_dwordx4 v[226:227], off
	v_lshl_add_u64 v[226:227], s[36:37], 0, v[134:135]
	s_mov_b32 m0, s42
	s_nop 0
	global_load_lds_dwordx4 v[226:227], off
	s_waitcnt vmcnt(8)
	s_waitcnt lgkmcnt(0)
	s_barrier
	s_setprio 1
	s_waitcnt lgkmcnt(0)
	v_mfma_f32_16x16x32_bf16 v[126:129], v[154:157], v[188:191], v[126:129]
	v_mfma_f32_16x16x32_bf16 v[122:125], v[162:165], v[188:191], v[122:125]
	v_mfma_f32_16x16x32_bf16 v[118:121], v[154:157], v[196:199], v[118:121]
	v_mfma_f32_16x16x32_bf16 v[110:113], v[162:165], v[196:199], v[110:113]
	v_mfma_f32_16x16x32_bf16 v[102:105], v[154:157], v[204:207], v[102:105]
	v_mfma_f32_16x16x32_bf16 v[94:97], v[162:165], v[204:207], v[94:97]
	v_mfma_f32_16x16x32_bf16 v[86:89], v[154:157], v[212:215], v[86:89]
	v_mfma_f32_16x16x32_bf16 v[78:81], v[162:165], v[212:215], v[78:81]
	v_mfma_f32_16x16x32_bf16 v[126:129], v[158:161], v[192:195], v[126:129]
	v_mfma_f32_16x16x32_bf16 v[122:125], v[166:169], v[192:195], v[122:125]
	v_mfma_f32_16x16x32_bf16 v[118:121], v[158:161], v[200:203], v[118:121]
	v_mfma_f32_16x16x32_bf16 v[110:113], v[166:169], v[200:203], v[110:113]
	v_mfma_f32_16x16x32_bf16 v[102:105], v[158:161], v[208:211], v[102:105]
	v_mfma_f32_16x16x32_bf16 v[94:97], v[166:169], v[208:211], v[94:97]
	v_mfma_f32_16x16x32_bf16 v[86:89], v[158:161], v[216:219], v[86:89]
	v_mfma_f32_16x16x32_bf16 v[78:81], v[166:169], v[216:219], v[78:81]
	s_setprio 0
	s_setprio 1
	v_mfma_f32_16x16x32_bf16 v[114:117], v[170:173], v[188:191], v[114:117]
	v_mfma_f32_16x16x32_bf16 v[106:109], v[178:181], v[188:191], v[106:109]
	v_mfma_f32_16x16x32_bf16 v[98:101], v[170:173], v[196:199], v[98:101]
	v_mfma_f32_16x16x32_bf16 v[90:93], v[178:181], v[196:199], v[90:93]
	v_mfma_f32_16x16x32_bf16 v[82:85], v[170:173], v[204:207], v[82:85]
	v_mfma_f32_16x16x32_bf16 v[74:77], v[178:181], v[204:207], v[74:77]
	v_mfma_f32_16x16x32_bf16 v[70:73], v[170:173], v[212:215], v[70:73]
	v_mfma_f32_16x16x32_bf16 v[66:69], v[178:181], v[212:215], v[66:69]
	v_mfma_f32_16x16x32_bf16 v[114:117], v[174:177], v[192:195], v[114:117]
	v_mfma_f32_16x16x32_bf16 v[106:109], v[182:185], v[192:195], v[106:109]
	v_mfma_f32_16x16x32_bf16 v[98:101], v[174:177], v[200:203], v[98:101]
	v_mfma_f32_16x16x32_bf16 v[90:93], v[182:185], v[200:203], v[90:93]
	v_mfma_f32_16x16x32_bf16 v[82:85], v[174:177], v[208:211], v[82:85]
	v_mfma_f32_16x16x32_bf16 v[74:77], v[182:185], v[208:211], v[74:77]
	v_mfma_f32_16x16x32_bf16 v[70:73], v[174:177], v[216:219], v[70:73]
	v_mfma_f32_16x16x32_bf16 v[66:69], v[182:185], v[216:219], v[66:69]
	s_setprio 0
	s_barrier
; #define PG8_STAGE(bufoff, gbase, voff) do { _Pragma("unroll") for (int _i = 0; _i < 2; ++_i) \
;         __builtin_amdgcn_global_load_lds((const unsigned*)((const char*)(gbase) + (voff)[_i]), (PG8_LAS unsigned*)(lds + (bufoff) + ldsw + _i * 8192), 16, 0, 0); } while (0)
; #define PG8_LDA(dst, b, h) do { _Pragma("unroll") for (int m = 0; m < 4; ++m) _Pragma("unroll") for (int k = 0; k < 2; ++k) dst[m][k] = *(const PG8_LAS bf16x8*)(lds + PG8_SA(b, h) + aoff + m * 2048 + k * 1024); } while (0)
; #define PG8_MMA(ai, bj, At, Bt) do { __builtin_amdgcn_s_setprio(1); _Pragma("unroll") for (int m = 0; m < 4; ++m) _Pragma("unroll") for (int n = 0; n < 2; ++n) _Pragma("unroll") for (int k = 0; k < 2; ++k) \
;         acc[ai][bj][m][n] = __builtin_amdgcn_mfma_f32_16x16x32_bf16(Bt[n][k], At[m][k], acc[ai][bj][m][n], 0, 0, 0); __builtin_amdgcn_s_setprio(0); } while (0)
; #define PG8_WAIT_V(n) asm volatile("s_waitcnt vmcnt(" #n ")" ::: "memory")
; #define PG8_WAIT_L(n) asm volatile("s_waitcnt lgkmcnt(" #n ")" ::: "memory")
; #define PG8_BAR __builtin_amdgcn_s_barrier()
; #define PG8_SCHED __builtin_amdgcn_sched_barrier(0)
; #define PG8_STAGE(bufoff, gbase, voff) do { _Pragma("unroll") for (int _i = 0; _i < 2; ++_i) \
;         __builtin_amdgcn_global_load_lds((const unsigned*)((const char*)(gbase) + (voff)[_i]), (PG8_LAS unsigned*)(lds + (bufoff) + ldsw + _i * 8192), 16, 0, 0); } while (0)
; #define PG8_LDA(dst, b, h) do { _Pragma("unroll") for (int m = 0; m < 4; ++m) _Pragma("unroll") for (int k = 0; k < 2; ++k) dst[m][k] = *(const PG8_LAS bf16x8*)(lds + PG8_SA(b, h) + aoff + m * 2048 + k * 1024); } while (0)
; #define PG8_WAIT_V(n) asm volatile("s_waitcnt vmcnt(" #n ")" ::: "memory")
; #define PG8_WAIT_L(n) asm volatile("s_waitcnt lgkmcnt(" #n ")" ::: "memory")
; #define PG8_BAR __builtin_amdgcn_s_barrier()
; template <class Epi, class Sched, bool ALIGN_EPI = false, bool SP2 = false>
; __device__ __forceinline__ void gemm_phase(PG8_LAS unsigned char* lds, const Gemm g, const Sched& S, const Epi& E) {
;     ...
;             PG8_LDA(At, 1, 1); PG8_STAGE(PG8_SB(1, 0), b3, voffB); PG8_STAGE(PG8_SB(1, 1), b3 + hstep, voffB); PG8_STAGE(PG8_SA(1, 0), a3, voffA);
;             PG8_WAIT_V(8); PG8_WAIT_L(0); PG8_BAR; PG8_MMA(1, 0, At, B0); PG8_MMA(1, 1, At, B1); PG8_BAR; PG8_SCHED;
;     ...
;         if constexpr (ALIGN_EPI) { if (wr == 0) PG8_BAR; }
	s_add_i32 s36, s58, s39
	v_lshl_add_u64 v[146:147], v[146:147], 0, s[10:11]
	s_mov_b32 m0, s36
	ds_read_b128 v[188:191], v152 offset:49152
	ds_read_b128 v[192:195], v152 offset:50176
	ds_read_b128 v[196:199], v152 offset:51200
	ds_read_b128 v[200:203], v152 offset:52224
	ds_read_b128 v[204:207], v152 offset:53248
	ds_read_b128 v[208:211], v152 offset:54272
	ds_read_b128 v[212:215], v152 offset:55296
	ds_read_b128 v[216:219], v152 offset:56320
	global_load_lds_dwordx4 v[146:147], off
	s_add_i32 m0, s36, 0x2000
	s_add_u32 s34, s34, 0x80080
	v_lshl_add_u64 v[146:147], v[220:221], 0, s[10:11]
	s_addc_u32 s35, s35, 0
	s_add_i32 s36, s59, s39
	global_load_lds_dwordx4 v[146:147], off
	v_lshl_add_u64 v[146:147], s[34:35], 0, v[132:133]
	s_mov_b32 m0, s36
	s_nop 0
	global_load_lds_dwordx4 v[146:147], off
	v_lshl_add_u64 v[146:147], s[34:35], 0, v[136:137]
	s_add_i32 m0, s36, 0x2000
	s_nop 0
	global_load_lds_dwordx4 v[146:147], off
	v_lshl_add_u64 v[146:147], v[222:223], 0, s[10:11]
	s_mov_b32 m0, s44
	s_nop 0
	global_load_lds_dwordx4 v[146:147], off
	v_lshl_add_u64 v[146:147], v[224:225], 0, s[10:11]
	s_mov_b32 m0, s45
	s_nop 0
	global_load_lds_dwordx4 v[146:147], off
	s_waitcnt vmcnt(8)
	s_waitcnt lgkmcnt(0)
	s_barrier
	s_setprio 1
	s_waitcnt lgkmcnt(0)
	v_mfma_f32_16x16x32_bf16 v[62:65], v[154:157], v[188:191], v[62:65]
	v_mfma_f32_16x16x32_bf16 v[58:61], v[162:165], v[188:191], v[58:61]
	v_mfma_f32_16x16x32_bf16 v[54:57], v[154:157], v[196:199], v[54:57]
	v_mfma_f32_16x16x32_bf16 v[46:49], v[162:165], v[196:199], v[46:49]
	v_mfma_f32_16x16x32_bf16 v[38:41], v[154:157], v[204:207], v[38:41]
	v_mfma_f32_16x16x32_bf16 v[30:33], v[162:165], v[204:207], v[30:33]
	v_mfma_f32_16x16x32_bf16 v[22:25], v[154:157], v[212:215], v[22:25]
	v_mfma_f32_16x16x32_bf16 v[14:17], v[162:165], v[212:215], v[14:17]
	v_mfma_f32_16x16x32_bf16 v[62:65], v[158:161], v[192:195], v[62:65]
	v_mfma_f32_16x16x32_bf16 v[58:61], v[166:169], v[192:195], v[58:61]
	v_mfma_f32_16x16x32_bf16 v[54:57], v[158:161], v[200:203], v[54:57]
	v_mfma_f32_16x16x32_bf16 v[46:49], v[166:169], v[200:203], v[46:49]
	v_mfma_f32_16x16x32_bf16 v[38:41], v[158:161], v[208:211], v[38:41]
	v_mfma_f32_16x16x32_bf16 v[30:33], v[166:169], v[208:211], v[30:33]
	v_mfma_f32_16x16x32_bf16 v[22:25], v[158:161], v[216:219], v[22:25]
	v_mfma_f32_16x16x32_bf16 v[14:17], v[166:169], v[216:219], v[14:17]
	s_setprio 0
	s_setprio 1
	v_mfma_f32_16x16x32_bf16 v[50:53], v[170:173], v[188:191], v[50:53]
	v_mfma_f32_16x16x32_bf16 v[42:45], v[178:181], v[188:191], v[42:45]
	v_mfma_f32_16x16x32_bf16 v[34:37], v[170:173], v[196:199], v[34:37]
	v_mfma_f32_16x16x32_bf16 v[26:29], v[178:181], v[196:199], v[26:29]
	v_mfma_f32_16x16x32_bf16 v[18:21], v[170:173], v[204:207], v[18:21]
	v_mfma_f32_16x16x32_bf16 v[10:13], v[178:181], v[204:207], v[10:13]
	v_mfma_f32_16x16x32_bf16 v[6:9], v[170:173], v[212:215], v[6:9]
	v_mfma_f32_16x16x32_bf16 v[2:5], v[178:181], v[212:215], v[2:5]
	v_mfma_f32_16x16x32_bf16 v[50:53], v[174:177], v[192:195], v[50:53]
	v_mfma_f32_16x16x32_bf16 v[42:45], v[182:185], v[192:195], v[42:45]
	v_mfma_f32_16x16x32_bf16 v[34:37], v[174:177], v[200:203], v[34:37]
	v_mfma_f32_16x16x32_bf16 v[26:29], v[182:185], v[200:203], v[26:29]
	v_mfma_f32_16x16x32_bf16 v[18:21], v[174:177], v[208:211], v[18:21]
	v_mfma_f32_16x16x32_bf16 v[10:13], v[182:185], v[208:211], v[10:13]
	v_mfma_f32_16x16x32_bf16 v[6:9], v[174:177], v[216:219], v[6:9]
	v_mfma_f32_16x16x32_bf16 v[2:5], v[182:185], v[216:219], v[2:5]
	s_setprio 0
	s_barrier
	s_add_i32 s57, s57, 2
	s_add_u32 s30, s30, 0x100
	s_addc_u32 s31, s31, 0
	s_add_u32 s55, s55, 0x100
	s_addc_u32 s56, s56, 0
	s_cmp_gt_u32 s57, 29
	s_cbranch_scc0 .LBB0_1011
	s_and_b64 vcc, exec, s[12:13]
	s_cbranch_vccz .LBB0_1014
	s_barrier
; __device__ __forceinline__ unsigned cvt_pk_bf16(float lo, float hi) { unsigned r; asm volatile("v_cvt_pk_bf16_f32 %0, %1, %2" : "=v"(r) : "v"(lo), "v"(hi)); return r; }
; #define PG8_BAR __builtin_amdgcn_s_barrier()
; #define PG8_BAR __builtin_amdgcn_s_barrier()
; template <class Epi, class Sched, bool ALIGN_EPI = false, bool SP2 = false>
; __device__ __forceinline__ void gemm_phase(PG8_LAS unsigned char* lds, const Gemm g, const Sched& S, const Epi& E) {
;     ...
;         if constexpr (!Epi::AFTER_DRAIN) { E(acc, cur, wr, wc, fr, fq); S.done(cur); }
;         if (!has_next) break;
; #pragma unroll
;         for (int a = 0; a < 2; ++a)
; #pragma unroll
;             for (int b = 0; b < 2; ++b)
; #pragma unroll
;                 for (int m = 0; m < 4; ++m)
; #pragma unroll
;                     for (int n = 0; n < 2; ++n) acc[a][b][m][n] = (f32x4){0.f, 0.f, 0.f, 0.f};
;         cur = nxt; cA = nA; cB = nB; ++ui;
;         if constexpr (ALIGN_EPI) { if (wr == 1) PG8_BAR; }
;     __device__ __forceinline__ void operator()(const f32x4 (&acc)[2][2][4][2], const pg8::Unit& u, int wr, int wc, int fr, int fq) const {
;         const int row0 = u.pm * 256 + wr * 64 + fr, col0 = u.pn * 256 + wc * 32 + 8 * fq;
; #pragma unroll
;         for (int ai = 0; ai < 2; ++ai)
; #pragma unroll
;             for (int m = 0; m < 4; ++m) { bf16* rowp = O + (size_t)(row0 + ai * 128 + m * 16) * ldc + col0;
; #pragma unroll
;                 for (int bj = 0; bj < 2; ++bj) { const f32x4 v0 = acc[ai][bj][m][0], v1 = acc[ai][bj][m][1];
;                     u32x4 w; w.x = pg8::cvt_pk_bf16(v0[0], v0[1]); w.y = pg8::cvt_pk_bf16(v0[2], v0[3]); w.z = pg8::cvt_pk_bf16(v1[0], v1[1]); w.w = pg8::cvt_pk_bf16(v1[2], v1[3]);
;                     *(u32x4*)(rowp + bj * 128) = w; } }
.LBB0_1014:
	v_lshl_add_u32 v154, s28, 8, v1
	v_lshl_or_b32 v146, s52, 8, v149
	v_ashrrev_i32_e32 v155, 31, v154
	v_ashrrev_i32_e32 v147, 31, v146
	v_lshlrev_b64 v[156:157], 12, v[154:155]
	v_lshl_add_u64 v[156:157], s[4:5], 0, v[156:157]
	v_lshlrev_b64 v[158:159], 1, v[146:147]
	v_lshl_add_u64 v[146:147], v[156:157], 0, v[158:159]
	v_cvt_pk_bf16_f32 v126, v126, v127
	v_cvt_pk_bf16_f32 v127, v128, v129
	v_cvt_pk_bf16_f32 v128, v122, v123
	v_cvt_pk_bf16_f32 v129, v124, v125
	global_store_dwordx4 v[146:147], v[126:129], off
	v_cvt_pk_bf16_f32 v114, v114, v115
	v_cvt_pk_bf16_f32 v115, v116, v117
	v_cvt_pk_bf16_f32 v116, v106, v107
	v_or_b32_e32 v106, 16, v154
	v_ashrrev_i32_e32 v107, 31, v106
	v_lshlrev_b64 v[106:107], 12, v[106:107]
	v_lshl_add_u64 v[106:107], s[4:5], 0, v[106:107]
	v_cvt_pk_bf16_f32 v117, v108, v109
	global_store_dwordx4 v[146:147], v[114:117], off offset:256
	s_nop 1
	v_lshl_add_u64 v[114:115], v[106:107], 0, v[158:159]
	v_cvt_pk_bf16_f32 v106, v118, v119
	v_cvt_pk_bf16_f32 v107, v120, v121
	v_cvt_pk_bf16_f32 v108, v110, v111
	v_cvt_pk_bf16_f32 v109, v112, v113
	global_store_dwordx4 v[114:115], v[106:109], off
	v_cvt_pk_bf16_f32 v98, v98, v99
	v_cvt_pk_bf16_f32 v99, v100, v101
	v_cvt_pk_bf16_f32 v100, v90, v91
	v_or_b32_e32 v90, 32, v154
	v_ashrrev_i32_e32 v91, 31, v90
	v_lshlrev_b64 v[90:91], 12, v[90:91]
	v_lshl_add_u64 v[90:91], s[4:5], 0, v[90:91]
	v_cvt_pk_bf16_f32 v101, v92, v93
	global_store_dwordx4 v[114:115], v[98:101], off offset:256
	s_nop 1
	v_lshl_add_u64 v[98:99], v[90:91], 0, v[158:159]
	v_cvt_pk_bf16_f32 v90, v102, v103
	v_cvt_pk_bf16_f32 v91, v104, v105
	v_cvt_pk_bf16_f32 v92, v94, v95
	v_cvt_pk_bf16_f32 v93, v96, v97
	global_store_dwordx4 v[98:99], v[90:93], off
	v_cvt_pk_bf16_f32 v82, v82, v83
	v_cvt_pk_bf16_f32 v83, v84, v85
	v_cvt_pk_bf16_f32 v84, v74, v75
	v_or_b32_e32 v74, 48, v154
	v_ashrrev_i32_e32 v75, 31, v74
	v_lshlrev_b64 v[74:75], 12, v[74:75]
	v_lshl_add_u64 v[74:75], s[4:5], 0, v[74:75]
	v_cvt_pk_bf16_f32 v85, v76, v77
	global_store_dwordx4 v[98:99], v[82:85], off offset:256
	s_nop 1
	v_lshl_add_u64 v[82:83], v[74:75], 0, v[158:159]
	v_cvt_pk_bf16_f32 v74, v86, v87
	v_cvt_pk_bf16_f32 v75, v88, v89
	v_cvt_pk_bf16_f32 v76, v78, v79
	v_cvt_pk_bf16_f32 v77, v80, v81
	global_store_dwordx4 v[82:83], v[74:77], off
	v_cvt_pk_bf16_f32 v70, v70, v71
	v_cvt_pk_bf16_f32 v71, v72, v73
	v_cvt_pk_bf16_f32 v72, v66, v67
	v_cvt_pk_bf16_f32 v73, v68, v69
	global_store_dwordx4 v[82:83], v[70:73], off offset:256
	v_cvt_pk_bf16_f32 v62, v62, v63
	v_cvt_pk_bf16_f32 v63, v64, v65
	v_cvt_pk_bf16_f32 v64, v58, v59
	v_add_co_u32_e32 v58, vcc, s48, v146
	v_lshl_add_u64 v[66:67], v[146:147], 0, s[0:1]
	s_nop 0
	v_addc_co_u32_e32 v59, vcc, 0, v147, vcc
	v_cvt_pk_bf16_f32 v65, v60, v61
	global_store_dwordx4 v[58:59], v[62:65], off
	v_cvt_pk_bf16_f32 v50, v50, v51
	v_cvt_pk_bf16_f32 v51, v52, v53
	v_cvt_pk_bf16_f32 v52, v42, v43
	v_cvt_pk_bf16_f32 v53, v44, v45
	global_store_dwordx4 v[66:67], v[50:53], off offset:256
	v_cvt_pk_bf16_f32 v42, v54, v55
	v_cvt_pk_bf16_f32 v43, v56, v57
	v_cvt_pk_bf16_f32 v44, v46, v47
	v_add_co_u32_e32 v46, vcc, s49, v146
	s_nop 0
	v_lshl_add_u64 v[50:51], v[146:147], 0, s[14:15]
	v_addc_co_u32_e32 v47, vcc, 0, v147, vcc
	v_cvt_pk_bf16_f32 v45, v48, v49
	global_store_dwordx4 v[46:47], v[42:45], off
	v_cvt_pk_bf16_f32 v34, v34, v35
	v_cvt_pk_bf16_f32 v35, v36, v37
	v_cvt_pk_bf16_f32 v36, v26, v27
	v_cvt_pk_bf16_f32 v37, v28, v29
	global_store_dwordx4 v[50:51], v[34:37], off offset:256
	v_cvt_pk_bf16_f32 v26, v38, v39
	v_cvt_pk_bf16_f32 v27, v40, v41
	v_cvt_pk_bf16_f32 v28, v30, v31
	v_add_co_u32_e32 v30, vcc, s50, v146
	s_nop 0
	v_lshl_add_u64 v[34:35], v[146:147], 0, s[16:17]
	v_addc_co_u32_e32 v31, vcc, 0, v147, vcc
	v_cvt_pk_bf16_f32 v29, v32, v33
	global_store_dwordx4 v[30:31], v[26:29], off
	v_cvt_pk_bf16_f32 v18, v18, v19
	v_cvt_pk_bf16_f32 v19, v20, v21
	v_cvt_pk_bf16_f32 v20, v10, v11
	v_cvt_pk_bf16_f32 v21, v12, v13
	global_store_dwordx4 v[34:35], v[18:21], off offset:256
	v_cvt_pk_bf16_f32 v10, v22, v23
	v_cvt_pk_bf16_f32 v11, v24, v25
	v_cvt_pk_bf16_f32 v12, v14, v15
	v_add_co_u32_e32 v14, vcc, s51, v146
	s_nop 0
	v_lshl_add_u64 v[18:19], v[146:147], 0, s[18:19]
	v_addc_co_u32_e32 v15, vcc, 0, v147, vcc
	s_andn2_b64 vcc, exec, s[8:9]
	s_mov_b64 s[8:9], -1
	v_cvt_pk_bf16_f32 v13, v16, v17
	global_store_dwordx4 v[14:15], v[10:13], off
	v_cvt_pk_bf16_f32 v6, v6, v7
	v_cvt_pk_bf16_f32 v7, v8, v9
	v_cvt_pk_bf16_f32 v8, v2, v3
	v_cvt_pk_bf16_f32 v9, v4, v5
	s_mov_b32 s98, 1
	global_store_dwordx4 v[18:19], v[6:9], off offset:256
	s_cbranch_vccnz .LBB0_1003
	s_andn2_b64 vcc, exec, s[2:3]
	s_cbranch_vccnz .LBB0_1002
	s_barrier
	s_branch .LBB0_1002

;     __device__ __forceinline__ bool next(int i, pg8::Unit& u) const { const int s = i >= R ? 1 : 0; const bool ok = so.next(i - s * R, u); u.sel = s; return ok && i < 2 * R; }
; template <class Epi, class Sched>
; __device__ __forceinline__ void gemm_phase_gather(PG8_LAS unsigned char* lds, const Gemm g, const int* __restrict__ gidx, PG8_LAS int* itab  , const Sched& S, const Epi& E) {
;     ...
;     { int vals[4];
; #pragma unroll
;       for (int k = 0; k < 4; ++k) { const int e = tid + 512 * k; Unit uu; const bool ok = S.next(e >> 8, uu); vals[k] = ok ? gidx[uu.pm * BM + (e & 255)] : 0; }
; #pragma unroll
;       for (int k = 0; k < 4; ++k) itab[tid + 512 * k] = vals[k];
;       asm volatile("s_waitcnt vmcnt(0) lgkmcnt(0)" ::: "memory"); __builtin_amdgcn_s_barrier(); asm volatile("" ::: "memory"); }
;     __device__ __forceinline__ bool next(int i, pg8::Unit& u) const {
;         constexpr int NWG = NE * 8 * NJ, Q = NWG / 8;
;         const int L = i * G + c; if (L >= NWG) return false;
;         const int wgid = (L % 8) * Q + L / 8;
;         const int e = wgid / (8 * NJ), w = wgid % (8 * NJ), rt = w % 8, j = w / 8, b = rt >> 1, half = rt & 1;
;         u.pm = (b * NE + e) * 2 + half; u.pn = e * NJ + j; return true;
;     }
.LBB0_1258:
	s_mov_b32 s98, 0
	s_cmp_lt_i32 s78, 11
	s_cselect_b64 s[0:1], -1, 0
	s_cmp_gt_i32 s79, 10
	s_cselect_b64 s[2:3], -1, 0
	s_and_b64 s[0:1], s[0:1], s[2:3]
	s_andn2_b64 vcc, exec, s[0:1]
	s_cbranch_vccnz .LBB0_1339
	s_mov_b64 s[0:1], s[74:75]
	s_load_dwordx2 s[0:1], s[0:1], 0xd8
	v_lshrrev_b32_e32 v2, 8, v0
	v_mul_lo_u32 v2, s86, v2
	v_add_u32_e32 v4, s88, v2
	s_movk_i32 s7, 0x800
	s_waitcnt lgkmcnt(0)
	s_add_u32 s2, s0, 0x400000
	v_readfirstlane_b32 s6, v0
	v_and_b32_e32 v1, 0xff, v0
	s_addc_u32 s3, s1, 0
	v_cmp_gt_i32_e32 vcc, s7, v4
	v_mov_b32_e32 v2, 0
	v_mov_b32_e32 v3, 0
	s_and_saveexec_b64 s[4:5], vcc
	s_cbranch_execz .LBB0_1261
	v_ashrrev_i32_e32 v3, 31, v4
	v_lshrrev_b32_e32 v3, 29, v3
	v_add_u32_e32 v3, v4, v3
	v_ashrrev_i32_e32 v5, 3, v3
	v_and_b32_e32 v3, 0xfffff8, v3
	v_sub_u32_e32 v3, v4, v3
	v_lshl_add_u32 v3, v3, 8, v5
	v_ashrrev_i32_e32 v5, 31, v3
	v_lshrrev_b32_e32 v5, 25, v5
	v_add_u32_e32 v5, v3, v5
	v_lshrrev_b32_e32 v6, 7, v5
	v_and_b32_e32 v5, 0xff80, v5
	v_sub_u32_e32 v3, v3, v5
	v_mov_b32_e32 v5, 12
	v_lshrrev_b16_sdwa v5, v5, sext(v3) dst_sel:DWORD dst_unused:UNUSED_PAD src0_sel:DWORD src1_sel:BYTE_0
	v_and_b32_e32 v5, 7, v5
	v_add_u16_e32 v5, v3, v5
	v_and_b32_e32 v5, 0xf8, v5
	v_sub_u16_e32 v3, v3, v5
	v_mov_b32_e32 v5, 3
	v_lshlrev_b32_sdwa v5, v5, sext(v3) dst_sel:DWORD dst_unused:UNUSED_PAD src0_sel:DWORD src1_sel:BYTE_0
	v_and_b32_e32 v5, 0x7ffff0, v5
	v_lshlrev_b32_e32 v3, 8, v3
	v_add_lshl_u32 v5, v5, v6, 9
	v_and_b32_e32 v3, 0x100, v3
	v_or3_b32 v6, v5, v3, v1
	v_ashrrev_i32_e32 v7, 31, v6
	v_lshl_add_u64 v[6:7], v[6:7], 2, s[2:3]
	global_load_dword v3, v[6:7], off

; #define PG8_GOFF(dst, ord) do { _Pragma("unroll") for (int _h = 0; _h < 2; ++_h) _Pragma("unroll") for (int _i = 0; _i < 2; ++_i) \
;         dst[_h][_i] = ((unsigned)itab[(ord) * BM + _h * HALF + RA[_i]] * (unsigned)K + (unsigned)CA[_i]) * 2u; } while (0)
;     __device__ __forceinline__ bool next(int i, pg8::Unit& u) const { const int s = i >= R ? 1 : 0; const bool ok = so.next(i - s * R, u); u.sel = s; return ok && i < 2 * R; }
; template <class Epi, class Sched>
; __device__ __forceinline__ void gemm_phase_gather(PG8_LAS unsigned char* lds, const Gemm g, const int* __restrict__ gidx, PG8_LAS int* itab  , const Sched& S, const Epi& E) {
;     ...
;     for (;;) {
;         const bool has_next = S.next(ui + 1, nxt);
;         if (has_next) { PG8_GOFF(nvo, ui + 1); } else {
; #pragma unroll
;             for (int _h = 0; _h < 2; ++_h)
; #pragma unroll
;                 for (int _i = 0; _i < 2; ++_i) nvo[_h][_i] = cvo[_h][_i]; }
;         const char* nB = has_next ? (const char*)g.Bt + (size_t)nxt.pn * tstep : cB;
;     ...
; #pragma unroll
;         for (int a = 0; a < 2; ++a)
; #pragma unroll
;             for (int b = 0; b < 2; ++b)
; #pragma unroll
;                 for (int m = 0; m < 4; ++m)
; #pragma unroll
;                     for (int n = 0; n < 2; ++n) acc[a][b][m][n] = (f32x4){0.f, 0.f, 0.f, 0.f};
;         cur = nxt; cB = nB; ++ui;
; #pragma unroll
;         for (int _h = 0; _h < 2; ++_h)
; #pragma unroll
;             for (int _i = 0; _i < 2; ++_i) cvo[_h][_i] = nvo[_h][_i];
.LBB0_1277:
	s_ashr_i32 s17, s16, 31
	s_lshl_b64 s[18:19], s[16:17], 20
	s_add_u32 s18, s29, s18
	s_addc_u32 s19, s30, s19
	s_and_b64 s[24:25], s[24:25], exec
	s_cselect_b32 s17, s19, s23
	s_cselect_b32 s46, s18, s22
	v_mov_b32_e32 v139, v135
	v_mov_b32_e32 v137, v135
	s_add_u32 s47, s22, 0x100
	v_mov_b32_e32 v26, 0
	v_lshl_add_u64 v[142:143], s[12:13], 0, v[136:137]
	v_lshl_add_u64 v[144:145], s[12:13], 0, v[138:139]
	s_addc_u32 s48, s23, 0
	s_mov_b32 s49, -2
	s_mov_b64 s[22:23], 0
	v_mov_b32_e32 v27, v26
	v_mov_b32_e32 v28, v26
	v_mov_b32_e32 v29, v26
	v_mov_b32_e32 v30, v26
	v_mov_b32_e32 v31, v26
	v_mov_b32_e32 v32, v26
	v_mov_b32_e32 v33, v26
	v_mov_b32_e32 v50, v26
	v_mov_b32_e32 v51, v26
	v_mov_b32_e32 v52, v26
	v_mov_b32_e32 v53, v26
	v_mov_b32_e32 v54, v26
	v_mov_b32_e32 v55, v26
	v_mov_b32_e32 v56, v26
	v_mov_b32_e32 v57, v26
	v_mov_b32_e32 v2, v26
	v_mov_b32_e32 v3, v26
	v_mov_b32_e32 v4, v26
	v_mov_b32_e32 v5, v26
	v_mov_b32_e32 v6, v26
	v_mov_b32_e32 v7, v26
	v_mov_b32_e32 v8, v26
	v_mov_b32_e32 v9, v26
	v_mov_b32_e32 v10, v26
	v_mov_b32_e32 v11, v26
	v_mov_b32_e32 v12, v26
	v_mov_b32_e32 v13, v26
	v_mov_b32_e32 v14, v26
	v_mov_b32_e32 v15, v26
	v_mov_b32_e32 v16, v26
	v_mov_b32_e32 v17, v26
	v_mov_b32_e32 v38, v26
	v_mov_b32_e32 v39, v26
	v_mov_b32_e32 v40, v26
	v_mov_b32_e32 v41, v26
	v_mov_b32_e32 v46, v26
	v_mov_b32_e32 v47, v26
	v_mov_b32_e32 v48, v26
	v_mov_b32_e32 v49, v26
	v_mov_b32_e32 v58, v26
	v_mov_b32_e32 v59, v26
	v_mov_b32_e32 v60, v26
	v_mov_b32_e32 v61, v26
	v_mov_b32_e32 v62, v26
	v_mov_b32_e32 v63, v26
	v_mov_b32_e32 v64, v26
	v_mov_b32_e32 v65, v26
	v_mov_b32_e32 v66, v26
	v_mov_b32_e32 v67, v26
	v_mov_b32_e32 v68, v26
	v_mov_b32_e32 v69, v26
	v_mov_b32_e32 v70, v26
	v_mov_b32_e32 v71, v26
	v_mov_b32_e32 v72, v26
	v_mov_b32_e32 v73, v26
	v_mov_b32_e32 v82, v26
	v_mov_b32_e32 v83, v26
	v_mov_b32_e32 v84, v26
	v_mov_b32_e32 v85, v26
	v_mov_b32_e32 v86, v26
	v_mov_b32_e32 v87, v26
	v_mov_b32_e32 v88, v26
	v_mov_b32_e32 v89, v26
	v_mov_b32_e32 v98, v26
	v_mov_b32_e32 v99, v26
	v_mov_b32_e32 v100, v26
	v_mov_b32_e32 v101, v26
	v_mov_b32_e32 v102, v26
	v_mov_b32_e32 v103, v26
	v_mov_b32_e32 v104, v26
	v_mov_b32_e32 v105, v26
	v_mov_b32_e32 v114, v26
	v_mov_b32_e32 v115, v26
	v_mov_b32_e32 v116, v26
	v_mov_b32_e32 v117, v26
	v_mov_b32_e32 v118, v26
	v_mov_b32_e32 v119, v26
	v_mov_b32_e32 v120, v26
	v_mov_b32_e32 v121, v26
	v_mov_b32_e32 v74, v26
	v_mov_b32_e32 v75, v26
	v_mov_b32_e32 v76, v26
	v_mov_b32_e32 v77, v26
	v_mov_b32_e32 v78, v26
	v_mov_b32_e32 v79, v26
	v_mov_b32_e32 v80, v26
	v_mov_b32_e32 v81, v26
	v_mov_b32_e32 v90, v26
	v_mov_b32_e32 v91, v26
	v_mov_b32_e32 v92, v26
	v_mov_b32_e32 v93, v26
	v_mov_b32_e32 v94, v26
	v_mov_b32_e32 v95, v26
	v_mov_b32_e32 v96, v26
	v_mov_b32_e32 v97, v26
	v_mov_b32_e32 v106, v26
	v_mov_b32_e32 v107, v26
	v_mov_b32_e32 v108, v26
	v_mov_b32_e32 v109, v26
	v_mov_b32_e32 v110, v26
	v_mov_b32_e32 v111, v26
	v_mov_b32_e32 v112, v26
	v_mov_b32_e32 v113, v26
	v_mov_b32_e32 v122, v26
	v_mov_b32_e32 v123, v26
	v_mov_b32_e32 v124, v26
	v_mov_b32_e32 v125, v26
	v_mov_b32_e32 v126, v26
	v_mov_b32_e32 v127, v26
	v_mov_b32_e32 v128, v26
	v_mov_b32_e32 v129, v26
	v_mov_b32_e32 v42, v26
	v_mov_b32_e32 v43, v26
	v_mov_b32_e32 v44, v26
	v_mov_b32_e32 v45, v26
	v_mov_b32_e32 v34, v26
	v_mov_b32_e32 v35, v26
	v_mov_b32_e32 v36, v26
	v_mov_b32_e32 v37, v26
	v_mov_b32_e32 v22, v26
	v_mov_b32_e32 v23, v26
	v_mov_b32_e32 v24, v26
	v_mov_b32_e32 v25, v26
	v_mov_b32_e32 v18, v26
	v_mov_b32_e32 v19, v26
	v_mov_b32_e32 v20, v26
	v_mov_b32_e32 v21, v26
	s_cmp_lg_u32 s98, 0
	s_cselect_b32 s99, -2, 0x7ffffff0
	s_branch .LBB0_1278
.Lrx10_a:
	s_waitcnt vmcnt(16)
	s_branch .Lrx10_a_done

; #define PG8_STAGE(bufoff, gbase, voff) do { _Pragma("unroll") for (int _i = 0; _i < 2; ++_i) \
;         __builtin_amdgcn_global_load_lds((const unsigned*)((const char*)(gbase) + (voff)[_i]), (PG8_LAS unsigned*)(lds + (bufoff) + ldsw + _i * 8192), 16, 0, 0); } while (0)
; #define PG8_LDA(dst, b, h) do { _Pragma("unroll") for (int m = 0; m < 4; ++m) _Pragma("unroll") for (int k = 0; k < 2; ++k) dst[m][k] = *(const PG8_LAS bf16x8*)(lds + PG8_SA(b, h) + aoff + m * 2048 + k * 1024); } while (0)
; #define PG8_LDB(dst, b, h) do { _Pragma("unroll") for (int n = 0; n < 2; ++n) _Pragma("unroll") for (int k = 0; k < 2; ++k) dst[n][k] = *(const PG8_LAS bf16x8*)(lds + PG8_SB(b, h) + boff + n * 2048 + k * 1024); } while (0)
; #define PG8_MMA(ai, bj, At, Bt) do { __builtin_amdgcn_s_setprio(1); _Pragma("unroll") for (int m = 0; m < 4; ++m) _Pragma("unroll") for (int n = 0; n < 2; ++n) _Pragma("unroll") for (int k = 0; k < 2; ++k) \
;         acc[ai][bj][m][n] = __builtin_amdgcn_mfma_f32_16x16x32_bf16(Bt[n][k], At[m][k], acc[ai][bj][m][n], 0, 0, 0); __builtin_amdgcn_s_setprio(0); } while (0)
; #define PG8_WAIT_V(n) asm volatile("s_waitcnt vmcnt(" #n ")" ::: "memory")
; #define PG8_WAIT_L(n) asm volatile("s_waitcnt lgkmcnt(" #n ")" ::: "memory")
; #define PG8_BAR __builtin_amdgcn_s_barrier()
; #define PG8_SCHED __builtin_amdgcn_sched_barrier(0)
; #define PG8_STAGE(bufoff, gbase, voff) do { _Pragma("unroll") for (int _i = 0; _i < 2; ++_i) \
;         __builtin_amdgcn_global_load_lds((const unsigned*)((const char*)(gbase) + (voff)[_i]), (PG8_LAS unsigned*)(lds + (bufoff) + ldsw + _i * 8192), 16, 0, 0); } while (0)
; #define PG8_BAR __builtin_amdgcn_s_barrier()
; template <class Epi, class Sched>
; __device__ __forceinline__ void gemm_phase_gather(PG8_LAS unsigned char* lds, const Gemm g, const int* __restrict__ gidx, PG8_LAS int* itab  , const Sched& S, const Epi& E) {
;     ...
;             PG8_LDB(B0, 0, 0); PG8_LDB(B1, 0, 1); PG8_SCHED; PG8_LDA(At, 0, 0); PG8_STAGE(PG8_SA(1, 1), a1, cvo[1]);
;             PG8_WAIT_V(8); PG8_WAIT_L(0); PG8_BAR; PG8_MMA(0, 0, At, B0); PG8_MMA(0, 1, At, B1); PG8_BAR; PG8_SCHED;
;             PG8_LDA(At, 0, 1); PG8_STAGE(PG8_SB(0, 0), b2, voffB); PG8_STAGE(PG8_SB(0, 1), b2 + hstep, voffB); PG8_STAGE(PG8_SA(0, 0), a2, vo2[0]);
;             PG8_WAIT_V(8); PG8_WAIT_L(0); PG8_BAR; PG8_MMA(1, 0, At, B0); PG8_MMA(1, 1, At, B1); PG8_BAR; PG8_SCHED;
.LBB0_1278:
	ds_read_b128 v[158:161], v150
	ds_read_b128 v[162:165], v150 offset:1024
	ds_read_b128 v[166:169], v150 offset:2048
	ds_read_b128 v[170:173], v150 offset:3072
	ds_read_b128 v[174:177], v151
	ds_read_b128 v[178:181], v151 offset:1024
	ds_read_b128 v[182:185], v151 offset:2048
	ds_read_b128 v[188:191], v151 offset:3072
	s_add_u32 s24, s0, s22
	s_addc_u32 s25, s1, s23
	s_add_u32 s26, s24, 0xe800100
	s_addc_u32 s27, s25, 0
	s_add_u32 s50, s47, s22
	s_addc_u32 s51, s48, s23
	s_cmpk_eq_i32 s22, 0xf00
	s_cselect_b64 vcc, -1, 0
	s_and_b64 s[24:25], vcc, exec
	v_cndmask_b32_e32 v134, v157, v153, vcc
	s_cselect_b32 s27, s3, s27
	s_cselect_b32 s26, s2, s26
	v_cndmask_b32_e32 v224, v140, v154, vcc
	v_cndmask_b32_e32 v137, v138, v155, vcc
	v_cndmask_b32_e32 v139, v136, v156, vcc
	s_cselect_b32 s25, s17, s51
	s_cselect_b32 s24, s46, s50
	s_mov_b32 m0, s43
	v_lshl_add_u64 v[226:227], v[144:145], 0, s[22:23]
	ds_read_b128 v[192:195], v152
	ds_read_b128 v[196:199], v152 offset:1024
	ds_read_b128 v[200:203], v152 offset:2048
	ds_read_b128 v[204:207], v152 offset:3072
	ds_read_b128 v[208:211], v152 offset:4096
	ds_read_b128 v[212:215], v152 offset:5120
	ds_read_b128 v[216:219], v152 offset:6144
	ds_read_b128 v[220:223], v152 offset:7168
	global_load_lds_dwordx4 v[226:227], off
	v_lshl_add_u64 v[226:227], v[142:143], 0, s[22:23]
	s_add_i32 m0, s21, 0xe000
	s_nop 0
	global_load_lds_dwordx4 v[226:227], off
	s_cmp_eq_u32 s49, s99
	s_cbranch_scc1 .Lrx10_a
	s_waitcnt vmcnt(8)
.Lrx10_a_done:
	s_waitcnt lgkmcnt(0)
	s_barrier
	s_setprio 1
	s_waitcnt lgkmcnt(0)
	v_mfma_f32_16x16x32_bf16 v[126:129], v[158:161], v[192:195], v[126:129]
	v_mfma_f32_16x16x32_bf16 v[122:125], v[166:169], v[192:195], v[122:125]
	v_mfma_f32_16x16x32_bf16 v[110:113], v[158:161], v[200:203], v[110:113]
	v_mfma_f32_16x16x32_bf16 v[106:109], v[166:169], v[200:203], v[106:109]
	v_mfma_f32_16x16x32_bf16 v[94:97], v[158:161], v[208:211], v[94:97]
	v_mfma_f32_16x16x32_bf16 v[90:93], v[166:169], v[208:211], v[90:93]
	v_mfma_f32_16x16x32_bf16 v[78:81], v[158:161], v[216:219], v[78:81]
	v_mfma_f32_16x16x32_bf16 v[74:77], v[166:169], v[216:219], v[74:77]
	v_mfma_f32_16x16x32_bf16 v[126:129], v[162:165], v[196:199], v[126:129]
	v_mfma_f32_16x16x32_bf16 v[122:125], v[170:173], v[196:199], v[122:125]
	v_mfma_f32_16x16x32_bf16 v[110:113], v[162:165], v[204:207], v[110:113]
	v_mfma_f32_16x16x32_bf16 v[106:109], v[170:173], v[204:207], v[106:109]
	v_mfma_f32_16x16x32_bf16 v[94:97], v[162:165], v[212:215], v[94:97]
	v_mfma_f32_16x16x32_bf16 v[90:93], v[170:173], v[212:215], v[90:93]
	v_mfma_f32_16x16x32_bf16 v[78:81], v[162:165], v[220:223], v[78:81]
	v_mfma_f32_16x16x32_bf16 v[74:77], v[170:173], v[220:223], v[74:77]
	s_setprio 0
	s_setprio 1
	v_mfma_f32_16x16x32_bf16 v[118:121], v[174:177], v[192:195], v[118:121]
	v_mfma_f32_16x16x32_bf16 v[114:117], v[182:185], v[192:195], v[114:117]
	v_mfma_f32_16x16x32_bf16 v[102:105], v[174:177], v[200:203], v[102:105]
	v_mfma_f32_16x16x32_bf16 v[98:101], v[182:185], v[200:203], v[98:101]
	v_mfma_f32_16x16x32_bf16 v[86:89], v[174:177], v[208:211], v[86:89]
	v_mfma_f32_16x16x32_bf16 v[82:85], v[182:185], v[208:211], v[82:85]
	v_mfma_f32_16x16x32_bf16 v[70:73], v[174:177], v[216:219], v[70:73]
	v_mfma_f32_16x16x32_bf16 v[66:69], v[182:185], v[216:219], v[66:69]
	v_mfma_f32_16x16x32_bf16 v[118:121], v[178:181], v[196:199], v[118:121]
	v_mfma_f32_16x16x32_bf16 v[114:117], v[188:191], v[196:199], v[114:117]
	v_mfma_f32_16x16x32_bf16 v[102:105], v[178:181], v[204:207], v[102:105]
	v_mfma_f32_16x16x32_bf16 v[98:101], v[188:191], v[204:207], v[98:101]
	v_mfma_f32_16x16x32_bf16 v[86:89], v[178:181], v[212:215], v[86:89]
	v_mfma_f32_16x16x32_bf16 v[82:85], v[188:191], v[212:215], v[82:85]
	v_mfma_f32_16x16x32_bf16 v[70:73], v[178:181], v[220:223], v[70:73]
	v_mfma_f32_16x16x32_bf16 v[66:69], v[188:191], v[220:223], v[66:69]
	s_setprio 0
	s_barrier
	s_add_i32 s50, s38, s28
	v_lshl_add_u64 v[226:227], s[24:25], 0, v[130:131]
	s_mov_b32 m0, s50
	ds_read_b128 v[192:195], v152 offset:16384
	ds_read_b128 v[196:199], v152 offset:17408
	ds_read_b128 v[200:203], v152 offset:18432
	ds_read_b128 v[204:207], v152 offset:19456
	ds_read_b128 v[208:211], v152 offset:20480
	ds_read_b128 v[212:215], v152 offset:21504
	ds_read_b128 v[216:219], v152 offset:22528
	ds_read_b128 v[220:223], v152 offset:23552
	global_load_lds_dwordx4 v[226:227], off
	s_add_i32 m0, s50, 0x2000
	s_add_u32 s50, s24, 0x80000
	v_lshl_add_u64 v[228:229], s[24:25], 0, v[132:133]
	s_addc_u32 s51, s25, 0
	s_add_i32 s52, s39, s28
	global_load_lds_dwordx4 v[228:229], off
	v_lshl_add_u64 v[230:231], s[50:51], 0, v[130:131]
	s_mov_b32 m0, s52
	v_mov_b32_e32 v225, v135
	global_load_lds_dwordx4 v[230:231], off
	v_lshl_add_u64 v[230:231], s[50:51], 0, v[132:133]
	s_add_i32 m0, s52, 0x2000
	s_nop 0
	global_load_lds_dwordx4 v[230:231], off
	s_mov_b32 m0, s21
	v_lshl_add_u64 v[230:231], s[26:27], 0, v[134:135]
	global_load_lds_dwordx4 v134, s[26:27]
	s_mov_b32 m0, s31
	s_nop 0
	global_load_lds_dwordx4 v224, s[26:27]
	s_cmp_eq_u32 s49, s99
	s_cbranch_scc1 .Lrx10_b
	s_waitcnt vmcnt(8)
; #define PG8_STAGE(bufoff, gbase, voff) do { _Pragma("unroll") for (int _i = 0; _i < 2; ++_i) \
;         __builtin_amdgcn_global_load_lds((const unsigned*)((const char*)(gbase) + (voff)[_i]), (PG8_LAS unsigned*)(lds + (bufoff) + ldsw + _i * 8192), 16, 0, 0); } while (0)
; #define PG8_LDA(dst, b, h) do { _Pragma("unroll") for (int m = 0; m < 4; ++m) _Pragma("unroll") for (int k = 0; k < 2; ++k) dst[m][k] = *(const PG8_LAS bf16x8*)(lds + PG8_SA(b, h) + aoff + m * 2048 + k * 1024); } while (0)
; #define PG8_LDB(dst, b, h) do { _Pragma("unroll") for (int n = 0; n < 2; ++n) _Pragma("unroll") for (int k = 0; k < 2; ++k) dst[n][k] = *(const PG8_LAS bf16x8*)(lds + PG8_SB(b, h) + boff + n * 2048 + k * 1024); } while (0)
; #define PG8_MMA(ai, bj, At, Bt) do { __builtin_amdgcn_s_setprio(1); _Pragma("unroll") for (int m = 0; m < 4; ++m) _Pragma("unroll") for (int n = 0; n < 2; ++n) _Pragma("unroll") for (int k = 0; k < 2; ++k) \
;         acc[ai][bj][m][n] = __builtin_amdgcn_mfma_f32_16x16x32_bf16(Bt[n][k], At[m][k], acc[ai][bj][m][n], 0, 0, 0); __builtin_amdgcn_s_setprio(0); } while (0)
; #define PG8_WAIT_V(n) asm volatile("s_waitcnt vmcnt(" #n ")" ::: "memory")
; #define PG8_WAIT_L(n) asm volatile("s_waitcnt lgkmcnt(" #n ")" ::: "memory")
; #define PG8_BAR __builtin_amdgcn_s_barrier()
; #define PG8_SCHED __builtin_amdgcn_sched_barrier(0)
; #define PG8_STAGE(bufoff, gbase, voff) do { _Pragma("unroll") for (int _i = 0; _i < 2; ++_i) \
;         __builtin_amdgcn_global_load_lds((const unsigned*)((const char*)(gbase) + (voff)[_i]), (PG8_LAS unsigned*)(lds + (bufoff) + ldsw + _i * 8192), 16, 0, 0); } while (0)
; #define PG8_WAIT_V(n) asm volatile("s_waitcnt vmcnt(" #n ")" ::: "memory")
; #define PG8_WAIT_L(n) asm volatile("s_waitcnt lgkmcnt(" #n ")" ::: "memory")
; #define PG8_BAR __builtin_amdgcn_s_barrier()
; template <class Epi, class Sched>
; __device__ __forceinline__ void gemm_phase_gather(PG8_LAS unsigned char* lds, const Gemm g, const int* __restrict__ gidx, PG8_LAS int* itab  , const Sched& S, const Epi& E) {
;     ...
;             PG8_WAIT_V(8); PG8_WAIT_L(0); PG8_BAR; PG8_MMA(1, 0, At, B0); PG8_MMA(1, 1, At, B1); PG8_BAR; PG8_SCHED;
;             PG8_LDB(B0, 1, 0); PG8_LDB(B1, 1, 1); PG8_SCHED; PG8_LDA(At, 1, 0); PG8_STAGE(PG8_SA(0, 1), a2, vo2[1]);
;             PG8_WAIT_V(8); PG8_WAIT_L(0); PG8_BAR; PG8_MMA(0, 0, At, B0); PG8_MMA(0, 1, At, B1); PG8_BAR; PG8_SCHED;
.Lrx10_b_done:
	s_waitcnt lgkmcnt(0)
	v_lshl_add_u64 v[224:225], s[26:27], 0, v[224:225]
	s_barrier
	s_setprio 1
	s_waitcnt lgkmcnt(0)
	v_mfma_f32_16x16x32_bf16 v[62:65], v[158:161], v[192:195], v[62:65]
	v_mfma_f32_16x16x32_bf16 v[58:61], v[166:169], v[192:195], v[58:61]
	v_mfma_f32_16x16x32_bf16 v[46:49], v[158:161], v[200:203], v[46:49]
	v_mfma_f32_16x16x32_bf16 v[38:41], v[166:169], v[200:203], v[38:41]
	v_mfma_f32_16x16x32_bf16 v[14:17], v[158:161], v[208:211], v[14:17]
	v_mfma_f32_16x16x32_bf16 v[10:13], v[166:169], v[208:211], v[10:13]
	v_mfma_f32_16x16x32_bf16 v[6:9], v[158:161], v[216:219], v[6:9]
	v_mfma_f32_16x16x32_bf16 v[2:5], v[166:169], v[216:219], v[2:5]
	v_mfma_f32_16x16x32_bf16 v[62:65], v[162:165], v[196:199], v[62:65]
	v_mfma_f32_16x16x32_bf16 v[58:61], v[170:173], v[196:199], v[58:61]
	v_mfma_f32_16x16x32_bf16 v[46:49], v[162:165], v[204:207], v[46:49]
	v_mfma_f32_16x16x32_bf16 v[38:41], v[170:173], v[204:207], v[38:41]
	v_mfma_f32_16x16x32_bf16 v[14:17], v[162:165], v[212:215], v[14:17]
	v_mfma_f32_16x16x32_bf16 v[10:13], v[170:173], v[212:215], v[10:13]
	v_mfma_f32_16x16x32_bf16 v[6:9], v[162:165], v[220:223], v[6:9]
	v_mfma_f32_16x16x32_bf16 v[2:5], v[170:173], v[220:223], v[2:5]
	s_setprio 0
	s_setprio 1
	v_mfma_f32_16x16x32_bf16 v[54:57], v[174:177], v[192:195], v[54:57]
	v_mfma_f32_16x16x32_bf16 v[50:53], v[182:185], v[192:195], v[50:53]
	v_mfma_f32_16x16x32_bf16 v[30:33], v[174:177], v[200:203], v[30:33]
	v_mfma_f32_16x16x32_bf16 v[26:29], v[182:185], v[200:203], v[26:29]
	v_mfma_f32_16x16x32_bf16 v[42:45], v[174:177], v[208:211], v[42:45]
	v_mfma_f32_16x16x32_bf16 v[34:37], v[182:185], v[208:211], v[34:37]
	v_mfma_f32_16x16x32_bf16 v[22:25], v[174:177], v[216:219], v[22:25]
	v_mfma_f32_16x16x32_bf16 v[18:21], v[182:185], v[216:219], v[18:21]
	v_mfma_f32_16x16x32_bf16 v[54:57], v[178:181], v[196:199], v[54:57]
	v_mfma_f32_16x16x32_bf16 v[50:53], v[188:191], v[196:199], v[50:53]
	v_mfma_f32_16x16x32_bf16 v[30:33], v[178:181], v[204:207], v[30:33]
	v_mfma_f32_16x16x32_bf16 v[26:29], v[188:191], v[204:207], v[26:29]
	v_mfma_f32_16x16x32_bf16 v[42:45], v[178:181], v[212:215], v[42:45]
	v_mfma_f32_16x16x32_bf16 v[34:37], v[188:191], v[212:215], v[34:37]
	v_mfma_f32_16x16x32_bf16 v[22:25], v[178:181], v[220:223], v[22:25]
	v_mfma_f32_16x16x32_bf16 v[18:21], v[188:191], v[220:223], v[18:21]
	s_setprio 0
	s_barrier
	s_add_i32 s50, 0, 0x18000
	v_add_u32_e32 v134, s50, v148
	s_add_i32 s51, 0, 0x1c000
	ds_read_b128 v[158:161], v134
	ds_read_b128 v[162:165], v134 offset:1024
	ds_read_b128 v[166:169], v134 offset:2048
	ds_read_b128 v[170:173], v134 offset:3072
	v_add_u32_e32 v134, s51, v148
	ds_read_b128 v[174:177], v134
	ds_read_b128 v[178:181], v134 offset:1024
	ds_read_b128 v[182:185], v134 offset:2048
	ds_read_b128 v[188:191], v134 offset:3072
	s_mov_b32 m0, s33
	ds_read_b128 v[192:195], v152 offset:32768
	ds_read_b128 v[196:199], v152 offset:33792
	ds_read_b128 v[200:203], v152 offset:34816
	ds_read_b128 v[204:207], v152 offset:35840
	ds_read_b128 v[208:211], v152 offset:36864
	ds_read_b128 v[212:215], v152 offset:37888
	ds_read_b128 v[216:219], v152 offset:38912
	ds_read_b128 v[220:223], v152 offset:39936
	global_load_lds_dwordx4 v137, s[26:27]
	s_mov_b32 m0, s34
	s_nop 0
	global_load_lds_dwordx4 v139, s[26:27]
	s_waitcnt vmcnt(8)
	s_waitcnt lgkmcnt(0)
	s_barrier
	s_setprio 1
	s_waitcnt lgkmcnt(0)
	v_mfma_f32_16x16x32_bf16 v[126:129], v[158:161], v[192:195], v[126:129]
	v_mfma_f32_16x16x32_bf16 v[122:125], v[166:169], v[192:195], v[122:125]
	v_mfma_f32_16x16x32_bf16 v[110:113], v[158:161], v[200:203], v[110:113]
	v_mfma_f32_16x16x32_bf16 v[106:109], v[166:169], v[200:203], v[106:109]
	v_mfma_f32_16x16x32_bf16 v[94:97], v[158:161], v[208:211], v[94:97]
	v_mfma_f32_16x16x32_bf16 v[90:93], v[166:169], v[208:211], v[90:93]
	v_mfma_f32_16x16x32_bf16 v[78:81], v[158:161], v[216:219], v[78:81]
	v_mfma_f32_16x16x32_bf16 v[74:77], v[166:169], v[216:219], v[74:77]
	v_mfma_f32_16x16x32_bf16 v[126:129], v[162:165], v[196:199], v[126:129]
	v_mfma_f32_16x16x32_bf16 v[122:125], v[170:173], v[196:199], v[122:125]
	v_mfma_f32_16x16x32_bf16 v[110:113], v[162:165], v[204:207], v[110:113]
	v_mfma_f32_16x16x32_bf16 v[106:109], v[170:173], v[204:207], v[106:109]
	v_mfma_f32_16x16x32_bf16 v[94:97], v[162:165], v[212:215], v[94:97]
	v_mfma_f32_16x16x32_bf16 v[90:93], v[170:173], v[212:215], v[90:93]
	v_mfma_f32_16x16x32_bf16 v[78:81], v[162:165], v[220:223], v[78:81]
	v_mfma_f32_16x16x32_bf16 v[74:77], v[170:173], v[220:223], v[74:77]
	s_setprio 0
	s_setprio 1
	v_mfma_f32_16x16x32_bf16 v[118:121], v[174:177], v[192:195], v[118:121]
	v_mfma_f32_16x16x32_bf16 v[114:117], v[182:185], v[192:195], v[114:117]
	v_mfma_f32_16x16x32_bf16 v[102:105], v[174:177], v[200:203], v[102:105]
	v_mfma_f32_16x16x32_bf16 v[98:101], v[182:185], v[200:203], v[98:101]
	v_mfma_f32_16x16x32_bf16 v[86:89], v[174:177], v[208:211], v[86:89]
	v_mfma_f32_16x16x32_bf16 v[82:85], v[182:185], v[208:211], v[82:85]
	v_mfma_f32_16x16x32_bf16 v[70:73], v[174:177], v[216:219], v[70:73]
	v_mfma_f32_16x16x32_bf16 v[66:69], v[182:185], v[216:219], v[66:69]
	v_mfma_f32_16x16x32_bf16 v[118:121], v[178:181], v[196:199], v[118:121]
	v_mfma_f32_16x16x32_bf16 v[114:117], v[188:191], v[196:199], v[114:117]
	v_mfma_f32_16x16x32_bf16 v[102:105], v[178:181], v[204:207], v[102:105]
	v_mfma_f32_16x16x32_bf16 v[98:101], v[188:191], v[204:207], v[98:101]
	v_mfma_f32_16x16x32_bf16 v[86:89], v[178:181], v[212:215], v[86:89]
	v_mfma_f32_16x16x32_bf16 v[82:85], v[188:191], v[212:215], v[82:85]
	v_mfma_f32_16x16x32_bf16 v[70:73], v[178:181], v[220:223], v[70:73]
	v_mfma_f32_16x16x32_bf16 v[66:69], v[188:191], v[220:223], v[66:69]
	s_setprio 0
	s_barrier
; #define PG8_STAGE(bufoff, gbase, voff) do { _Pragma("unroll") for (int _i = 0; _i < 2; ++_i) \
;         __builtin_amdgcn_global_load_lds((const unsigned*)((const char*)(gbase) + (voff)[_i]), (PG8_LAS unsigned*)(lds + (bufoff) + ldsw + _i * 8192), 16, 0, 0); } while (0)
; #define PG8_LDA(dst, b, h) do { _Pragma("unroll") for (int m = 0; m < 4; ++m) _Pragma("unroll") for (int k = 0; k < 2; ++k) dst[m][k] = *(const PG8_LAS bf16x8*)(lds + PG8_SA(b, h) + aoff + m * 2048 + k * 1024); } while (0)
; #define PG8_MMA(ai, bj, At, Bt) do { __builtin_amdgcn_s_setprio(1); _Pragma("unroll") for (int m = 0; m < 4; ++m) _Pragma("unroll") for (int n = 0; n < 2; ++n) _Pragma("unroll") for (int k = 0; k < 2; ++k) \
;         acc[ai][bj][m][n] = __builtin_amdgcn_mfma_f32_16x16x32_bf16(Bt[n][k], At[m][k], acc[ai][bj][m][n], 0, 0, 0); __builtin_amdgcn_s_setprio(0); } while (0)
; #define PG8_WAIT_V(n) asm volatile("s_waitcnt vmcnt(" #n ")" ::: "memory")
; #define PG8_WAIT_L(n) asm volatile("s_waitcnt lgkmcnt(" #n ")" ::: "memory")
; #define PG8_BAR __builtin_amdgcn_s_barrier()
; #define PG8_SCHED __builtin_amdgcn_sched_barrier(0)
; template <class Epi, class Sched>
; __device__ __forceinline__ void gemm_phase_gather(PG8_LAS unsigned char* lds, const Gemm g, const int* __restrict__ gidx, PG8_LAS int* itab  , const Sched& S, const Epi& E) {
;     ...
;             PG8_LDA(At, 1, 1); PG8_STAGE(PG8_SB(1, 0), b3, voffB); PG8_STAGE(PG8_SB(1, 1), b3 + hstep, voffB); PG8_STAGE(PG8_SA(1, 0), a3, vo2[0]);
;             PG8_WAIT_V(8); PG8_WAIT_L(0); PG8_BAR; PG8_MMA(1, 0, At, B0); PG8_MMA(1, 1, At, B1); PG8_BAR; PG8_SCHED;
;         }
;         if (wr == 0) PG8_BAR;
;         E(acc, cur, wr, wc, fr, fq); S.done(cur);
;     __device__ __forceinline__ void operator()(const f32x4 (&acc)[2][2][4][2], const pg8::Unit& u, int wr, int wc, int fr, int fq) const {
;         const int row0 = u.pm * 256 + wr * 64 + fr, col0 = (u.pn & 15) * 128 + wc * 32 + 8 * fq;
; #pragma unroll
;         for (int ai = 0; ai < 2; ++ai)
; #pragma unroll
;             for (int m = 0; m < 4; ++m) { float o[8];
; #pragma unroll
;                 for (int q = 0; q < 4; ++q) { o[q] = siluf(acc[ai][0][m][0][q]) * acc[ai][1][m][0][q]; o[4 + q] = siluf(acc[ai][0][m][1][q]) * acc[ai][1][m][1][q]; }
;                 *(v4u*)(ACT + (size_t)(row0 + ai * 128 + m * 16) * FF + col0) = pack8(o); }
	s_add_i32 s26, s50, s28
	v_lshl_add_u64 v[226:227], v[226:227], 0, s[10:11]
	s_mov_b32 m0, s26
	ds_read_b128 v[192:195], v152 offset:49152
	ds_read_b128 v[196:199], v152 offset:50176
	ds_read_b128 v[200:203], v152 offset:51200
	ds_read_b128 v[204:207], v152 offset:52224
	ds_read_b128 v[208:211], v152 offset:53248
	ds_read_b128 v[212:215], v152 offset:54272
	ds_read_b128 v[216:219], v152 offset:55296
	ds_read_b128 v[220:223], v152 offset:56320
	global_load_lds_dwordx4 v[226:227], off
	s_add_i32 m0, s26, 0x2000
	s_add_u32 s24, s24, 0x80080
	v_lshl_add_u64 v[226:227], v[228:229], 0, s[10:11]
	s_addc_u32 s25, s25, 0
	s_add_i32 s26, s51, s28
	global_load_lds_dwordx4 v[226:227], off
	v_lshl_add_u64 v[226:227], s[24:25], 0, v[130:131]
	s_mov_b32 m0, s26
	v_lshl_add_u64 v[224:225], v[224:225], 0, s[10:11]
	global_load_lds_dwordx4 v[226:227], off
	v_lshl_add_u64 v[226:227], s[24:25], 0, v[132:133]
	s_add_i32 m0, s26, 0x2000
	s_nop 0
	global_load_lds_dwordx4 v[226:227], off
	v_lshl_add_u64 v[226:227], v[230:231], 0, s[10:11]
	s_mov_b32 m0, s35
	s_nop 0
	global_load_lds_dwordx4 v[226:227], off
	s_mov_b32 m0, s36
	s_nop 0
	global_load_lds_dwordx4 v[224:225], off
	s_waitcnt vmcnt(8)
	s_waitcnt lgkmcnt(0)
	s_barrier
	s_setprio 1
	s_waitcnt lgkmcnt(0)
	v_mfma_f32_16x16x32_bf16 v[62:65], v[158:161], v[192:195], v[62:65]
	v_mfma_f32_16x16x32_bf16 v[58:61], v[166:169], v[192:195], v[58:61]
	v_mfma_f32_16x16x32_bf16 v[46:49], v[158:161], v[200:203], v[46:49]
	v_mfma_f32_16x16x32_bf16 v[38:41], v[166:169], v[200:203], v[38:41]
	v_mfma_f32_16x16x32_bf16 v[14:17], v[158:161], v[208:211], v[14:17]
	v_mfma_f32_16x16x32_bf16 v[10:13], v[166:169], v[208:211], v[10:13]
	v_mfma_f32_16x16x32_bf16 v[6:9], v[158:161], v[216:219], v[6:9]
	v_mfma_f32_16x16x32_bf16 v[2:5], v[166:169], v[216:219], v[2:5]
	v_mfma_f32_16x16x32_bf16 v[62:65], v[162:165], v[196:199], v[62:65]
	v_mfma_f32_16x16x32_bf16 v[58:61], v[170:173], v[196:199], v[58:61]
	v_mfma_f32_16x16x32_bf16 v[46:49], v[162:165], v[204:207], v[46:49]
	v_mfma_f32_16x16x32_bf16 v[38:41], v[170:173], v[204:207], v[38:41]
	v_mfma_f32_16x16x32_bf16 v[14:17], v[162:165], v[212:215], v[14:17]
	v_mfma_f32_16x16x32_bf16 v[10:13], v[170:173], v[212:215], v[10:13]
	v_mfma_f32_16x16x32_bf16 v[6:9], v[162:165], v[220:223], v[6:9]
	v_mfma_f32_16x16x32_bf16 v[2:5], v[170:173], v[220:223], v[2:5]
	s_setprio 0
	s_setprio 1
	v_mfma_f32_16x16x32_bf16 v[54:57], v[174:177], v[192:195], v[54:57]
	v_mfma_f32_16x16x32_bf16 v[50:53], v[182:185], v[192:195], v[50:53]
	v_mfma_f32_16x16x32_bf16 v[30:33], v[174:177], v[200:203], v[30:33]
	v_mfma_f32_16x16x32_bf16 v[26:29], v[182:185], v[200:203], v[26:29]
	v_mfma_f32_16x16x32_bf16 v[42:45], v[174:177], v[208:211], v[42:45]
	v_mfma_f32_16x16x32_bf16 v[34:37], v[182:185], v[208:211], v[34:37]
	v_mfma_f32_16x16x32_bf16 v[22:25], v[174:177], v[216:219], v[22:25]
	v_mfma_f32_16x16x32_bf16 v[18:21], v[182:185], v[216:219], v[18:21]
	v_mfma_f32_16x16x32_bf16 v[54:57], v[178:181], v[196:199], v[54:57]
	v_mfma_f32_16x16x32_bf16 v[50:53], v[188:191], v[196:199], v[50:53]
	v_mfma_f32_16x16x32_bf16 v[30:33], v[178:181], v[204:207], v[30:33]
	v_mfma_f32_16x16x32_bf16 v[26:29], v[188:191], v[204:207], v[26:29]
	v_mfma_f32_16x16x32_bf16 v[42:45], v[178:181], v[212:215], v[42:45]
	v_mfma_f32_16x16x32_bf16 v[34:37], v[188:191], v[212:215], v[34:37]
	v_mfma_f32_16x16x32_bf16 v[22:25], v[178:181], v[220:223], v[22:25]
	v_mfma_f32_16x16x32_bf16 v[18:21], v[188:191], v[220:223], v[18:21]
	s_setprio 0
	s_barrier
	s_add_i32 s49, s49, 2
	s_add_u32 s22, s22, 0x100
	s_addc_u32 s23, s23, 0
	s_cmp_gt_u32 s49, 29
	s_cbranch_scc0 .LBB0_1278
	s_and_b64 vcc, exec, s[14:15]
	s_cbranch_vccz .LBB0_1281
	s_barrier
.LBB0_1281:
	v_mul_f32_e32 v137, 0xbfb8aa3b, v126
	v_mul_f32_e32 v138, 0xbfb8aa3b, v122
	v_exp_f32_e32 v137, v137
	v_exp_f32_e32 v139, v138
	v_mul_f32_e32 v138, 0xbfb8aa3b, v127
	v_exp_f32_e32 v140, v138
	v_add_f32_e32 v137, 1.0, v137
	v_rcp_f32_e32 v138, v137
	v_add_f32_e32 v137, 1.0, v139
	v_add_f32_e32 v139, 1.0, v140
	v_rcp_f32_e32 v139, v139
	v_mul_f32_e32 v140, 0xbfb8aa3b, v123
	v_exp_f32_e32 v140, v140
	v_rcp_f32_e32 v142, v137
	v_pk_mul_f32 v[126:127], v[126:127], v[138:139]
	v_mul_f32_e32 v137, 0xbfb8aa3b, v129
	v_pk_mul_f32 v[118:119], v[126:127], v[118:119]
	v_add_f32_e32 v126, 1.0, v140
	v_mul_f32_e32 v127, 0xbfb8aa3b, v124
	v_rcp_f32_e32 v143, v126
	v_mul_f32_e32 v126, 0xbfb8aa3b, v128
	v_exp_f32_e32 v127, v127
	v_exp_f32_e32 v126, v126
	v_exp_f32_e32 v137, v137
	v_mul_f32_e32 v138, 0xbfb8aa3b, v125
	v_exp_f32_e32 v139, v138
	v_add_f32_e32 v127, 1.0, v127
	v_add_f32_e32 v126, 1.0, v126
	v_rcp_f32_e32 v138, v127
	v_add_f32_e32 v127, 1.0, v137
	v_rcp_f32_e32 v126, v126
	v_rcp_f32_e32 v127, v127
	v_add_f32_e32 v137, 1.0, v139
	v_rcp_f32_e32 v139, v137
	v_pk_mul_f32 v[122:123], v[122:123], v[142:143]
	v_lshl_add_u32 v136, s45, 8, v141
	s_lshl_b32 s17, s20, 7
	v_pk_mul_f32 v[114:115], v[122:123], v[114:115]
	v_pk_mul_f32 v[122:123], v[128:129], v[126:127]
	s_and_b32 s17, s17, 0x780
	v_pk_mul_f32 v[120:121], v[122:123], v[120:121]
	v_pk_mul_f32 v[122:123], v[124:125], v[138:139]
	v_ashrrev_i32_e32 v137, 31, v136
	v_or_b32_e32 v134, s17, v149
	v_pk_mul_f32 v[122:123], v[122:123], v[116:117]
	v_cvt_pk_bf16_f32 v116, v118, v119
	v_cvt_pk_bf16_f32 v118, v114, v115
	v_lshlrev_b64 v[114:115], 12, v[136:137]
	v_lshl_add_u64 v[114:115], s[8:9], 0, v[114:115]
	v_lshlrev_b32_e32 v134, 1, v134
	v_cvt_pk_bf16_f32 v117, v120, v121
	v_cvt_pk_bf16_f32 v119, v122, v123
	v_lshl_add_u64 v[114:115], v[114:115], 0, v[134:135]
	global_store_dwordx4 v[114:115], v[116:119], off
	s_nop 1
	v_mul_f32_e32 v116, 0xbfb8aa3b, v110
; __device__ __forceinline__ v4u pack8(const float (&o)[8]) { v4u w; w.x = pk2(o[0], o[1]); w.y = pk2(o[2], o[3]); w.z = pk2(o[4], o[5]); w.w = pk2(o[6], o[7]); return w; }
; __device__ __forceinline__ float siluf(float x) { return x * __builtin_amdgcn_rcpf(1.f + __expf(-x)); }
;     __device__ __forceinline__ void operator()(const f32x4 (&acc)[2][2][4][2], const pg8::Unit& u, int wr, int wc, int fr, int fq) const {
;         const int row0 = u.pm * 256 + wr * 64 + fr, col0 = (u.pn & 15) * 128 + wc * 32 + 8 * fq;
; #pragma unroll
;         for (int ai = 0; ai < 2; ++ai)
; #pragma unroll
;             for (int m = 0; m < 4; ++m) { float o[8];
; #pragma unroll
;                 for (int q = 0; q < 4; ++q) { o[q] = siluf(acc[ai][0][m][0][q]) * acc[ai][1][m][0][q]; o[4 + q] = siluf(acc[ai][0][m][1][q]) * acc[ai][1][m][1][q]; }
;                 *(v4u*)(ACT + (size_t)(row0 + ai * 128 + m * 16) * FF + col0) = pack8(o); }
	v_mul_f32_e32 v117, 0xbfb8aa3b, v106
	v_mul_f32_e32 v118, 0xbfb8aa3b, v111
	v_exp_f32_e32 v116, v116
	v_exp_f32_e32 v117, v117
	v_exp_f32_e32 v118, v118
	v_add_f32_e32 v116, 1.0, v116
	v_add_f32_e32 v119, 1.0, v117
	v_add_f32_e32 v117, 1.0, v118
	v_rcp_f32_e32 v116, v116
	v_rcp_f32_e32 v117, v117
	v_mul_f32_e32 v118, 0xbfb8aa3b, v107
	v_exp_f32_e32 v120, v118
	v_rcp_f32_e32 v118, v119
	v_pk_mul_f32 v[110:111], v[110:111], v[116:117]
	v_mul_f32_e32 v116, 0xbfb8aa3b, v113
	v_pk_mul_f32 v[102:103], v[110:111], v[102:103]
	v_add_f32_e32 v110, 1.0, v120
	v_rcp_f32_e32 v119, v110
	v_mul_f32_e32 v111, 0xbfb8aa3b, v108
	v_mul_f32_e32 v110, 0xbfb8aa3b, v112
	v_exp_f32_e32 v111, v111
	v_exp_f32_e32 v110, v110
	v_exp_f32_e32 v117, v116
	v_mul_f32_e32 v116, 0xbfb8aa3b, v109
	v_pk_mul_f32 v[106:107], v[106:107], v[118:119]
	v_exp_f32_e32 v118, v116
	v_add_f32_e32 v111, 1.0, v111
	v_add_f32_e32 v110, 1.0, v110
	v_rcp_f32_e32 v116, v111
	v_add_f32_e32 v111, 1.0, v117
	v_rcp_f32_e32 v110, v110
	v_rcp_f32_e32 v111, v111
	v_add_f32_e32 v117, 1.0, v118
	v_rcp_f32_e32 v117, v117
	v_pk_mul_f32 v[106:107], v[106:107], v[98:99]
	v_pk_mul_f32 v[98:99], v[112:113], v[110:111]
	s_nop 0
	v_pk_mul_f32 v[104:105], v[98:99], v[104:105]
	v_pk_mul_f32 v[98:99], v[108:109], v[116:117]
	s_nop 0
	v_pk_mul_f32 v[108:109], v[98:99], v[100:101]
	v_cvt_pk_bf16_f32 v98, v102, v103
	v_or_b32_e32 v102, 16, v136
	v_ashrrev_i32_e32 v103, 31, v102
	v_lshlrev_b64 v[102:103], 12, v[102:103]
	v_lshl_add_u64 v[102:103], s[8:9], 0, v[102:103]
	v_cvt_pk_bf16_f32 v99, v104, v105
	v_cvt_pk_bf16_f32 v100, v106, v107
	v_cvt_pk_bf16_f32 v101, v108, v109
	v_lshl_add_u64 v[102:103], v[102:103], 0, v[134:135]
	global_store_dwordx4 v[102:103], v[98:101], off
	s_nop 1
	v_mul_f32_e32 v98, 0xbfb8aa3b, v94
	v_mul_f32_e32 v99, 0xbfb8aa3b, v90
	v_mul_f32_e32 v100, 0xbfb8aa3b, v95
	v_exp_f32_e32 v98, v98
	v_exp_f32_e32 v99, v99
	v_exp_f32_e32 v100, v100
	v_add_f32_e32 v98, 1.0, v98
	v_add_f32_e32 v101, 1.0, v99
	v_add_f32_e32 v99, 1.0, v100
	v_rcp_f32_e32 v98, v98
	v_rcp_f32_e32 v99, v99
	v_mul_f32_e32 v100, 0xbfb8aa3b, v91
	v_exp_f32_e32 v102, v100
	v_rcp_f32_e32 v100, v101
	v_pk_mul_f32 v[94:95], v[94:95], v[98:99]
	v_mul_f32_e32 v98, 0xbfb8aa3b, v97
	v_pk_mul_f32 v[86:87], v[94:95], v[86:87]
	v_add_f32_e32 v94, 1.0, v102
	v_rcp_f32_e32 v101, v94
	v_mul_f32_e32 v95, 0xbfb8aa3b, v92
	v_mul_f32_e32 v94, 0xbfb8aa3b, v96
	v_exp_f32_e32 v95, v95
	v_exp_f32_e32 v94, v94
	v_exp_f32_e32 v99, v98
	v_mul_f32_e32 v98, 0xbfb8aa3b, v93
	v_pk_mul_f32 v[90:91], v[90:91], v[100:101]
	v_exp_f32_e32 v100, v98
	v_add_f32_e32 v95, 1.0, v95
	v_add_f32_e32 v94, 1.0, v94
	v_rcp_f32_e32 v98, v95
	v_add_f32_e32 v95, 1.0, v99
	v_rcp_f32_e32 v94, v94
	v_rcp_f32_e32 v95, v95
	v_add_f32_e32 v99, 1.0, v100
	v_rcp_f32_e32 v99, v99
	v_pk_mul_f32 v[90:91], v[90:91], v[82:83]
	v_pk_mul_f32 v[82:83], v[96:97], v[94:95]
	s_nop 0
	v_pk_mul_f32 v[88:89], v[82:83], v[88:89]
	v_pk_mul_f32 v[82:83], v[92:93], v[98:99]
	s_nop 0
	v_pk_mul_f32 v[92:93], v[82:83], v[84:85]
	v_cvt_pk_bf16_f32 v82, v86, v87
	v_or_b32_e32 v86, 32, v136
	v_ashrrev_i32_e32 v87, 31, v86
	v_lshlrev_b64 v[86:87], 12, v[86:87]
	v_lshl_add_u64 v[86:87], s[8:9], 0, v[86:87]
	v_cvt_pk_bf16_f32 v83, v88, v89
	v_cvt_pk_bf16_f32 v84, v90, v91
	v_cvt_pk_bf16_f32 v85, v92, v93
	v_lshl_add_u64 v[86:87], v[86:87], 0, v[134:135]
	global_store_dwordx4 v[86:87], v[82:85], off
	s_nop 1
	v_mul_f32_e32 v82, 0xbfb8aa3b, v78
	v_mul_f32_e32 v83, 0xbfb8aa3b, v74
	v_mul_f32_e32 v84, 0xbfb8aa3b, v79
	v_exp_f32_e32 v82, v82
	v_exp_f32_e32 v83, v83
	v_exp_f32_e32 v84, v84
	v_add_f32_e32 v82, 1.0, v82
	v_add_f32_e32 v85, 1.0, v83
	v_add_f32_e32 v83, 1.0, v84
	v_rcp_f32_e32 v82, v82
	v_rcp_f32_e32 v83, v83
	v_mul_f32_e32 v84, 0xbfb8aa3b, v75
	v_exp_f32_e32 v86, v84
	v_rcp_f32_e32 v84, v85
	v_pk_mul_f32 v[78:79], v[78:79], v[82:83]
	v_mul_f32_e32 v82, 0xbfb8aa3b, v81
	v_pk_mul_f32 v[70:71], v[78:79], v[70:71]
	v_add_f32_e32 v78, 1.0, v86
	v_rcp_f32_e32 v85, v78
	v_mul_f32_e32 v79, 0xbfb8aa3b, v76
	v_mul_f32_e32 v78, 0xbfb8aa3b, v80
	v_exp_f32_e32 v79, v79
	v_exp_f32_e32 v78, v78
	v_exp_f32_e32 v83, v82
	v_mul_f32_e32 v82, 0xbfb8aa3b, v77
	v_pk_mul_f32 v[74:75], v[74:75], v[84:85]
	v_exp_f32_e32 v84, v82
	v_add_f32_e32 v79, 1.0, v79
	v_add_f32_e32 v78, 1.0, v78
	v_rcp_f32_e32 v82, v79
	v_add_f32_e32 v79, 1.0, v83
	v_rcp_f32_e32 v78, v78
	v_rcp_f32_e32 v79, v79
	v_add_f32_e32 v83, 1.0, v84
	v_rcp_f32_e32 v83, v83
	v_pk_mul_f32 v[74:75], v[74:75], v[66:67]
	v_pk_mul_f32 v[66:67], v[80:81], v[78:79]
	s_nop 0
	v_pk_mul_f32 v[72:73], v[66:67], v[72:73]
	v_pk_mul_f32 v[66:67], v[76:77], v[82:83]
	s_nop 0
	v_pk_mul_f32 v[76:77], v[66:67], v[68:69]
	v_cvt_pk_bf16_f32 v66, v70, v71
	v_or_b32_e32 v70, 48, v136
	v_ashrrev_i32_e32 v71, 31, v70
	v_lshlrev_b64 v[70:71], 12, v[70:71]
	v_lshl_add_u64 v[70:71], s[8:9], 0, v[70:71]
	v_cvt_pk_bf16_f32 v67, v72, v73
	v_cvt_pk_bf16_f32 v68, v74, v75
	v_cvt_pk_bf16_f32 v69, v76, v77
	v_lshl_add_u64 v[70:71], v[70:71], 0, v[134:135]
	global_store_dwordx4 v[70:71], v[66:69], off
	s_nop 1
	v_mul_f32_e32 v66, 0xbfb8aa3b, v62
	v_mul_f32_e32 v67, 0xbfb8aa3b, v58
	v_mul_f32_e32 v68, 0xbfb8aa3b, v63
	v_exp_f32_e32 v66, v66
	v_exp_f32_e32 v67, v67
	v_exp_f32_e32 v68, v68
	v_add_f32_e32 v66, 1.0, v66
	v_add_f32_e32 v69, 1.0, v67
	v_add_f32_e32 v67, 1.0, v68
	v_rcp_f32_e32 v66, v66
	v_rcp_f32_e32 v67, v67
	v_mul_f32_e32 v68, 0xbfb8aa3b, v59
	v_exp_f32_e32 v70, v68
	v_rcp_f32_e32 v68, v69
	v_pk_mul_f32 v[62:63], v[62:63], v[66:67]
	v_mul_f32_e32 v66, 0xbfb8aa3b, v65
	v_pk_mul_f32 v[54:55], v[62:63], v[54:55]
	v_add_f32_e32 v62, 1.0, v70
	v_rcp_f32_e32 v69, v62
; #define PG8_BAR __builtin_amdgcn_s_barrier()
; #define PG8_BAR __builtin_amdgcn_s_barrier()
; __device__ __forceinline__ v4u pack8(const float (&o)[8]) { v4u w; w.x = pk2(o[0], o[1]); w.y = pk2(o[2], o[3]); w.z = pk2(o[4], o[5]); w.w = pk2(o[6], o[7]); return w; }
; __device__ __forceinline__ float siluf(float x) { return x * __builtin_amdgcn_rcpf(1.f + __expf(-x)); }
; template <class Epi, class Sched>
; __device__ __forceinline__ void gemm_phase_gather(PG8_LAS unsigned char* lds, const Gemm g, const int* __restrict__ gidx, PG8_LAS int* itab  , const Sched& S, const Epi& E) {
;     ...
;         E(acc, cur, wr, wc, fr, fq); S.done(cur);
;         if (!has_next) break;
; #pragma unroll
;         for (int a = 0; a < 2; ++a)
; #pragma unroll
;             for (int b = 0; b < 2; ++b)
; #pragma unroll
;                 for (int m = 0; m < 4; ++m)
; #pragma unroll
;                     for (int n = 0; n < 2; ++n) acc[a][b][m][n] = (f32x4){0.f, 0.f, 0.f, 0.f};
;         cur = nxt; cB = nB; ++ui;
; #pragma unroll
;         for (int _h = 0; _h < 2; ++_h)
; #pragma unroll
;             for (int _i = 0; _i < 2; ++_i) cvo[_h][_i] = nvo[_h][_i];
;         if (wr == 1) PG8_BAR;
;     __device__ __forceinline__ void operator()(const f32x4 (&acc)[2][2][4][2], const pg8::Unit& u, int wr, int wc, int fr, int fq) const {
;         const int row0 = u.pm * 256 + wr * 64 + fr, col0 = (u.pn & 15) * 128 + wc * 32 + 8 * fq;
; #pragma unroll
;         for (int ai = 0; ai < 2; ++ai)
; #pragma unroll
;             for (int m = 0; m < 4; ++m) { float o[8];
; #pragma unroll
;                 for (int q = 0; q < 4; ++q) { o[q] = siluf(acc[ai][0][m][0][q]) * acc[ai][1][m][0][q]; o[4 + q] = siluf(acc[ai][0][m][1][q]) * acc[ai][1][m][1][q]; }
;                 *(v4u*)(ACT + (size_t)(row0 + ai * 128 + m * 16) * FF + col0) = pack8(o); }
	v_mul_f32_e32 v63, 0xbfb8aa3b, v60
	v_mul_f32_e32 v62, 0xbfb8aa3b, v64
	v_exp_f32_e32 v63, v63
	v_exp_f32_e32 v62, v62
	v_exp_f32_e32 v67, v66
	v_mul_f32_e32 v66, 0xbfb8aa3b, v61
	v_pk_mul_f32 v[58:59], v[58:59], v[68:69]
	v_exp_f32_e32 v68, v66
	v_add_f32_e32 v63, 1.0, v63
	v_add_f32_e32 v62, 1.0, v62
	v_rcp_f32_e32 v66, v63
	v_add_f32_e32 v63, 1.0, v67
	v_rcp_f32_e32 v62, v62
	v_rcp_f32_e32 v63, v63
	v_add_f32_e32 v67, 1.0, v68
	v_rcp_f32_e32 v67, v67
	v_pk_mul_f32 v[58:59], v[58:59], v[50:51]
	v_pk_mul_f32 v[50:51], v[64:65], v[62:63]
	s_nop 0
	v_pk_mul_f32 v[56:57], v[50:51], v[56:57]
	v_pk_mul_f32 v[50:51], v[60:61], v[66:67]
	s_nop 0
	v_pk_mul_f32 v[60:61], v[50:51], v[52:53]
	v_cvt_pk_bf16_f32 v50, v54, v55
	v_add_co_u32_e32 v54, vcc, s40, v114
	v_cvt_pk_bf16_f32 v51, v56, v57
	v_cvt_pk_bf16_f32 v52, v58, v59
	v_cvt_pk_bf16_f32 v53, v60, v61
	v_addc_co_u32_e32 v55, vcc, 0, v115, vcc
	global_store_dwordx4 v[54:55], v[50:53], off
	s_nop 1
	v_mul_f32_e32 v50, 0xbfb8aa3b, v46
	v_mul_f32_e32 v51, 0xbfb8aa3b, v38
	v_mul_f32_e32 v52, 0xbfb8aa3b, v47
	v_exp_f32_e32 v50, v50
	v_exp_f32_e32 v51, v51
	v_exp_f32_e32 v52, v52
	v_add_f32_e32 v50, 1.0, v50
	v_add_f32_e32 v53, 1.0, v51
	v_add_f32_e32 v51, 1.0, v52
	v_rcp_f32_e32 v50, v50
	v_rcp_f32_e32 v51, v51
	v_mul_f32_e32 v52, 0xbfb8aa3b, v39
	v_exp_f32_e32 v54, v52
	v_rcp_f32_e32 v52, v53
	v_pk_mul_f32 v[46:47], v[46:47], v[50:51]
	v_mul_f32_e32 v50, 0xbfb8aa3b, v49
	v_pk_mul_f32 v[30:31], v[46:47], v[30:31]
	v_add_f32_e32 v46, 1.0, v54
	v_rcp_f32_e32 v53, v46
	v_mul_f32_e32 v47, 0xbfb8aa3b, v40
	v_mul_f32_e32 v46, 0xbfb8aa3b, v48
	v_exp_f32_e32 v47, v47
	v_exp_f32_e32 v46, v46
	v_exp_f32_e32 v51, v50
	v_mul_f32_e32 v50, 0xbfb8aa3b, v41
	v_pk_mul_f32 v[38:39], v[38:39], v[52:53]
	v_exp_f32_e32 v52, v50
	v_add_f32_e32 v47, 1.0, v47
	v_add_f32_e32 v46, 1.0, v46
	v_rcp_f32_e32 v50, v47
	v_add_f32_e32 v47, 1.0, v51
	v_rcp_f32_e32 v46, v46
	v_rcp_f32_e32 v47, v47
	v_add_f32_e32 v51, 1.0, v52
	v_rcp_f32_e32 v51, v51
	v_pk_mul_f32 v[38:39], v[38:39], v[26:27]
	v_pk_mul_f32 v[26:27], v[48:49], v[46:47]
	s_nop 0
	v_pk_mul_f32 v[32:33], v[26:27], v[32:33]
	v_pk_mul_f32 v[26:27], v[40:41], v[50:51]
	s_nop 0
	v_pk_mul_f32 v[40:41], v[26:27], v[28:29]
	v_cvt_pk_bf16_f32 v26, v30, v31
	v_add_co_u32_e32 v30, vcc, s41, v114
	v_cvt_pk_bf16_f32 v27, v32, v33
	v_cvt_pk_bf16_f32 v28, v38, v39
	v_cvt_pk_bf16_f32 v29, v40, v41
	v_addc_co_u32_e32 v31, vcc, 0, v115, vcc
	global_store_dwordx4 v[30:31], v[26:29], off
	s_nop 1
	v_mul_f32_e32 v26, 0xbfb8aa3b, v14
	v_mul_f32_e32 v27, 0xbfb8aa3b, v10
	v_mul_f32_e32 v28, 0xbfb8aa3b, v15
	v_exp_f32_e32 v26, v26
	v_exp_f32_e32 v27, v27
	v_exp_f32_e32 v28, v28
	v_add_f32_e32 v26, 1.0, v26
	v_add_f32_e32 v29, 1.0, v27
	v_add_f32_e32 v27, 1.0, v28
	v_mul_f32_e32 v28, 0xbfb8aa3b, v11
	v_rcp_f32_e32 v26, v26
	v_rcp_f32_e32 v27, v27
	v_exp_f32_e32 v30, v28
	v_rcp_f32_e32 v28, v29
	v_pk_mul_f32 v[14:15], v[14:15], v[26:27]
	v_add_f32_e32 v26, 1.0, v30
	v_rcp_f32_e32 v29, v26
	v_mul_f32_e32 v27, 0xbfb8aa3b, v12
	v_mul_f32_e32 v26, 0xbfb8aa3b, v16
	v_exp_f32_e32 v27, v27
	v_pk_mul_f32 v[10:11], v[10:11], v[28:29]
	v_mul_f32_e32 v28, 0xbfb8aa3b, v17
	v_exp_f32_e32 v26, v26
	v_exp_f32_e32 v29, v28
	v_mul_f32_e32 v28, 0xbfb8aa3b, v13
	v_exp_f32_e32 v30, v28
	v_add_f32_e32 v27, 1.0, v27
	v_add_f32_e32 v26, 1.0, v26
	v_rcp_f32_e32 v28, v27
	v_add_f32_e32 v27, 1.0, v29
	v_rcp_f32_e32 v26, v26
	v_rcp_f32_e32 v27, v27
	v_add_f32_e32 v29, 1.0, v30
	v_rcp_f32_e32 v29, v29
	v_pk_mul_f32 v[30:31], v[10:11], v[34:35]
	v_pk_mul_f32 v[10:11], v[16:17], v[26:27]
	v_pk_mul_f32 v[14:15], v[14:15], v[42:43]
	v_pk_mul_f32 v[16:17], v[10:11], v[44:45]
	v_pk_mul_f32 v[10:11], v[12:13], v[28:29]
	v_cvt_pk_bf16_f32 v12, v30, v31
	v_pk_mul_f32 v[26:27], v[10:11], v[36:37]
	v_cvt_pk_bf16_f32 v10, v14, v15
	v_add_co_u32_e32 v14, vcc, s42, v114
	v_cvt_pk_bf16_f32 v11, v16, v17
	v_cvt_pk_bf16_f32 v13, v26, v27
	v_addc_co_u32_e32 v15, vcc, 0, v115, vcc
	global_store_dwordx4 v[14:15], v[10:13], off
	s_nop 1
	v_mul_f32_e32 v10, 0xbfb8aa3b, v6
	v_mul_f32_e32 v11, 0xbfb8aa3b, v2
	v_mul_f32_e32 v12, 0xbfb8aa3b, v7
	v_exp_f32_e32 v10, v10
	v_exp_f32_e32 v11, v11
	v_exp_f32_e32 v12, v12
	v_add_f32_e32 v10, 1.0, v10
	v_add_f32_e32 v13, 1.0, v11
	v_add_f32_e32 v11, 1.0, v12
	v_mul_f32_e32 v12, 0xbfb8aa3b, v3
	v_rcp_f32_e32 v10, v10
	v_rcp_f32_e32 v11, v11
	v_exp_f32_e32 v14, v12
	v_rcp_f32_e32 v12, v13
	v_pk_mul_f32 v[6:7], v[6:7], v[10:11]
	v_add_f32_e32 v10, 1.0, v14
	v_rcp_f32_e32 v13, v10
	v_mul_f32_e32 v11, 0xbfb8aa3b, v4
	v_mul_f32_e32 v10, 0xbfb8aa3b, v8
	v_exp_f32_e32 v11, v11
	v_pk_mul_f32 v[2:3], v[2:3], v[12:13]
	v_mul_f32_e32 v12, 0xbfb8aa3b, v9
	v_exp_f32_e32 v10, v10
	v_exp_f32_e32 v13, v12
	v_mul_f32_e32 v12, 0xbfb8aa3b, v5
	v_exp_f32_e32 v14, v12
	v_add_f32_e32 v11, 1.0, v11
	v_add_f32_e32 v10, 1.0, v10
	v_rcp_f32_e32 v12, v11
	v_add_f32_e32 v11, 1.0, v13
	v_rcp_f32_e32 v10, v10
	v_rcp_f32_e32 v11, v11
	v_add_f32_e32 v13, 1.0, v14
	v_rcp_f32_e32 v13, v13
	v_pk_mul_f32 v[14:15], v[2:3], v[18:19]
	v_pk_mul_f32 v[2:3], v[8:9], v[10:11]
	v_pk_mul_f32 v[6:7], v[6:7], v[22:23]
	v_pk_mul_f32 v[8:9], v[2:3], v[24:25]
	v_pk_mul_f32 v[2:3], v[4:5], v[12:13]
	v_cvt_pk_bf16_f32 v4, v14, v15
	v_pk_mul_f32 v[10:11], v[2:3], v[20:21]
	v_cvt_pk_bf16_f32 v2, v6, v7
	v_add_co_u32_e32 v6, vcc, 0xb0000, v114
	v_cvt_pk_bf16_f32 v3, v8, v9
	s_nop 0
	v_addc_co_u32_e32 v7, vcc, 0, v115, vcc
	v_cvt_pk_bf16_f32 v5, v10, v11
	s_and_b64 vcc, exec, s[6:7]
	s_mov_b64 s[6:7], -1
	s_mov_b32 s98, 1
	global_store_dwordx4 v[6:7], v[2:5], off
	s_cbranch_vccnz .LBB0_1272
	s_andn2_b64 vcc, exec, s[4:5]
	s_cbranch_vccnz .LBB0_1271
	s_barrier
	s_branch .LBB0_1271

; #define PG8_WAIT_V(n) asm volatile("s_waitcnt vmcnt(" #n ")" ::: "memory")
; template <class Epi, class Sched, bool ALIGN_EPI = false, bool SP2 = false>
; __device__ __forceinline__ void gemm_phase(PG8_LAS unsigned char* lds, const Gemm g, const Sched& S, const Epi& E) {
;     const int tid = threadIdx.x, wid = __builtin_amdgcn_readfirstlane(tid >> 6), lane = tid & 63, wr = wid >> 2, wc = wid & 3, fr = lane & 15, fq = lane >> 4;
;     const int K = g.K, nt = K / BK;
;     unsigned voffA[2], voffB[2];
; #pragma unroll
;     for (int i = 0; i < 2; ++i) { int R, C; stage_rc(tid * 16 + i * 8192, R, C); const int Rb = Epi::PERM ? ((R & ~31) + perm32(R & 31)) : R;
;         voffA[i] = (unsigned)(R * K + C) * 2u; voffB[i] = (unsigned)(Rb * K + C) * 2u; }
;     const size_t kstep = (size_t)(BK * 2);
;     const size_t hstep = (size_t)HALF * K * 2;
;     const size_t tstep = 2 * hstep;
;     const unsigned ldsw = (unsigned)wid * 1024u;
;     const int aoff = lds_byte(wr * 64 + fr, fq * 8), boff = lds_byte(wc * 32 + fr, fq * 8);
;     ...
;     Unit cur, nxt; int ui = 0;
;     if (!S.next(0, cur)) return;
;     f32x4 acc[2][2][4][2];
; #pragma unroll
;     for (int a = 0; a < 2; ++a)
; #pragma unroll
;         for (int b = 0; b < 2; ++b)
; #pragma unroll
;             for (int m = 0; m < 4; ++m)
; #pragma unroll
;                 for (int n = 0; n < 2; ++n) acc[a][b][m][n] = (f32x4){0.f, 0.f, 0.f, 0.f};
;     bf16x8 At[4][2], B0[2][2], B1[2][2];
;     const char* cA = (const char*)(cur.sel ? g.A2 : g.A) + (size_t)cur.pm * tstep; const char* cB = (const char*)(cur.sel ? g.Bt2 : g.Bt) + (size_t)cur.pn * tstep;
;     S.a_ready(cur);
;     if constexpr (SP2) {
;         PG8_STAGE(PG8_SB(0, 0), cB, voffB); PG8_STAGE(PG8_SB(0, 1), cB + hstep, voffB); PG8_STAGE(PG8_SA(0, 0), cA, voffA); PG8_STAGE(PG8_SA(0, 1), cA + hstep, voffA);
;         if (wr == 1) PG8_BAR;
;         PG8_WAIT_V(2); PG8_BAR;
;         PG8_STAGE(PG8_SB(1, 0), cB + kstep, voffB); PG8_STAGE(PG8_SA(1, 0), cA + kstep, voffA); PG8_STAGE(PG8_SB(1, 1), cB + hstep + kstep, voffB);
;         PG8_WAIT_V(6); PG8_BAR;
; __global__ void __launch_bounds__(NWAVES * 64, 2) mk_fwd(Args args) {
;     ...
;     if (IN(11)) { PHASE_BASES();
;         pg8::Gemm g{ACT, W2, NB * NE * CAP, NE * D, FF}; OrderMoe<8> S; S.init(G, bx); EpiMoe2 E{OUTE, VAL};
;         pg8::gemm_phase<EpiMoe2, OrderMoe<8>, true, true>(lds, g, S, E);
.LBB0_1339:
	s_mov_b32 s98, 0
	s_cmp_lt_i32 s78, 12
	s_cselect_b64 s[0:1], -1, 0
	s_cmp_gt_i32 s79, 11
	s_cselect_b64 s[2:3], -1, 0
	s_and_b64 s[0:1], s[0:1], s[2:3]
	s_andn2_b64 vcc, exec, s[0:1]
	s_cbranch_vccnz .LBB0_1410
	s_mov_b64 s[0:1], s[74:75]
	s_cmpk_gt_i32 s88, 0x3ff
	v_readfirstlane_b32 s10, v0
	s_cbranch_scc1 .LBB0_1356
	s_load_dwordx2 s[6:7], s[0:1], 0xd8
	v_lshrrev_b32_e32 v1, 5, v0
	v_lshrrev_b32_e32 v3, 1, v0
	v_and_b32_e32 v1, 4, v1
	v_bfe_u32 v2, v0, 2, 2
	v_and_b32_e32 v12, 24, v3
	v_lshlrev_b32_e32 v3, 4, v0
	s_waitcnt lgkmcnt(0)
	s_add_u32 s33, s6, 0x2800000
	v_or3_b32 v2, v1, v2, v12
	v_or_b32_e32 v1, 0x2000, v3
	s_addc_u32 s40, s7, 0
	v_lshrrev_b32_e32 v4, 7, v1
	s_movk_i32 s0, 0x60
	s_add_u32 s41, s6, 0x39700000
	v_and_or_b32 v5, v4, s0, v2
	v_bfe_u32 v13, v0, 2, 4
	s_movk_i32 s0, 0x70
	s_addc_u32 s42, s7, 0
	v_and_or_b32 v4, v4, s0, v13
	s_lshr_b32 s0, s89, 29
	s_add_i32 s0, s88, s0
	s_ashr_i32 s0, s0, 3
	s_lshl_b32 s1, s88, 7
	s_mulk_i32 s0, 0xfc01
	s_add_i32 s0, s0, s1
	s_ashr_i32 s1, s0, 31
	s_lshr_b32 s1, s1, 26
	s_add_i32 s1, s0, s1
	s_ashr_i32 s2, s1, 6
	s_andn2_b32 s1, s1, 63
	s_sub_i32 s0, s0, s1
	s_bfe_i32 s1, s0, 0x80000
	s_bfe_u32 s1, s1, 0x3000c
	s_add_i32 s1, s0, s1
	s_bfe_i32 s3, s1, 0x80000
	s_and_b32 s1, s1, 0xf8
	s_sub_i32 s0, s0, s1
	s_sext_i32_i16 s3, s3
	s_sext_i32_i8 s0, s0
	s_ashr_i32 s1, s3, 3
	s_and_b32 s3, s0, 1
	s_lshl_b32 s0, s0, 3
	s_and_b32 s0, s0, 0x7ffffff0
	s_add_i32 s0, s0, s2
	s_lshl_b32 s0, s0, 1
	s_or_b32 s30, s0, s3
	s_lshl_b32 s0, s2, 3
	v_and_b32_e32 v6, 32, v0
	s_add_i32 s28, s0, s1
	s_lshr_b32 s8, s10, 6
	v_bitop3_b32 v10, v3, v6, 48 bitop3:0x6c
	v_and_b32_e32 v11, 64, v0
	s_ashr_i32 s31, s30, 31
	s_ashr_i32 s29, s28, 31
	s_lshr_b32 s11, s10, 8
	s_lshl_b32 s43, s8, 10
	v_or_b32_e32 v3, v10, v11
	s_lshl_b64 s[0:1], s[30:31], 20
	s_lshl_b64 s[2:3], s[28:29], 20
	s_waitcnt vmcnt(0)
	v_lshl_or_b32 v130, v4, 12, v3
	v_lshrrev_b32_e32 v4, 3, v0
	s_add_u32 s36, s41, s2
	v_and_or_b32 v2, v4, 32, v2
	s_addc_u32 s37, s42, s3
	s_add_i32 s29, s43, 0
	v_lshl_or_b32 v132, v2, 12, v3
	s_add_i32 m0, s29, 0x10000
	v_lshl_or_b32 v128, v5, 12, v3
	global_load_lds_dwordx4 v132, s[36:37]
	s_add_i32 m0, s29, 0x12000
	s_add_u32 s2, s36, 0x80000
	global_load_lds_dwordx4 v128, s[36:37]
	s_addc_u32 s3, s37, 0
	s_add_i32 m0, s29, 0x14000
	v_and_or_b32 v2, v4, 48, v13
	global_load_lds_dwordx4 v132, s[2:3]
	s_add_i32 m0, s29, 0x16000
	s_add_u32 s34, s33, s0
	s_addc_u32 s35, s40, s1
	s_add_i32 s31, s29, 0x2000
	v_lshl_or_b32 v134, v2, 12, v3
	global_load_lds_dwordx4 v128, s[2:3]
	s_mov_b32 m0, s29
	s_add_u32 s0, s34, 0x80000
	global_load_lds_dwordx4 v134, s[34:35]
	s_mov_b32 m0, s31
	s_addc_u32 s1, s35, 0
	s_add_i32 s44, s29, 0x4000
	global_load_lds_dwordx4 v130, s[34:35]
	s_mov_b32 m0, s44
	s_add_i32 s45, s29, 0x6000
	global_load_lds_dwordx4 v134, s[0:1]
	s_mov_b32 m0, s45
	v_mov_b32_e32 v137, 0
	global_load_lds_dwordx4 v130, s[0:1]
	v_mov_b32_e32 v133, v137
	v_mov_b32_e32 v129, v137
	v_mov_b32_e32 v135, v137
	v_mov_b32_e32 v131, v137
	s_cmp_eq_u32 s11, 1
	s_mov_b32 s46, 0
	v_lshl_add_u64 v[8:9], s[36:37], 0, v[132:133]
	v_lshl_add_u64 v[4:5], s[36:37], 0, v[128:129]
	s_mov_b64 s[0:1], 0x80000
	v_lshl_add_u64 v[2:3], s[34:35], 0, v[134:135]
	s_cselect_b64 s[2:3], -1, 0
	s_cmp_lg_u32 s11, 1
	v_lshl_add_u64 v[6:7], s[34:35], 0, v[130:131]
	s_cbranch_scc1 .LBB0_1343
	s_barrier

;     __device__ __forceinline__ unsigned claim_issue(int wid, int lane) const { unsigned r = 0u; if (wid == 0 && lane == 0) { unsigned z; asm volatile("v_mov_b32 %0, 0" : "=v"(z)); r = __hip_atomic_fetch_add(q + z, 1u, __ATOMIC_RELAXED, __HIP_MEMORY_SCOPE_AGENT); } return r; }
;     __device__ __forceinline__ bool next(int i, pg8::Unit& u) const { const int s = i >= R ? 1 : 0; const bool ok = so.next(i - s * R, u); u.sel = s; return ok && i < 2 * R; }
; template <class Epi, class Sched, bool ALIGN_EPI = false, bool SP2 = false>
; __device__ __forceinline__ void gemm_phase(PG8_LAS unsigned char* lds, const Gemm g, const Sched& S, const Epi& E) {
;     ...
;     for (;;) {
;         const bool has_next = S.next(ui + 1, nxt);
;         unsigned pend = 0u; if constexpr (Sched::DYNAMIC) pend = S.claim_issue(wid, lane);
;         const char* nA = has_next ? (const char*)(nxt.sel ? g.A2 : g.A) + (size_t)nxt.pm * tstep : cA; const char* nB = has_next ? (const char*)(nxt.sel ? g.Bt2 : g.Bt) + (size_t)nxt.pn * tstep : cB;
;         for (int t = 0; t < nt; t += 2) {
;             const bool last = (t == nt - 2);
;             const char* a1 = cA + (size_t)(t + 1) * kstep;
;             const char* a2 = last ? nA : cA + (size_t)(t + 2) * kstep; const char* b2 = last ? nB : cB + (size_t)(t + 2) * kstep;
;             const char* a3 = a2 + kstep; const char* b3 = b2 + kstep;
;             if (last && has_next) S.a_ready(nxt);
;     ...
; #pragma unroll
;         for (int a = 0; a < 2; ++a)
; #pragma unroll
;             for (int b = 0; b < 2; ++b)
; #pragma unroll
;                 for (int m = 0; m < 4; ++m)
; #pragma unroll
;                     for (int n = 0; n < 2; ++n) acc[a][b][m][n] = (f32x4){0.f, 0.f, 0.f, 0.f};
;         cur = nxt; cA = nA; cB = nB; ++ui;
.LBB0_1348:
	s_ashr_i32 s19, s18, 31
	s_lshl_b64 s[24:25], s[18:19], 20
	s_add_u32 s24, s33, s24
	s_addc_u32 s25, s40, s25
	s_and_b64 s[26:27], s[22:23], exec
	s_cselect_b32 s19, s25, s35
	s_cselect_b32 s55, s24, s34
	s_ashr_i32 s21, s20, 31
	s_lshl_b64 s[26:27], s[20:21], 20
	s_add_u32 s26, s41, s26
	s_addc_u32 s27, s42, s27
	s_and_b64 s[38:39], s[22:23], exec
	s_cselect_b32 s21, s27, s37
	s_cselect_b32 s56, s26, s36
	s_add_u32 s34, s34, 0x80080
	s_addc_u32 s35, s35, 0
	s_add_u32 s57, s36, 0x100
	v_mov_b32_e32 v0, 0
	s_addc_u32 s58, s37, 0
	s_mov_b32 s59, -2
	v_mov_b32_e32 v1, v0
	v_mov_b32_e32 v2, v0
	v_mov_b32_e32 v3, v0
	v_mov_b32_e32 v4, v0
	v_mov_b32_e32 v5, v0
	v_mov_b32_e32 v6, v0
	v_mov_b32_e32 v7, v0
	v_mov_b32_e32 v8, v0
	v_mov_b32_e32 v9, v0
	v_mov_b32_e32 v10, v0
	v_mov_b32_e32 v11, v0
	v_mov_b32_e32 v16, v0
	v_mov_b32_e32 v17, v0
	v_mov_b32_e32 v18, v0
	v_mov_b32_e32 v19, v0
	v_mov_b32_e32 v24, v0
	v_mov_b32_e32 v25, v0
	v_mov_b32_e32 v26, v0
	v_mov_b32_e32 v27, v0
	v_mov_b32_e32 v32, v0
	v_mov_b32_e32 v33, v0
	v_mov_b32_e32 v34, v0
	v_mov_b32_e32 v35, v0
	v_mov_b32_e32 v40, v0
	v_mov_b32_e32 v41, v0
	v_mov_b32_e32 v42, v0
	v_mov_b32_e32 v43, v0
	v_mov_b32_e32 v48, v0
	v_mov_b32_e32 v49, v0
	v_mov_b32_e32 v50, v0
	v_mov_b32_e32 v51, v0
	v_mov_b32_e32 v12, v0
	v_mov_b32_e32 v13, v0
	v_mov_b32_e32 v14, v0
	v_mov_b32_e32 v15, v0
	v_mov_b32_e32 v20, v0
	v_mov_b32_e32 v21, v0
	v_mov_b32_e32 v22, v0
	v_mov_b32_e32 v23, v0
	v_mov_b32_e32 v28, v0
	v_mov_b32_e32 v29, v0
	v_mov_b32_e32 v30, v0
	v_mov_b32_e32 v31, v0
	v_mov_b32_e32 v36, v0
	v_mov_b32_e32 v37, v0
	v_mov_b32_e32 v38, v0
	v_mov_b32_e32 v39, v0
	v_mov_b32_e32 v44, v0
	v_mov_b32_e32 v45, v0
	v_mov_b32_e32 v46, v0
	v_mov_b32_e32 v47, v0
	v_mov_b32_e32 v52, v0
	v_mov_b32_e32 v53, v0
	v_mov_b32_e32 v54, v0
	v_mov_b32_e32 v55, v0
	v_mov_b32_e32 v56, v0
	v_mov_b32_e32 v57, v0
	v_mov_b32_e32 v58, v0
	v_mov_b32_e32 v59, v0
	v_mov_b32_e32 v60, v0
	v_mov_b32_e32 v61, v0
	v_mov_b32_e32 v62, v0
	v_mov_b32_e32 v63, v0
	v_mov_b32_e32 v64, v0
	v_mov_b32_e32 v65, v0
	v_mov_b32_e32 v66, v0
	v_mov_b32_e32 v67, v0
	v_mov_b32_e32 v68, v0
	v_mov_b32_e32 v69, v0
	v_mov_b32_e32 v70, v0
	v_mov_b32_e32 v71, v0
	v_mov_b32_e32 v80, v0
	v_mov_b32_e32 v81, v0
	v_mov_b32_e32 v82, v0
	v_mov_b32_e32 v83, v0
	v_mov_b32_e32 v84, v0
	v_mov_b32_e32 v85, v0
	v_mov_b32_e32 v86, v0
	v_mov_b32_e32 v87, v0
	v_mov_b32_e32 v88, v0
	v_mov_b32_e32 v89, v0
	v_mov_b32_e32 v90, v0
	v_mov_b32_e32 v91, v0
	v_mov_b32_e32 v92, v0
	v_mov_b32_e32 v93, v0
	v_mov_b32_e32 v94, v0
	v_mov_b32_e32 v95, v0
	v_mov_b32_e32 v104, v0
	v_mov_b32_e32 v105, v0
	v_mov_b32_e32 v106, v0
	v_mov_b32_e32 v107, v0
	v_mov_b32_e32 v108, v0
	v_mov_b32_e32 v109, v0
	v_mov_b32_e32 v110, v0
	v_mov_b32_e32 v111, v0
	v_mov_b32_e32 v72, v0
	v_mov_b32_e32 v73, v0
	v_mov_b32_e32 v74, v0
	v_mov_b32_e32 v75, v0
	v_mov_b32_e32 v76, v0
	v_mov_b32_e32 v77, v0
	v_mov_b32_e32 v78, v0
	v_mov_b32_e32 v79, v0
	v_mov_b32_e32 v96, v0
	v_mov_b32_e32 v97, v0
	v_mov_b32_e32 v98, v0
	v_mov_b32_e32 v99, v0
	v_mov_b32_e32 v100, v0
	v_mov_b32_e32 v101, v0
	v_mov_b32_e32 v102, v0
	v_mov_b32_e32 v103, v0
	v_mov_b32_e32 v112, v0
	v_mov_b32_e32 v113, v0
	v_mov_b32_e32 v114, v0
	v_mov_b32_e32 v115, v0
	v_mov_b32_e32 v116, v0
	v_mov_b32_e32 v117, v0
	v_mov_b32_e32 v118, v0
	v_mov_b32_e32 v119, v0
	v_mov_b32_e32 v120, v0
	v_mov_b32_e32 v121, v0
	v_mov_b32_e32 v122, v0
	v_mov_b32_e32 v123, v0
	v_mov_b32_e32 v124, v0
	v_mov_b32_e32 v125, v0
	v_mov_b32_e32 v126, v0
	v_mov_b32_e32 v127, v0
	s_cmp_lg_u32 s98, 0
	s_cselect_b32 s99, -2, 0x7ffffff0
	s_branch .LBB0_1349

; #define PG8_STAGE(bufoff, gbase, voff) do { _Pragma("unroll") for (int _i = 0; _i < 2; ++_i) \
;         __builtin_amdgcn_global_load_lds((const unsigned*)((const char*)(gbase) + (voff)[_i]), (PG8_LAS unsigned*)(lds + (bufoff) + ldsw + _i * 8192), 16, 0, 0); } while (0)
; #define PG8_LDA(dst, b, h) do { _Pragma("unroll") for (int m = 0; m < 4; ++m) _Pragma("unroll") for (int k = 0; k < 2; ++k) dst[m][k] = *(const PG8_LAS bf16x8*)(lds + PG8_SA(b, h) + aoff + m * 2048 + k * 1024); } while (0)
; #define PG8_LDB(dst, b, h) do { _Pragma("unroll") for (int n = 0; n < 2; ++n) _Pragma("unroll") for (int k = 0; k < 2; ++k) dst[n][k] = *(const PG8_LAS bf16x8*)(lds + PG8_SB(b, h) + boff + n * 2048 + k * 1024); } while (0)
; #define PG8_MMA(ai, bj, At, Bt) do { __builtin_amdgcn_s_setprio(1); _Pragma("unroll") for (int m = 0; m < 4; ++m) _Pragma("unroll") for (int n = 0; n < 2; ++n) _Pragma("unroll") for (int k = 0; k < 2; ++k) \
;         acc[ai][bj][m][n] = __builtin_amdgcn_mfma_f32_16x16x32_bf16(Bt[n][k], At[m][k], acc[ai][bj][m][n], 0, 0, 0); __builtin_amdgcn_s_setprio(0); } while (0)
; #define PG8_WAIT_V(n) asm volatile("s_waitcnt vmcnt(" #n ")" ::: "memory")
; #define PG8_WAIT_L(n) asm volatile("s_waitcnt lgkmcnt(" #n ")" ::: "memory")
; #define PG8_BAR __builtin_amdgcn_s_barrier()
; #define PG8_SCHED __builtin_amdgcn_sched_barrier(0)
; #define PG8_STAGE(bufoff, gbase, voff) do { _Pragma("unroll") for (int _i = 0; _i < 2; ++_i) \
;         __builtin_amdgcn_global_load_lds((const unsigned*)((const char*)(gbase) + (voff)[_i]), (PG8_LAS unsigned*)(lds + (bufoff) + ldsw + _i * 8192), 16, 0, 0); } while (0)
; #define PG8_WAIT_V(n) asm volatile("s_waitcnt vmcnt(" #n ")" ::: "memory")
; #define PG8_BAR __builtin_amdgcn_s_barrier()
; template <class Epi, class Sched, bool ALIGN_EPI = false, bool SP2 = false>
; __device__ __forceinline__ void gemm_phase(PG8_LAS unsigned char* lds, const Gemm g, const Sched& S, const Epi& E) {
;     ...
;             if constexpr (SP2) {
;             PG8_LDB(B0, 0, 0); PG8_LDB(B1, 0, 1); PG8_SCHED; PG8_LDA(At, 0, 0); PG8_STAGE(PG8_SA(1, 1), a1 + hstep, voffA);
;             PG8_WAIT_V(8); PG8_WAIT_L(0); PG8_BAR; PG8_MMA(0, 0, At, B0); PG8_MMA(0, 1, At, B1); PG8_BAR; PG8_SCHED;
;             PG8_LDA(At, 0, 1); PG8_STAGE(PG8_SB(0, 0), b2, voffB); PG8_STAGE(PG8_SB(0, 1), b2 + hstep, voffB); PG8_STAGE(PG8_SA(0, 0), a2, voffA);
.LBB0_1349:
	ds_read_b128 v[152:155], v148
	ds_read_b128 v[156:159], v148 offset:1024
	ds_read_b128 v[160:163], v148 offset:2048
	ds_read_b128 v[164:167], v148 offset:3072
	ds_read_b128 v[168:171], v149
	ds_read_b128 v[172:175], v149 offset:1024
	ds_read_b128 v[176:179], v149 offset:2048
	ds_read_b128 v[180:183], v149 offset:3072
	s_add_u32 s36, s34, 0xfff80080
	s_addc_u32 s37, s35, -1
	s_cmp_eq_u32 s59, 28
	s_cselect_b32 s39, s19, s37
	s_cselect_b32 s38, s55, s36
	s_cselect_b32 s37, s21, s58
	s_cselect_b32 s36, s56, s57
	v_lshl_add_u64 v[144:145], s[34:35], 0, v[138:139]
	s_add_i32 m0, s29, 0xc000
	ds_read_b128 v[188:191], v150
	ds_read_b128 v[192:195], v150 offset:1024
	ds_read_b128 v[196:199], v150 offset:2048
	ds_read_b128 v[200:203], v150 offset:3072
	ds_read_b128 v[204:207], v150 offset:4096
	ds_read_b128 v[208:211], v150 offset:5120
	ds_read_b128 v[212:215], v150 offset:6144
	ds_read_b128 v[216:219], v150 offset:7168
	global_load_lds_dwordx4 v[144:145], off
	v_lshl_add_u64 v[144:145], s[34:35], 0, v[140:141]
	s_add_i32 m0, s29, 0xe000
	s_nop 0
	global_load_lds_dwordx4 v[144:145], off
	s_cmp_eq_u32 s59, s99
	s_cbranch_scc1 .Lrx11_a
	s_waitcnt vmcnt(8)
.Lrx11_a_done:
	s_waitcnt lgkmcnt(0)
	s_barrier
	s_setprio 1
	s_waitcnt lgkmcnt(0)
	v_mfma_f32_16x16x32_bf16 v[124:127], v[152:155], v[188:191], v[124:127]
	v_mfma_f32_16x16x32_bf16 v[120:123], v[160:163], v[188:191], v[120:123]
	v_mfma_f32_16x16x32_bf16 v[116:119], v[152:155], v[196:199], v[116:119]
	v_mfma_f32_16x16x32_bf16 v[112:115], v[160:163], v[196:199], v[112:115]
	v_mfma_f32_16x16x32_bf16 v[100:103], v[152:155], v[204:207], v[100:103]
	v_mfma_f32_16x16x32_bf16 v[96:99], v[160:163], v[204:207], v[96:99]
	v_mfma_f32_16x16x32_bf16 v[76:79], v[152:155], v[212:215], v[76:79]
	v_mfma_f32_16x16x32_bf16 v[72:75], v[160:163], v[212:215], v[72:75]
	v_mfma_f32_16x16x32_bf16 v[124:127], v[156:159], v[192:195], v[124:127]
	v_mfma_f32_16x16x32_bf16 v[120:123], v[164:167], v[192:195], v[120:123]
	v_mfma_f32_16x16x32_bf16 v[116:119], v[156:159], v[200:203], v[116:119]
	v_mfma_f32_16x16x32_bf16 v[112:115], v[164:167], v[200:203], v[112:115]
	v_mfma_f32_16x16x32_bf16 v[100:103], v[156:159], v[208:211], v[100:103]
	v_mfma_f32_16x16x32_bf16 v[96:99], v[164:167], v[208:211], v[96:99]
	v_mfma_f32_16x16x32_bf16 v[76:79], v[156:159], v[216:219], v[76:79]
	v_mfma_f32_16x16x32_bf16 v[72:75], v[164:167], v[216:219], v[72:75]
	s_setprio 0
	s_setprio 1
	v_mfma_f32_16x16x32_bf16 v[108:111], v[168:171], v[188:191], v[108:111]
	v_mfma_f32_16x16x32_bf16 v[104:107], v[176:179], v[188:191], v[104:107]
	v_mfma_f32_16x16x32_bf16 v[92:95], v[168:171], v[196:199], v[92:95]
	v_mfma_f32_16x16x32_bf16 v[88:91], v[176:179], v[196:199], v[88:91]
	v_mfma_f32_16x16x32_bf16 v[84:87], v[168:171], v[204:207], v[84:87]
	v_mfma_f32_16x16x32_bf16 v[80:83], v[176:179], v[204:207], v[80:83]
	v_mfma_f32_16x16x32_bf16 v[68:71], v[168:171], v[212:215], v[68:71]
	v_mfma_f32_16x16x32_bf16 v[64:67], v[176:179], v[212:215], v[64:67]
	v_mfma_f32_16x16x32_bf16 v[108:111], v[172:175], v[192:195], v[108:111]
	v_mfma_f32_16x16x32_bf16 v[104:107], v[180:183], v[192:195], v[104:107]
	v_mfma_f32_16x16x32_bf16 v[92:95], v[172:175], v[200:203], v[92:95]
	v_mfma_f32_16x16x32_bf16 v[88:91], v[180:183], v[200:203], v[88:91]
	v_mfma_f32_16x16x32_bf16 v[84:87], v[172:175], v[208:211], v[84:87]
	v_mfma_f32_16x16x32_bf16 v[80:83], v[180:183], v[208:211], v[80:83]
	v_mfma_f32_16x16x32_bf16 v[68:71], v[172:175], v[216:219], v[68:71]
	v_mfma_f32_16x16x32_bf16 v[64:67], v[180:183], v[216:219], v[64:67]
	s_setprio 0
	s_barrier
	s_add_i32 s60, s49, s43
	v_lshl_add_u64 v[144:145], s[36:37], 0, v[132:133]
	s_mov_b32 m0, s60
	ds_read_b128 v[188:191], v150 offset:16384
	ds_read_b128 v[192:195], v150 offset:17408
	ds_read_b128 v[196:199], v150 offset:18432
	ds_read_b128 v[200:203], v150 offset:19456
	ds_read_b128 v[204:207], v150 offset:20480
	ds_read_b128 v[208:211], v150 offset:21504
	ds_read_b128 v[212:215], v150 offset:22528
	ds_read_b128 v[216:219], v150 offset:23552
	global_load_lds_dwordx4 v[144:145], off
	s_add_i32 m0, s60, 0x2000
	s_add_u32 s60, s36, 0x80000
	v_lshl_add_u64 v[184:185], s[36:37], 0, v[128:129]
	s_addc_u32 s61, s37, 0
	s_add_i32 s62, s50, s43
	global_load_lds_dwordx4 v[184:185], off
	v_lshl_add_u64 v[220:221], s[60:61], 0, v[132:133]
	s_mov_b32 m0, s62
	v_lshl_add_u64 v[222:223], s[38:39], 0, v[130:131]
	global_load_lds_dwordx4 v[220:221], off
	v_lshl_add_u64 v[220:221], s[60:61], 0, v[128:129]
	s_add_i32 m0, s62, 0x2000
	s_nop 0
	global_load_lds_dwordx4 v[220:221], off
	v_lshl_add_u64 v[220:221], s[38:39], 0, v[134:135]
	s_mov_b32 m0, s29
	s_nop 0
	global_load_lds_dwordx4 v[220:221], off
	s_mov_b32 m0, s31
	s_nop 0
	global_load_lds_dwordx4 v[222:223], off
	s_cmp_eq_u32 s59, s99
	s_cbranch_scc1 .Lrx11_b
	s_waitcnt vmcnt(8)
; #define PG8_STAGE(bufoff, gbase, voff) do { _Pragma("unroll") for (int _i = 0; _i < 2; ++_i) \
;         __builtin_amdgcn_global_load_lds((const unsigned*)((const char*)(gbase) + (voff)[_i]), (PG8_LAS unsigned*)(lds + (bufoff) + ldsw + _i * 8192), 16, 0, 0); } while (0)
; #define PG8_LDA(dst, b, h) do { _Pragma("unroll") for (int m = 0; m < 4; ++m) _Pragma("unroll") for (int k = 0; k < 2; ++k) dst[m][k] = *(const PG8_LAS bf16x8*)(lds + PG8_SA(b, h) + aoff + m * 2048 + k * 1024); } while (0)
; #define PG8_LDB(dst, b, h) do { _Pragma("unroll") for (int n = 0; n < 2; ++n) _Pragma("unroll") for (int k = 0; k < 2; ++k) dst[n][k] = *(const PG8_LAS bf16x8*)(lds + PG8_SB(b, h) + boff + n * 2048 + k * 1024); } while (0)
; #define PG8_MMA(ai, bj, At, Bt) do { __builtin_amdgcn_s_setprio(1); _Pragma("unroll") for (int m = 0; m < 4; ++m) _Pragma("unroll") for (int n = 0; n < 2; ++n) _Pragma("unroll") for (int k = 0; k < 2; ++k) \
;         acc[ai][bj][m][n] = __builtin_amdgcn_mfma_f32_16x16x32_bf16(Bt[n][k], At[m][k], acc[ai][bj][m][n], 0, 0, 0); __builtin_amdgcn_s_setprio(0); } while (0)
; #define PG8_WAIT_V(n) asm volatile("s_waitcnt vmcnt(" #n ")" ::: "memory")
; #define PG8_WAIT_L(n) asm volatile("s_waitcnt lgkmcnt(" #n ")" ::: "memory")
; #define PG8_BAR __builtin_amdgcn_s_barrier()
; #define PG8_SCHED __builtin_amdgcn_sched_barrier(0)
; #define PG8_STAGE(bufoff, gbase, voff) do { _Pragma("unroll") for (int _i = 0; _i < 2; ++_i) \
;         __builtin_amdgcn_global_load_lds((const unsigned*)((const char*)(gbase) + (voff)[_i]), (PG8_LAS unsigned*)(lds + (bufoff) + ldsw + _i * 8192), 16, 0, 0); } while (0)
; #define PG8_WAIT_V(n) asm volatile("s_waitcnt vmcnt(" #n ")" ::: "memory")
; #define PG8_WAIT_L(n) asm volatile("s_waitcnt lgkmcnt(" #n ")" ::: "memory")
; #define PG8_BAR __builtin_amdgcn_s_barrier()
; template <class Epi, class Sched, bool ALIGN_EPI = false, bool SP2 = false>
; __device__ __forceinline__ void gemm_phase(PG8_LAS unsigned char* lds, const Gemm g, const Sched& S, const Epi& E) {
;     ...
;             PG8_WAIT_V(8); PG8_WAIT_L(0); PG8_BAR; PG8_MMA(1, 0, At, B0); PG8_MMA(1, 1, At, B1); PG8_BAR; PG8_SCHED;
;             PG8_LDB(B0, 1, 0); PG8_LDB(B1, 1, 1); PG8_SCHED; PG8_LDA(At, 1, 0); PG8_STAGE(PG8_SA(0, 1), a2 + hstep, voffA);
;             PG8_WAIT_V(8); PG8_WAIT_L(0); PG8_BAR; PG8_MMA(0, 0, At, B0); PG8_MMA(0, 1, At, B1); PG8_BAR; PG8_SCHED;
.Lrx11_b_done:
	s_waitcnt lgkmcnt(0)
	s_barrier
	s_setprio 1
	s_waitcnt lgkmcnt(0)
	v_mfma_f32_16x16x32_bf16 v[60:63], v[152:155], v[188:191], v[60:63]
	v_mfma_f32_16x16x32_bf16 v[56:59], v[160:163], v[188:191], v[56:59]
	v_mfma_f32_16x16x32_bf16 v[52:55], v[152:155], v[196:199], v[52:55]
	v_mfma_f32_16x16x32_bf16 v[44:47], v[160:163], v[196:199], v[44:47]
	v_mfma_f32_16x16x32_bf16 v[36:39], v[152:155], v[204:207], v[36:39]
	v_mfma_f32_16x16x32_bf16 v[28:31], v[160:163], v[204:207], v[28:31]
	v_mfma_f32_16x16x32_bf16 v[20:23], v[152:155], v[212:215], v[20:23]
	v_mfma_f32_16x16x32_bf16 v[12:15], v[160:163], v[212:215], v[12:15]
	v_mfma_f32_16x16x32_bf16 v[60:63], v[156:159], v[192:195], v[60:63]
	v_mfma_f32_16x16x32_bf16 v[56:59], v[164:167], v[192:195], v[56:59]
	v_mfma_f32_16x16x32_bf16 v[52:55], v[156:159], v[200:203], v[52:55]
	v_mfma_f32_16x16x32_bf16 v[44:47], v[164:167], v[200:203], v[44:47]
	v_mfma_f32_16x16x32_bf16 v[36:39], v[156:159], v[208:211], v[36:39]
	v_mfma_f32_16x16x32_bf16 v[28:31], v[164:167], v[208:211], v[28:31]
	v_mfma_f32_16x16x32_bf16 v[20:23], v[156:159], v[216:219], v[20:23]
	v_mfma_f32_16x16x32_bf16 v[12:15], v[164:167], v[216:219], v[12:15]
	s_setprio 0
	s_setprio 1
	v_mfma_f32_16x16x32_bf16 v[48:51], v[168:171], v[188:191], v[48:51]
	v_mfma_f32_16x16x32_bf16 v[40:43], v[176:179], v[188:191], v[40:43]
	v_mfma_f32_16x16x32_bf16 v[32:35], v[168:171], v[196:199], v[32:35]
	v_mfma_f32_16x16x32_bf16 v[24:27], v[176:179], v[196:199], v[24:27]
	v_mfma_f32_16x16x32_bf16 v[16:19], v[168:171], v[204:207], v[16:19]
	v_mfma_f32_16x16x32_bf16 v[8:11], v[176:179], v[204:207], v[8:11]
	v_mfma_f32_16x16x32_bf16 v[4:7], v[168:171], v[212:215], v[4:7]
	v_mfma_f32_16x16x32_bf16 v[0:3], v[176:179], v[212:215], v[0:3]
	v_mfma_f32_16x16x32_bf16 v[48:51], v[172:175], v[192:195], v[48:51]
	v_mfma_f32_16x16x32_bf16 v[40:43], v[180:183], v[192:195], v[40:43]
	v_mfma_f32_16x16x32_bf16 v[32:35], v[172:175], v[200:203], v[32:35]
	v_mfma_f32_16x16x32_bf16 v[24:27], v[180:183], v[200:203], v[24:27]
	v_mfma_f32_16x16x32_bf16 v[16:19], v[172:175], v[208:211], v[16:19]
	v_mfma_f32_16x16x32_bf16 v[8:11], v[180:183], v[208:211], v[8:11]
	v_mfma_f32_16x16x32_bf16 v[4:7], v[172:175], v[216:219], v[4:7]
	v_mfma_f32_16x16x32_bf16 v[0:3], v[180:183], v[216:219], v[0:3]
	s_setprio 0
	s_barrier
	s_add_i32 s60, 0, 0x18000
	v_add_u32_e32 v136, s60, v146
	s_add_i32 s61, 0, 0x1c000
	ds_read_b128 v[152:155], v136
	ds_read_b128 v[156:159], v136 offset:1024
	ds_read_b128 v[160:163], v136 offset:2048
	ds_read_b128 v[164:167], v136 offset:3072
	v_add_u32_e32 v136, s61, v146
	ds_read_b128 v[168:171], v136
	ds_read_b128 v[172:175], v136 offset:1024
	ds_read_b128 v[176:179], v136 offset:2048
	ds_read_b128 v[180:183], v136 offset:3072
	s_add_u32 s38, s38, 0x80000
	s_addc_u32 s39, s39, 0
	s_mov_b32 m0, s44
	v_lshl_add_u64 v[224:225], s[38:39], 0, v[134:135]
	ds_read_b128 v[188:191], v150 offset:32768
	ds_read_b128 v[192:195], v150 offset:33792
	ds_read_b128 v[196:199], v150 offset:34816
	ds_read_b128 v[200:203], v150 offset:35840
	ds_read_b128 v[204:207], v150 offset:36864
	ds_read_b128 v[208:211], v150 offset:37888
	ds_read_b128 v[212:215], v150 offset:38912
	ds_read_b128 v[216:219], v150 offset:39936
	global_load_lds_dwordx4 v[224:225], off
	v_lshl_add_u64 v[224:225], s[38:39], 0, v[130:131]
	s_mov_b32 m0, s45
	s_nop 0
	global_load_lds_dwordx4 v[224:225], off
	s_waitcnt vmcnt(8)
	s_waitcnt lgkmcnt(0)
	s_barrier
	s_setprio 1
	s_waitcnt lgkmcnt(0)
	v_mfma_f32_16x16x32_bf16 v[124:127], v[152:155], v[188:191], v[124:127]
	v_mfma_f32_16x16x32_bf16 v[120:123], v[160:163], v[188:191], v[120:123]
	v_mfma_f32_16x16x32_bf16 v[116:119], v[152:155], v[196:199], v[116:119]
	v_mfma_f32_16x16x32_bf16 v[112:115], v[160:163], v[196:199], v[112:115]
	v_mfma_f32_16x16x32_bf16 v[100:103], v[152:155], v[204:207], v[100:103]
	v_mfma_f32_16x16x32_bf16 v[96:99], v[160:163], v[204:207], v[96:99]
	v_mfma_f32_16x16x32_bf16 v[76:79], v[152:155], v[212:215], v[76:79]
	v_mfma_f32_16x16x32_bf16 v[72:75], v[160:163], v[212:215], v[72:75]
	v_mfma_f32_16x16x32_bf16 v[124:127], v[156:159], v[192:195], v[124:127]
	v_mfma_f32_16x16x32_bf16 v[120:123], v[164:167], v[192:195], v[120:123]
	v_mfma_f32_16x16x32_bf16 v[116:119], v[156:159], v[200:203], v[116:119]
	v_mfma_f32_16x16x32_bf16 v[112:115], v[164:167], v[200:203], v[112:115]
	v_mfma_f32_16x16x32_bf16 v[100:103], v[156:159], v[208:211], v[100:103]
	v_mfma_f32_16x16x32_bf16 v[96:99], v[164:167], v[208:211], v[96:99]
	v_mfma_f32_16x16x32_bf16 v[76:79], v[156:159], v[216:219], v[76:79]
	v_mfma_f32_16x16x32_bf16 v[72:75], v[164:167], v[216:219], v[72:75]
	s_setprio 0
	s_setprio 1
	v_mfma_f32_16x16x32_bf16 v[108:111], v[168:171], v[188:191], v[108:111]
	v_mfma_f32_16x16x32_bf16 v[104:107], v[176:179], v[188:191], v[104:107]
	v_mfma_f32_16x16x32_bf16 v[92:95], v[168:171], v[196:199], v[92:95]
	v_mfma_f32_16x16x32_bf16 v[88:91], v[176:179], v[196:199], v[88:91]
	v_mfma_f32_16x16x32_bf16 v[84:87], v[168:171], v[204:207], v[84:87]
	v_mfma_f32_16x16x32_bf16 v[80:83], v[176:179], v[204:207], v[80:83]
	v_mfma_f32_16x16x32_bf16 v[68:71], v[168:171], v[212:215], v[68:71]
	v_mfma_f32_16x16x32_bf16 v[64:67], v[176:179], v[212:215], v[64:67]
	v_mfma_f32_16x16x32_bf16 v[108:111], v[172:175], v[192:195], v[108:111]
	v_mfma_f32_16x16x32_bf16 v[104:107], v[180:183], v[192:195], v[104:107]
	v_mfma_f32_16x16x32_bf16 v[92:95], v[172:175], v[200:203], v[92:95]
	v_mfma_f32_16x16x32_bf16 v[88:91], v[180:183], v[200:203], v[88:91]
	v_mfma_f32_16x16x32_bf16 v[84:87], v[172:175], v[208:211], v[84:87]
	v_mfma_f32_16x16x32_bf16 v[80:83], v[180:183], v[208:211], v[80:83]
	v_mfma_f32_16x16x32_bf16 v[68:71], v[172:175], v[216:219], v[68:71]
	v_mfma_f32_16x16x32_bf16 v[64:67], v[180:183], v[216:219], v[64:67]
	s_setprio 0
	s_barrier
; #define PG8_STAGE(bufoff, gbase, voff) do { _Pragma("unroll") for (int _i = 0; _i < 2; ++_i) \
;         __builtin_amdgcn_global_load_lds((const unsigned*)((const char*)(gbase) + (voff)[_i]), (PG8_LAS unsigned*)(lds + (bufoff) + ldsw + _i * 8192), 16, 0, 0); } while (0)
; #define PG8_LDA(dst, b, h) do { _Pragma("unroll") for (int m = 0; m < 4; ++m) _Pragma("unroll") for (int k = 0; k < 2; ++k) dst[m][k] = *(const PG8_LAS bf16x8*)(lds + PG8_SA(b, h) + aoff + m * 2048 + k * 1024); } while (0)
; #define PG8_MMA(ai, bj, At, Bt) do { __builtin_amdgcn_s_setprio(1); _Pragma("unroll") for (int m = 0; m < 4; ++m) _Pragma("unroll") for (int n = 0; n < 2; ++n) _Pragma("unroll") for (int k = 0; k < 2; ++k) \
;         acc[ai][bj][m][n] = __builtin_amdgcn_mfma_f32_16x16x32_bf16(Bt[n][k], At[m][k], acc[ai][bj][m][n], 0, 0, 0); __builtin_amdgcn_s_setprio(0); } while (0)
; #define PG8_WAIT_V(n) asm volatile("s_waitcnt vmcnt(" #n ")" ::: "memory")
; #define PG8_WAIT_L(n) asm volatile("s_waitcnt lgkmcnt(" #n ")" ::: "memory")
; #define PG8_BAR __builtin_amdgcn_s_barrier()
; #define PG8_SCHED __builtin_amdgcn_sched_barrier(0)
; #define PG8_STAGE(bufoff, gbase, voff) do { _Pragma("unroll") for (int _i = 0; _i < 2; ++_i) \
;         __builtin_amdgcn_global_load_lds((const unsigned*)((const char*)(gbase) + (voff)[_i]), (PG8_LAS unsigned*)(lds + (bufoff) + ldsw + _i * 8192), 16, 0, 0); } while (0)
; #define PG8_WAIT_V(n) asm volatile("s_waitcnt vmcnt(" #n ")" ::: "memory")
; template <class Epi, class Sched, bool ALIGN_EPI = false, bool SP2 = false>
; __device__ __forceinline__ void gemm_phase(PG8_LAS unsigned char* lds, const Gemm g, const Sched& S, const Epi& E) {
;     ...
;             PG8_LDA(At, 1, 1); PG8_STAGE(PG8_SB(1, 0), b3, voffB); PG8_STAGE(PG8_SB(1, 1), b3 + hstep, voffB); PG8_STAGE(PG8_SA(1, 0), a3, voffA);
;             PG8_WAIT_V(8); PG8_WAIT_L(0); PG8_BAR; PG8_MMA(1, 0, At, B0); PG8_MMA(1, 1, At, B1); PG8_BAR; PG8_SCHED;
;     __device__ __forceinline__ void operator()(const f32x4 (&acc)[2][2][4][2], const pg8::Unit& u, int wr, int wc, int fr, int fq) const {
;         const int row0 = u.pm * 256 + wr * 64 + fr, col0 = (u.pn & 7) * 256 + wc * 32 + 8 * fq;
;         float sv[2][4];
; #pragma unroll
;         for (int ai = 0; ai < 2; ++ai)
; #pragma unroll
;             for (int m = 0; m < 4; ++m) sv[ai][m] = VAL[row0 + ai * 128 + m * 16];
	s_add_i32 s38, s60, s43
	v_lshl_add_u64 v[144:145], v[144:145], 0, s[8:9]
	s_mov_b32 m0, s38
	ds_read_b128 v[188:191], v150 offset:49152
	ds_read_b128 v[192:195], v150 offset:50176
	ds_read_b128 v[196:199], v150 offset:51200
	ds_read_b128 v[200:203], v150 offset:52224
	ds_read_b128 v[204:207], v150 offset:53248
	ds_read_b128 v[208:211], v150 offset:54272
	ds_read_b128 v[212:215], v150 offset:55296
	ds_read_b128 v[216:219], v150 offset:56320
	global_load_lds_dwordx4 v[144:145], off
	s_add_i32 m0, s38, 0x2000
	s_add_u32 s36, s36, 0x80080
	v_lshl_add_u64 v[144:145], v[184:185], 0, s[8:9]
	s_addc_u32 s37, s37, 0
	s_add_i32 s38, s61, s43
	global_load_lds_dwordx4 v[144:145], off
	v_lshl_add_u64 v[144:145], s[36:37], 0, v[132:133]
	s_mov_b32 m0, s38
	s_nop 0
	global_load_lds_dwordx4 v[144:145], off
	v_lshl_add_u64 v[144:145], s[36:37], 0, v[128:129]
	s_add_i32 m0, s38, 0x2000
	s_nop 0
	global_load_lds_dwordx4 v[144:145], off
	v_lshl_add_u64 v[144:145], v[220:221], 0, s[8:9]
	s_mov_b32 m0, s47
	s_nop 0
	global_load_lds_dwordx4 v[144:145], off
	v_lshl_add_u64 v[144:145], v[222:223], 0, s[8:9]
	s_mov_b32 m0, s48
	s_nop 0
	global_load_lds_dwordx4 v[144:145], off
	s_waitcnt vmcnt(8)
	s_waitcnt lgkmcnt(0)
	s_barrier
	s_setprio 1
	s_waitcnt lgkmcnt(0)
	v_mfma_f32_16x16x32_bf16 v[60:63], v[152:155], v[188:191], v[60:63]
	v_mfma_f32_16x16x32_bf16 v[56:59], v[160:163], v[188:191], v[56:59]
	v_mfma_f32_16x16x32_bf16 v[52:55], v[152:155], v[196:199], v[52:55]
	v_mfma_f32_16x16x32_bf16 v[44:47], v[160:163], v[196:199], v[44:47]
	v_mfma_f32_16x16x32_bf16 v[36:39], v[152:155], v[204:207], v[36:39]
	v_mfma_f32_16x16x32_bf16 v[28:31], v[160:163], v[204:207], v[28:31]
	v_mfma_f32_16x16x32_bf16 v[20:23], v[152:155], v[212:215], v[20:23]
	v_mfma_f32_16x16x32_bf16 v[12:15], v[160:163], v[212:215], v[12:15]
	v_mfma_f32_16x16x32_bf16 v[60:63], v[156:159], v[192:195], v[60:63]
	v_mfma_f32_16x16x32_bf16 v[56:59], v[164:167], v[192:195], v[56:59]
	v_mfma_f32_16x16x32_bf16 v[52:55], v[156:159], v[200:203], v[52:55]
	v_mfma_f32_16x16x32_bf16 v[44:47], v[164:167], v[200:203], v[44:47]
	v_mfma_f32_16x16x32_bf16 v[36:39], v[156:159], v[208:211], v[36:39]
	v_mfma_f32_16x16x32_bf16 v[28:31], v[164:167], v[208:211], v[28:31]
	v_mfma_f32_16x16x32_bf16 v[20:23], v[156:159], v[216:219], v[20:23]
	v_mfma_f32_16x16x32_bf16 v[12:15], v[164:167], v[216:219], v[12:15]
	s_setprio 0
	s_setprio 1
	v_mfma_f32_16x16x32_bf16 v[48:51], v[168:171], v[188:191], v[48:51]
	v_mfma_f32_16x16x32_bf16 v[40:43], v[176:179], v[188:191], v[40:43]
	v_mfma_f32_16x16x32_bf16 v[32:35], v[168:171], v[196:199], v[32:35]
	v_mfma_f32_16x16x32_bf16 v[24:27], v[176:179], v[196:199], v[24:27]
	v_mfma_f32_16x16x32_bf16 v[16:19], v[168:171], v[204:207], v[16:19]
	v_mfma_f32_16x16x32_bf16 v[8:11], v[176:179], v[204:207], v[8:11]
	v_mfma_f32_16x16x32_bf16 v[4:7], v[168:171], v[212:215], v[4:7]
	v_mfma_f32_16x16x32_bf16 v[0:3], v[176:179], v[212:215], v[0:3]
	v_mfma_f32_16x16x32_bf16 v[48:51], v[172:175], v[192:195], v[48:51]
	v_mfma_f32_16x16x32_bf16 v[40:43], v[180:183], v[192:195], v[40:43]
	v_mfma_f32_16x16x32_bf16 v[32:35], v[172:175], v[200:203], v[32:35]
	v_mfma_f32_16x16x32_bf16 v[24:27], v[180:183], v[200:203], v[24:27]
	v_mfma_f32_16x16x32_bf16 v[16:19], v[172:175], v[208:211], v[16:19]
	v_mfma_f32_16x16x32_bf16 v[8:11], v[180:183], v[208:211], v[8:11]
	v_mfma_f32_16x16x32_bf16 v[4:7], v[172:175], v[216:219], v[4:7]
	v_mfma_f32_16x16x32_bf16 v[0:3], v[180:183], v[216:219], v[0:3]
	s_setprio 0
	s_barrier
	s_add_i32 s59, s59, 2
	s_add_u32 s34, s34, 0x100
	s_addc_u32 s35, s35, 0
	s_add_u32 s57, s57, 0x100
	s_addc_u32 s58, s58, 0
	s_cmp_gt_u32 s59, 29
	s_cbranch_scc0 .LBB0_1349
	s_and_b64 vcc, exec, s[10:11]
	s_cbranch_vccz .LBB0_1352
	s_barrier
.LBB0_1352:
	v_lshl_add_u32 v144, s30, 8, v143
	v_or_b32_e32 v156, 16, v144
	v_ashrrev_i32_e32 v145, 31, v144
	v_ashrrev_i32_e32 v157, 31, v156
	v_or_b32_e32 v160, 32, v144
	v_lshl_add_u64 v[152:153], v[144:145], 2, s[6:7]
	v_lshl_add_u64 v[158:159], v[156:157], 2, s[6:7]
	v_ashrrev_i32_e32 v161, 31, v160
	global_load_dword v154, v[152:153], off
	v_lshl_add_u64 v[162:163], v[160:161], 2, s[6:7]
	global_load_dword v158, v[158:159], off
	v_or_b32_e32 v164, 48, v144
	global_load_dword v162, v[162:163], off
	v_ashrrev_i32_e32 v165, 31, v164
	v_lshl_add_u64 v[166:167], v[164:165], 2, s[6:7]
	global_load_dword v166, v[166:167], off
	s_nop 0
	global_load_dword v168, v[152:153], off offset:512
	global_load_dword v170, v[152:153], off offset:576
	global_load_dword v172, v[152:153], off offset:640
	global_load_dword v142, v[152:153], off offset:704
	s_lshl_b32 s19, s28, 8
	s_and_b32 s19, s19, 0x700
	v_or_b32_e32 v136, s19, v147
	v_lshlrev_b64 v[144:145], 12, v[144:145]
	v_lshlrev_b64 v[156:157], 12, v[156:157]
	v_lshl_add_u64 v[144:145], s[4:5], 0, v[144:145]
	v_lshlrev_b32_e32 v136, 1, v136
	v_lshlrev_b64 v[160:161], 12, v[160:161]
	v_lshl_add_u64 v[152:153], s[4:5], 0, v[156:157]
	v_lshl_add_u64 v[144:145], v[144:145], 0, v[136:137]
	v_lshl_add_u64 v[156:157], s[4:5], 0, v[160:161]
	v_lshl_add_u64 v[152:153], v[152:153], 0, v[136:137]
	v_lshl_add_u64 v[156:157], v[156:157], 0, v[136:137]
	s_waitcnt vmcnt(0)
; __device__ __forceinline__ unsigned pk2(float lo, float hi) { typedef float f2v __attribute__((ext_vector_type(2))); typedef __bf16 b2v __attribute__((ext_vector_type(2))); const f2v v = {lo, hi}; return __builtin_bit_cast(unsigned, __builtin_convertvector(v, b2v)); }
;     __device__ __forceinline__ void operator()(const f32x4 (&acc)[2][2][4][2], const pg8::Unit& u, int wr, int wc, int fr, int fq) const {
;     ...
; #pragma unroll
;         for (int ai = 0; ai < 2; ++ai)
; #pragma unroll
;             for (int m = 0; m < 4; ++m) { const int row = row0 + ai * 128 + m * 16; const float s = sv[ai][m]; bf16* rowp = O + (size_t)row * D + col0;
; #pragma unroll
;                 for (int bj = 0; bj < 2; ++bj) { const f32x4 v0 = acc[ai][bj][m][0] * s, v1 = acc[ai][bj][m][1] * s;
;                     v4u w; w.x = pk2(v0[0], v0[1]); w.y = pk2(v0[2], v0[3]); w.z = pk2(v1[0], v1[1]); w.w = pk2(v1[2], v1[3]);
;                     *(v4u*)(rowp + bj * 128) = w; } }
	v_pk_mul_f32 v[126:127], v[126:127], v[154:155] op_sel_hi:[1,0]
	v_pk_mul_f32 v[124:125], v[124:125], v[154:155] op_sel_hi:[1,0]
	v_pk_mul_f32 v[122:123], v[122:123], v[154:155] op_sel_hi:[1,0]
	v_pk_mul_f32 v[120:121], v[120:121], v[154:155] op_sel_hi:[1,0]
	v_pk_mul_f32 v[118:119], v[118:119], v[158:159] op_sel_hi:[1,0]
	v_pk_mul_f32 v[116:117], v[116:117], v[158:159] op_sel_hi:[1,0]
	v_pk_mul_f32 v[114:115], v[114:115], v[158:159] op_sel_hi:[1,0]
	v_pk_mul_f32 v[112:113], v[112:113], v[158:159] op_sel_hi:[1,0]
	v_pk_mul_f32 v[110:111], v[110:111], v[154:155] op_sel_hi:[1,0]
	v_pk_mul_f32 v[108:109], v[108:109], v[154:155] op_sel_hi:[1,0]
	v_pk_mul_f32 v[160:161], v[106:107], v[154:155] op_sel_hi:[1,0]
	v_pk_mul_f32 v[154:155], v[104:105], v[154:155] op_sel_hi:[1,0]
	v_cvt_pk_bf16_f32 v104, v124, v125
	v_cvt_pk_bf16_f32 v105, v126, v127
	v_cvt_pk_bf16_f32 v106, v120, v121
	v_cvt_pk_bf16_f32 v107, v122, v123
	v_pk_mul_f32 v[94:95], v[94:95], v[158:159] op_sel_hi:[1,0]
	v_pk_mul_f32 v[92:93], v[92:93], v[158:159] op_sel_hi:[1,0]
	v_pk_mul_f32 v[90:91], v[90:91], v[158:159] op_sel_hi:[1,0]
	v_pk_mul_f32 v[88:89], v[88:89], v[158:159] op_sel_hi:[1,0]
	v_pk_mul_f32 v[102:103], v[102:103], v[162:163] op_sel_hi:[1,0]
	v_pk_mul_f32 v[100:101], v[100:101], v[162:163] op_sel_hi:[1,0]
	v_pk_mul_f32 v[98:99], v[98:99], v[162:163] op_sel_hi:[1,0]
	v_pk_mul_f32 v[96:97], v[96:97], v[162:163] op_sel_hi:[1,0]
	v_pk_mul_f32 v[120:121], v[86:87], v[162:163] op_sel_hi:[1,0]
	v_pk_mul_f32 v[122:123], v[84:85], v[162:163] op_sel_hi:[1,0]
	v_pk_mul_f32 v[124:125], v[82:83], v[162:163] op_sel_hi:[1,0]
	v_pk_mul_f32 v[126:127], v[80:81], v[162:163] op_sel_hi:[1,0]
	v_cvt_pk_bf16_f32 v80, v116, v117
	v_cvt_pk_bf16_f32 v81, v118, v119
	v_cvt_pk_bf16_f32 v82, v112, v113
	v_cvt_pk_bf16_f32 v83, v114, v115
	v_cvt_pk_bf16_f32 v108, v108, v109
	v_cvt_pk_bf16_f32 v109, v110, v111
	v_cvt_pk_bf16_f32 v110, v154, v155
	v_cvt_pk_bf16_f32 v111, v160, v161
	global_store_dwordx4 v[144:145], v[104:107], off
	global_store_dwordx4 v[144:145], v[108:111], off offset:256
	v_cvt_pk_bf16_f32 v84, v92, v93
	v_cvt_pk_bf16_f32 v85, v94, v95
	v_cvt_pk_bf16_f32 v86, v88, v89
	v_cvt_pk_bf16_f32 v87, v90, v91
	v_cvt_pk_bf16_f32 v88, v100, v101
	v_cvt_pk_bf16_f32 v89, v102, v103
	v_cvt_pk_bf16_f32 v90, v96, v97
	v_cvt_pk_bf16_f32 v91, v98, v99
	v_cvt_pk_bf16_f32 v92, v122, v123
	v_cvt_pk_bf16_f32 v93, v120, v121
	v_cvt_pk_bf16_f32 v94, v126, v127
	v_cvt_pk_bf16_f32 v95, v124, v125
	global_store_dwordx4 v[152:153], v[80:83], off
	global_store_dwordx4 v[152:153], v[84:87], off offset:256
	global_store_dwordx4 v[156:157], v[88:91], off
	global_store_dwordx4 v[156:157], v[92:95], off offset:256
	v_lshlrev_b64 v[80:81], 12, v[164:165]
	v_lshl_add_u64 v[80:81], s[4:5], 0, v[80:81]
	v_pk_mul_f32 v[78:79], v[78:79], v[166:167] op_sel_hi:[1,0]
	v_pk_mul_f32 v[76:77], v[76:77], v[166:167] op_sel_hi:[1,0]
	v_pk_mul_f32 v[82:83], v[74:75], v[166:167] op_sel_hi:[1,0]
	v_pk_mul_f32 v[74:75], v[72:73], v[166:167] op_sel_hi:[1,0]
	v_lshl_add_u64 v[80:81], v[80:81], 0, v[136:137]
	v_cvt_pk_bf16_f32 v72, v76, v77
	v_cvt_pk_bf16_f32 v73, v78, v79
	v_cvt_pk_bf16_f32 v74, v74, v75
	v_cvt_pk_bf16_f32 v75, v82, v83
	global_store_dwordx4 v[80:81], v[72:75], off
	v_pk_mul_f32 v[70:71], v[70:71], v[166:167] op_sel_hi:[1,0]
	v_pk_mul_f32 v[68:69], v[68:69], v[166:167] op_sel_hi:[1,0]
	v_pk_mul_f32 v[72:73], v[66:67], v[166:167] op_sel_hi:[1,0]
	v_pk_mul_f32 v[66:67], v[64:65], v[166:167] op_sel_hi:[1,0]
	v_cvt_pk_bf16_f32 v64, v68, v69
	v_cvt_pk_bf16_f32 v65, v70, v71
	v_cvt_pk_bf16_f32 v66, v66, v67
	v_cvt_pk_bf16_f32 v67, v72, v73
	v_pk_mul_f32 v[60:61], v[60:61], v[168:169] op_sel_hi:[1,0]
	global_store_dwordx4 v[80:81], v[64:67], off offset:256
	v_pk_mul_f32 v[62:63], v[62:63], v[168:169] op_sel_hi:[1,0]
	v_pk_mul_f32 v[50:51], v[50:51], v[168:169] op_sel_hi:[1,0]
	v_pk_mul_f32 v[66:67], v[58:59], v[168:169] op_sel_hi:[1,0]
; #define PG8_BAR __builtin_amdgcn_s_barrier()
; #define PG8_BAR __builtin_amdgcn_s_barrier()
; __device__ __forceinline__ unsigned pk2(float lo, float hi) { typedef float f2v __attribute__((ext_vector_type(2))); typedef __bf16 b2v __attribute__((ext_vector_type(2))); const f2v v = {lo, hi}; return __builtin_bit_cast(unsigned, __builtin_convertvector(v, b2v)); }
; template <class Epi, class Sched, bool ALIGN_EPI = false, bool SP2 = false>
; __device__ __forceinline__ void gemm_phase(PG8_LAS unsigned char* lds, const Gemm g, const Sched& S, const Epi& E) {
;     ...
;         if constexpr (!Epi::AFTER_DRAIN) { E(acc, cur, wr, wc, fr, fq); S.done(cur); }
;         if (!has_next) break;
; #pragma unroll
;         for (int a = 0; a < 2; ++a)
; #pragma unroll
;             for (int b = 0; b < 2; ++b)
; #pragma unroll
;                 for (int m = 0; m < 4; ++m)
; #pragma unroll
;                     for (int n = 0; n < 2; ++n) acc[a][b][m][n] = (f32x4){0.f, 0.f, 0.f, 0.f};
;         cur = nxt; cA = nA; cB = nB; ++ui;
;         if constexpr (ALIGN_EPI) { if (wr == 1) PG8_BAR; }
;     __device__ __forceinline__ void operator()(const f32x4 (&acc)[2][2][4][2], const pg8::Unit& u, int wr, int wc, int fr, int fq) const {
;     ...
; #pragma unroll
;         for (int ai = 0; ai < 2; ++ai)
; #pragma unroll
;             for (int m = 0; m < 4; ++m) { const int row = row0 + ai * 128 + m * 16; const float s = sv[ai][m]; bf16* rowp = O + (size_t)row * D + col0;
; #pragma unroll
;                 for (int bj = 0; bj < 2; ++bj) { const f32x4 v0 = acc[ai][bj][m][0] * s, v1 = acc[ai][bj][m][1] * s;
;                     v4u w; w.x = pk2(v0[0], v0[1]); w.y = pk2(v0[2], v0[3]); w.z = pk2(v1[0], v1[1]); w.w = pk2(v1[2], v1[3]);
;                     *(v4u*)(rowp + bj * 128) = w; } }
	v_pk_mul_f32 v[58:59], v[56:57], v[168:169] op_sel_hi:[1,0]
	v_cvt_pk_bf16_f32 v56, v60, v61
	v_add_co_u32_e32 v60, vcc, s51, v144
	v_cvt_pk_bf16_f32 v57, v62, v63
	v_cvt_pk_bf16_f32 v58, v58, v59
	v_cvt_pk_bf16_f32 v59, v66, v67
	v_addc_co_u32_e32 v61, vcc, 0, v145, vcc
	global_store_dwordx4 v[60:61], v[56:59], off
	v_pk_mul_f32 v[48:49], v[48:49], v[168:169] op_sel_hi:[1,0]
	v_lshl_add_u64 v[64:65], v[144:145], 0, s[0:1]
	v_pk_mul_f32 v[56:57], v[42:43], v[168:169] op_sel_hi:[1,0]
	v_pk_mul_f32 v[42:43], v[40:41], v[168:169] op_sel_hi:[1,0]
	v_cvt_pk_bf16_f32 v40, v48, v49
	v_cvt_pk_bf16_f32 v41, v50, v51
	v_cvt_pk_bf16_f32 v42, v42, v43
	v_cvt_pk_bf16_f32 v43, v56, v57
	global_store_dwordx4 v[64:65], v[40:43], off offset:256
	v_pk_mul_f32 v[44:45], v[44:45], v[170:171] op_sel_hi:[1,0]
	v_pk_mul_f32 v[46:47], v[46:47], v[170:171] op_sel_hi:[1,0]
	v_pk_mul_f32 v[42:43], v[54:55], v[170:171] op_sel_hi:[1,0]
	v_pk_mul_f32 v[40:41], v[52:53], v[170:171] op_sel_hi:[1,0]
	v_pk_mul_f32 v[34:35], v[34:35], v[170:171] op_sel_hi:[1,0]
	v_cvt_pk_bf16_f32 v40, v40, v41
	v_cvt_pk_bf16_f32 v41, v42, v43
	v_cvt_pk_bf16_f32 v42, v44, v45
	v_add_co_u32_e32 v44, vcc, s52, v144
	v_cvt_pk_bf16_f32 v43, v46, v47
	s_nop 0
	v_addc_co_u32_e32 v45, vcc, 0, v145, vcc
	global_store_dwordx4 v[44:45], v[40:43], off
	v_pk_mul_f32 v[32:33], v[32:33], v[170:171] op_sel_hi:[1,0]
	v_lshl_add_u64 v[48:49], v[144:145], 0, s[12:13]
	v_pk_mul_f32 v[40:41], v[26:27], v[170:171] op_sel_hi:[1,0]
	v_pk_mul_f32 v[26:27], v[24:25], v[170:171] op_sel_hi:[1,0]
	v_cvt_pk_bf16_f32 v24, v32, v33
	v_cvt_pk_bf16_f32 v25, v34, v35
	v_cvt_pk_bf16_f32 v26, v26, v27
	v_cvt_pk_bf16_f32 v27, v40, v41
	global_store_dwordx4 v[48:49], v[24:27], off offset:256
	v_pk_mul_f32 v[28:29], v[28:29], v[172:173] op_sel_hi:[1,0]
	v_pk_mul_f32 v[30:31], v[30:31], v[172:173] op_sel_hi:[1,0]
	v_pk_mul_f32 v[26:27], v[38:39], v[172:173] op_sel_hi:[1,0]
	v_pk_mul_f32 v[24:25], v[36:37], v[172:173] op_sel_hi:[1,0]
	v_pk_mul_f32 v[18:19], v[18:19], v[172:173] op_sel_hi:[1,0]
	v_cvt_pk_bf16_f32 v24, v24, v25
	v_cvt_pk_bf16_f32 v25, v26, v27
	v_cvt_pk_bf16_f32 v26, v28, v29
	v_add_co_u32_e32 v28, vcc, s53, v144
	v_cvt_pk_bf16_f32 v27, v30, v31
	s_nop 0
	v_addc_co_u32_e32 v29, vcc, 0, v145, vcc
	global_store_dwordx4 v[28:29], v[24:27], off
	v_pk_mul_f32 v[16:17], v[16:17], v[172:173] op_sel_hi:[1,0]
	v_lshl_add_u64 v[32:33], v[144:145], 0, s[14:15]
	v_pk_mul_f32 v[24:25], v[10:11], v[172:173] op_sel_hi:[1,0]
	v_pk_mul_f32 v[10:11], v[8:9], v[172:173] op_sel_hi:[1,0]
	v_cvt_pk_bf16_f32 v8, v16, v17
	v_cvt_pk_bf16_f32 v9, v18, v19
	v_cvt_pk_bf16_f32 v10, v10, v11
	v_cvt_pk_bf16_f32 v11, v24, v25
	global_store_dwordx4 v[32:33], v[8:11], off offset:256
	v_pk_mul_f32 v[12:13], v[12:13], v[142:143] op_sel_hi:[1,0]
	v_pk_mul_f32 v[14:15], v[14:15], v[142:143] op_sel_hi:[1,0]
	v_pk_mul_f32 v[10:11], v[22:23], v[142:143] op_sel_hi:[1,0]
	v_pk_mul_f32 v[8:9], v[20:21], v[142:143] op_sel_hi:[1,0]
	v_pk_mul_f32 v[6:7], v[6:7], v[142:143] op_sel_hi:[1,0]
	v_cvt_pk_bf16_f32 v8, v8, v9
	v_cvt_pk_bf16_f32 v9, v10, v11
	v_cvt_pk_bf16_f32 v10, v12, v13
	v_add_co_u32_e32 v12, vcc, s54, v144
	v_cvt_pk_bf16_f32 v11, v14, v15
	s_nop 0
	v_addc_co_u32_e32 v13, vcc, 0, v145, vcc
	global_store_dwordx4 v[12:13], v[8:11], off
	v_pk_mul_f32 v[4:5], v[4:5], v[142:143] op_sel_hi:[1,0]
	v_lshl_add_u64 v[16:17], v[144:145], 0, s[16:17]
	v_pk_mul_f32 v[8:9], v[2:3], v[142:143] op_sel_hi:[1,0]
	v_pk_mul_f32 v[2:3], v[0:1], v[142:143] op_sel_hi:[1,0]
	v_cvt_pk_bf16_f32 v0, v4, v5
	v_cvt_pk_bf16_f32 v1, v6, v7
	v_cvt_pk_bf16_f32 v2, v2, v3
	v_cvt_pk_bf16_f32 v3, v8, v9
	s_andn2_b64 vcc, exec, s[22:23]
	s_mov_b64 s[22:23], -1
	s_mov_b32 s98, 1
	global_store_dwordx4 v[16:17], v[0:3], off offset:256
	s_cbranch_vccnz .LBB0_1345
	s_andn2_b64 vcc, exec, s[2:3]
	s_cbranch_vccnz .LBB0_1344
	s_barrier
	s_branch .LBB0_1344
